# adds: Hyena filter last layer (16x64 . 64x1024 f32) as packed f32 FMAs on position pairs (f2 stored position-minor in LDS), same operations per accumulator
# speedup vs baseline: 1.0005x; 1.0005x over previous
;     ...
;             for (int o = F.tid; o < 16 * 64; o += 512) { const int p = o >> 6, j = o & 63; float s = b2[j];
; #pragma unroll 8
;                 for (int i = 0; i < 64; ++i) s += f1[p * 64 + i] * w2[i * 64 + j];
;                 f2[o] = sinf(fq[j] * s); }
.LBB0_250:
	s_or_b64 exec, exec, s[4:5]
	v_mul_f32_e32 v25, v24, v24
	v_fmamk_f32 v26, v25, 0xb94c1982, v218
	v_fmaak_f32 v26, v25, v26, 0xbe2aaa9d
	v_mul_f32_e32 v26, v25, v26
	v_fmac_f32_e32 v24, v24, v26
	v_fmamk_f32 v26, v25, 0x37d75334, v213
	v_fmaak_f32 v26, v25, v26, 0x3d2aabf7
	v_fmaak_f32 v26, v25, v26, 0xbf000004
	v_fma_f32 v25, v25, v26, 1.0
	v_and_b32_e32 v26, 1, v23
	v_lshlrev_b32_e32 v23, 30, v23
	v_cmp_eq_u32_e32 vcc, 0, v26
	v_and_b32_e32 v23, 0x80000000, v23
	v_xor_b32_e32 v22, v22, v21
	v_cndmask_b32_e32 v24, v25, v24, vcc
	v_xor_b32_e32 v22, v22, v23
	s_movk_i32 s4, 0x1f8
	v_xor_b32_e32 v22, v22, v24
	v_cmp_class_f32_e64 vcc, v21, s4
	s_movk_i32 s4, 0x1ff
	s_nop 0
	v_cndmask_b32_e32 v21, v244, v22, vcc
	v_and_b32_e32 v22, 63, v20
	v_lshrrev_b32_e32 v25, 6, v20
	v_lshlrev_b32_e32 v25, 2, v25
	v_lshl_add_u32 v22, v22, 6, v25
	ds_write_b32 v22, v21 offset:8192
	v_add_u32_e32 v21, 0x200, v20
	v_cmp_lt_i32_e32 vcc, s4, v20
	s_or_b64 s[2:3], vcc, s[2:3]
	v_mov_b32_e32 v20, v21
	s_andn2_b64 exec, exec, s[2:3]
	s_cbranch_execz .LBB0_257

; __device__ __forceinline__ void lds_barrier() { asm volatile("s_waitcnt lgkmcnt(0)" ::: "memory"); __builtin_amdgcn_s_barrier(); asm volatile("" ::: "memory"); }
;     ...
;             lds_barrier();
; #pragma unroll
;             for (int cc = 0; cc < 2; ++cc) { const int col = F.tid + cc * 512; float acc[16];
; #pragma unroll
;                 for (int p = 0; p < 16; ++p) acc[p] = 0.f;
;                 for (int k = 0; k < 64; ++k) { const float w = w3[k * 1024 + col];
; #pragma unroll
;                     for (int p = 0; p < 16; ++p) acc[p] += f2[p * 64 + k] * w; }
.LBB0_257:
	s_or_b64 exec, exec, s[0:1]
	s_waitcnt lgkmcnt(0)
	s_barrier
	v_mov_b32_e32 v18, 0
	s_add_i32 s0, 0, 0x2000
	s_mov_b32 s1, 0
	v_mov_b32_e32 v19, v18
	v_mov_b32_e32 v32, v18
	v_mov_b32_e32 v33, v18
	v_mov_b32_e32 v28, v18
	v_mov_b32_e32 v29, v18
	v_mov_b32_e32 v36, v18
	v_mov_b32_e32 v37, v18
	v_mov_b32_e32 v34, v18
	v_mov_b32_e32 v35, v18
	v_mov_b32_e32 v30, v18
	v_mov_b32_e32 v31, v18
	v_mov_b32_e32 v24, v18
	v_mov_b32_e32 v25, v18
	v_mov_b32_e32 v22, v18
	v_mov_b32_e32 v23, v18
	v_lshlrev_b32_e32 v186, 2, v0
	s_add_u32 s6, s20, 0x1000
	s_addc_u32 s7, s21, 0
	global_load_dword v120, v186, s[6:7] offset:-4096
	global_load_dword v121, v186, s[6:7]
	s_add_u32 s6, s6, 0x2000
	s_addc_u32 s7, s7, 0
	global_load_dword v122, v186, s[6:7] offset:-4096
	global_load_dword v123, v186, s[6:7]
	s_add_u32 s6, s6, 0x2000
	s_addc_u32 s7, s7, 0
	global_load_dword v124, v186, s[6:7] offset:-4096
	global_load_dword v125, v186, s[6:7]
	s_add_u32 s6, s6, 0x2000
	s_addc_u32 s7, s7, 0
	global_load_dword v126, v186, s[6:7] offset:-4096
	global_load_dword v127, v186, s[6:7]
	s_add_u32 s6, s6, 0x2000
	s_addc_u32 s7, s7, 0
	global_load_dword v128, v186, s[6:7] offset:-4096
	global_load_dword v129, v186, s[6:7]
	s_add_u32 s6, s6, 0x2000
	s_addc_u32 s7, s7, 0
	global_load_dword v130, v186, s[6:7] offset:-4096
	global_load_dword v131, v186, s[6:7]
	s_add_u32 s6, s6, 0x2000
	s_addc_u32 s7, s7, 0
	global_load_dword v132, v186, s[6:7] offset:-4096
	global_load_dword v133, v186, s[6:7]
	s_add_u32 s6, s6, 0x2000
	s_addc_u32 s7, s7, 0
	global_load_dword v134, v186, s[6:7] offset:-4096
	global_load_dword v135, v186, s[6:7]
	s_add_u32 s6, s6, 0x2000
	s_addc_u32 s7, s7, 0
	global_load_dword v136, v186, s[6:7] offset:-4096
	global_load_dword v137, v186, s[6:7]
	s_add_u32 s6, s6, 0x2000
	s_addc_u32 s7, s7, 0
	global_load_dword v138, v186, s[6:7] offset:-4096
	global_load_dword v139, v186, s[6:7]
	s_add_u32 s6, s6, 0x2000
	s_addc_u32 s7, s7, 0
	global_load_dword v140, v186, s[6:7] offset:-4096
	global_load_dword v141, v186, s[6:7]
	s_add_u32 s6, s6, 0x2000
	s_addc_u32 s7, s7, 0
	global_load_dword v142, v186, s[6:7] offset:-4096
	global_load_dword v143, v186, s[6:7]
	s_add_u32 s6, s6, 0x2000
	s_addc_u32 s7, s7, 0
	global_load_dword v144, v186, s[6:7] offset:-4096
	global_load_dword v145, v186, s[6:7]
	s_add_u32 s6, s6, 0x2000
	s_addc_u32 s7, s7, 0
	global_load_dword v146, v186, s[6:7] offset:-4096
	global_load_dword v147, v186, s[6:7]
	s_add_u32 s6, s6, 0x2000
	s_addc_u32 s7, s7, 0
	global_load_dword v148, v186, s[6:7] offset:-4096
	global_load_dword v149, v186, s[6:7]
	s_add_u32 s6, s6, 0x2000
	s_addc_u32 s7, s7, 0
	global_load_dword v150, v186, s[6:7] offset:-4096
	global_load_dword v151, v186, s[6:7]
	s_add_u32 s6, s6, 0x2000
	s_addc_u32 s7, s7, 0
	global_load_dword v152, v186, s[6:7] offset:-4096
	global_load_dword v153, v186, s[6:7]
	s_add_u32 s6, s6, 0x2000
	s_addc_u32 s7, s7, 0
	global_load_dword v154, v186, s[6:7] offset:-4096
	global_load_dword v155, v186, s[6:7]
	s_add_u32 s6, s6, 0x2000
	s_addc_u32 s7, s7, 0
	global_load_dword v156, v186, s[6:7] offset:-4096
	global_load_dword v157, v186, s[6:7]
	s_add_u32 s6, s6, 0x2000
	s_addc_u32 s7, s7, 0
	global_load_dword v158, v186, s[6:7] offset:-4096
	global_load_dword v159, v186, s[6:7]
	s_add_u32 s6, s6, 0x2000
	s_addc_u32 s7, s7, 0
	global_load_dword v160, v186, s[6:7] offset:-4096
	global_load_dword v161, v186, s[6:7]
	s_add_u32 s6, s6, 0x2000
	s_addc_u32 s7, s7, 0
	global_load_dword v162, v186, s[6:7] offset:-4096
	global_load_dword v163, v186, s[6:7]
	s_add_u32 s6, s6, 0x2000
	s_addc_u32 s7, s7, 0
	global_load_dword v164, v186, s[6:7] offset:-4096
	global_load_dword v165, v186, s[6:7]
	s_add_u32 s6, s6, 0x2000
	s_addc_u32 s7, s7, 0
	global_load_dword v166, v186, s[6:7] offset:-4096
	global_load_dword v167, v186, s[6:7]
	s_add_u32 s6, s6, 0x2000
	s_addc_u32 s7, s7, 0
	v_mov_b32_e32 v187, 0x2000
	ds_read_b128 v[56:59], v187
	ds_read_b128 v[60:63], v187 offset:16
	ds_read_b128 v[64:67], v187 offset:32
	ds_read_b128 v[68:71], v187 offset:48
	ds_read_b128 v[72:75], v187 offset:64
	ds_read_b128 v[76:79], v187 offset:80
	ds_read_b128 v[80:83], v187 offset:96
	ds_read_b128 v[84:87], v187 offset:112
	s_waitcnt lgkmcnt(0)
	ds_read_b128 v[88:91], v187 offset:128
	ds_read_b128 v[92:95], v187 offset:144
	ds_read_b128 v[96:99], v187 offset:160
	ds_read_b128 v[100:103], v187 offset:176
	ds_read_b128 v[104:107], v187 offset:192
	ds_read_b128 v[108:111], v187 offset:208
	ds_read_b128 v[112:115], v187 offset:224
	ds_read_b128 v[116:119], v187 offset:240
	s_waitcnt vmcnt(44)
	v_pk_fma_f32 v[32:33], v[56:57], v[120:121], v[32:33] op_sel_hi:[1,0,1]
	v_pk_fma_f32 v[28:29], v[58:59], v[120:121], v[28:29] op_sel_hi:[1,0,1]
	v_pk_fma_f32 v[36:37], v[60:61], v[120:121], v[36:37] op_sel_hi:[1,0,1]
	v_pk_fma_f32 v[34:35], v[62:63], v[120:121], v[34:35] op_sel_hi:[1,0,1]
	v_pk_fma_f32 v[30:31], v[64:65], v[120:121], v[30:31] op_sel_hi:[1,0,1]
	v_pk_fma_f32 v[24:25], v[66:67], v[120:121], v[24:25] op_sel_hi:[1,0,1]
	v_pk_fma_f32 v[22:23], v[68:69], v[120:121], v[22:23] op_sel_hi:[1,0,1]
	v_pk_fma_f32 v[18:19], v[70:71], v[120:121], v[18:19] op_sel_hi:[1,0,1]
	v_pk_fma_f32 v[32:33], v[72:73], v[120:121], v[32:33] op_sel:[0,1,0]
	v_pk_fma_f32 v[28:29], v[74:75], v[120:121], v[28:29] op_sel:[0,1,0]
	v_pk_fma_f32 v[36:37], v[76:77], v[120:121], v[36:37] op_sel:[0,1,0]
	v_pk_fma_f32 v[34:35], v[78:79], v[120:121], v[34:35] op_sel:[0,1,0]
	v_pk_fma_f32 v[30:31], v[80:81], v[120:121], v[30:31] op_sel:[0,1,0]
	v_pk_fma_f32 v[24:25], v[82:83], v[120:121], v[24:25] op_sel:[0,1,0]
	v_pk_fma_f32 v[22:23], v[84:85], v[120:121], v[22:23] op_sel:[0,1,0]
	v_pk_fma_f32 v[18:19], v[86:87], v[120:121], v[18:19] op_sel:[0,1,0]
	s_waitcnt lgkmcnt(0)
;     ...
;                 for (int k = 0; k < 64; ++k) { const float w = w3[k * 1024 + col];
; #pragma unroll
;                     for (int p = 0; p < 16; ++p) acc[p] += f2[p * 64 + k] * w; }
	ds_read_b128 v[56:59], v187 offset:256
	ds_read_b128 v[60:63], v187 offset:272
	ds_read_b128 v[64:67], v187 offset:288
	ds_read_b128 v[68:71], v187 offset:304
	ds_read_b128 v[72:75], v187 offset:320
	ds_read_b128 v[76:79], v187 offset:336
	ds_read_b128 v[80:83], v187 offset:352
	ds_read_b128 v[84:87], v187 offset:368
	v_pk_fma_f32 v[32:33], v[88:89], v[122:123], v[32:33] op_sel_hi:[1,0,1]
	v_pk_fma_f32 v[28:29], v[90:91], v[122:123], v[28:29] op_sel_hi:[1,0,1]
	v_pk_fma_f32 v[36:37], v[92:93], v[122:123], v[36:37] op_sel_hi:[1,0,1]
	v_pk_fma_f32 v[34:35], v[94:95], v[122:123], v[34:35] op_sel_hi:[1,0,1]
	v_pk_fma_f32 v[30:31], v[96:97], v[122:123], v[30:31] op_sel_hi:[1,0,1]
	v_pk_fma_f32 v[24:25], v[98:99], v[122:123], v[24:25] op_sel_hi:[1,0,1]
	v_pk_fma_f32 v[22:23], v[100:101], v[122:123], v[22:23] op_sel_hi:[1,0,1]
	v_pk_fma_f32 v[18:19], v[102:103], v[122:123], v[18:19] op_sel_hi:[1,0,1]
	v_pk_fma_f32 v[32:33], v[104:105], v[122:123], v[32:33] op_sel:[0,1,0]
	v_pk_fma_f32 v[28:29], v[106:107], v[122:123], v[28:29] op_sel:[0,1,0]
	v_pk_fma_f32 v[36:37], v[108:109], v[122:123], v[36:37] op_sel:[0,1,0]
	v_pk_fma_f32 v[34:35], v[110:111], v[122:123], v[34:35] op_sel:[0,1,0]
	v_pk_fma_f32 v[30:31], v[112:113], v[122:123], v[30:31] op_sel:[0,1,0]
	v_pk_fma_f32 v[24:25], v[114:115], v[122:123], v[24:25] op_sel:[0,1,0]
	v_pk_fma_f32 v[22:23], v[116:117], v[122:123], v[22:23] op_sel:[0,1,0]
	v_pk_fma_f32 v[18:19], v[118:119], v[122:123], v[18:19] op_sel:[0,1,0]
	s_waitcnt lgkmcnt(0)
	ds_read_b128 v[88:91], v187 offset:384
	ds_read_b128 v[92:95], v187 offset:400
	ds_read_b128 v[96:99], v187 offset:416
	ds_read_b128 v[100:103], v187 offset:432
	ds_read_b128 v[104:107], v187 offset:448
	ds_read_b128 v[108:111], v187 offset:464
	ds_read_b128 v[112:115], v187 offset:480
	ds_read_b128 v[116:119], v187 offset:496
	s_waitcnt vmcnt(40)
	v_pk_fma_f32 v[32:33], v[56:57], v[124:125], v[32:33] op_sel_hi:[1,0,1]
	v_pk_fma_f32 v[28:29], v[58:59], v[124:125], v[28:29] op_sel_hi:[1,0,1]
	v_pk_fma_f32 v[36:37], v[60:61], v[124:125], v[36:37] op_sel_hi:[1,0,1]
	v_pk_fma_f32 v[34:35], v[62:63], v[124:125], v[34:35] op_sel_hi:[1,0,1]
	v_pk_fma_f32 v[30:31], v[64:65], v[124:125], v[30:31] op_sel_hi:[1,0,1]
	v_pk_fma_f32 v[24:25], v[66:67], v[124:125], v[24:25] op_sel_hi:[1,0,1]
	v_pk_fma_f32 v[22:23], v[68:69], v[124:125], v[22:23] op_sel_hi:[1,0,1]
	v_pk_fma_f32 v[18:19], v[70:71], v[124:125], v[18:19] op_sel_hi:[1,0,1]
	v_pk_fma_f32 v[32:33], v[72:73], v[124:125], v[32:33] op_sel:[0,1,0]
	v_pk_fma_f32 v[28:29], v[74:75], v[124:125], v[28:29] op_sel:[0,1,0]
	v_pk_fma_f32 v[36:37], v[76:77], v[124:125], v[36:37] op_sel:[0,1,0]
	v_pk_fma_f32 v[34:35], v[78:79], v[124:125], v[34:35] op_sel:[0,1,0]
	v_pk_fma_f32 v[30:31], v[80:81], v[124:125], v[30:31] op_sel:[0,1,0]
	v_pk_fma_f32 v[24:25], v[82:83], v[124:125], v[24:25] op_sel:[0,1,0]
	v_pk_fma_f32 v[22:23], v[84:85], v[124:125], v[22:23] op_sel:[0,1,0]
	v_pk_fma_f32 v[18:19], v[86:87], v[124:125], v[18:19] op_sel:[0,1,0]
	s_waitcnt lgkmcnt(0)
	ds_read_b128 v[56:59], v187 offset:512
	ds_read_b128 v[60:63], v187 offset:528
	ds_read_b128 v[64:67], v187 offset:544
	ds_read_b128 v[68:71], v187 offset:560
	ds_read_b128 v[72:75], v187 offset:576
	ds_read_b128 v[76:79], v187 offset:592
	ds_read_b128 v[80:83], v187 offset:608
	ds_read_b128 v[84:87], v187 offset:624
	v_pk_fma_f32 v[32:33], v[88:89], v[126:127], v[32:33] op_sel_hi:[1,0,1]
	v_pk_fma_f32 v[28:29], v[90:91], v[126:127], v[28:29] op_sel_hi:[1,0,1]
	v_pk_fma_f32 v[36:37], v[92:93], v[126:127], v[36:37] op_sel_hi:[1,0,1]
	v_pk_fma_f32 v[34:35], v[94:95], v[126:127], v[34:35] op_sel_hi:[1,0,1]
	v_pk_fma_f32 v[30:31], v[96:97], v[126:127], v[30:31] op_sel_hi:[1,0,1]
	v_pk_fma_f32 v[24:25], v[98:99], v[126:127], v[24:25] op_sel_hi:[1,0,1]
	v_pk_fma_f32 v[22:23], v[100:101], v[126:127], v[22:23] op_sel_hi:[1,0,1]
	v_pk_fma_f32 v[18:19], v[102:103], v[126:127], v[18:19] op_sel_hi:[1,0,1]
	v_pk_fma_f32 v[32:33], v[104:105], v[126:127], v[32:33] op_sel:[0,1,0]
	v_pk_fma_f32 v[28:29], v[106:107], v[126:127], v[28:29] op_sel:[0,1,0]
	v_pk_fma_f32 v[36:37], v[108:109], v[126:127], v[36:37] op_sel:[0,1,0]
	v_pk_fma_f32 v[34:35], v[110:111], v[126:127], v[34:35] op_sel:[0,1,0]
	v_pk_fma_f32 v[30:31], v[112:113], v[126:127], v[30:31] op_sel:[0,1,0]
	v_pk_fma_f32 v[24:25], v[114:115], v[126:127], v[24:25] op_sel:[0,1,0]
	v_pk_fma_f32 v[22:23], v[116:117], v[126:127], v[22:23] op_sel:[0,1,0]
	v_pk_fma_f32 v[18:19], v[118:119], v[126:127], v[18:19] op_sel:[0,1,0]
	s_waitcnt lgkmcnt(0)
	ds_read_b128 v[88:91], v187 offset:640
	ds_read_b128 v[92:95], v187 offset:656
	ds_read_b128 v[96:99], v187 offset:672
	ds_read_b128 v[100:103], v187 offset:688
	ds_read_b128 v[104:107], v187 offset:704
	ds_read_b128 v[108:111], v187 offset:720
	ds_read_b128 v[112:115], v187 offset:736
	ds_read_b128 v[116:119], v187 offset:752
	global_load_dword v168, v186, s[6:7] offset:-4096
	global_load_dword v169, v186, s[6:7]
	s_add_u32 s6, s6, 0x2000
	s_addc_u32 s7, s7, 0
	global_load_dword v170, v186, s[6:7] offset:-4096
	global_load_dword v171, v186, s[6:7]
	s_add_u32 s6, s6, 0x2000
	s_addc_u32 s7, s7, 0
	global_load_dword v172, v186, s[6:7] offset:-4096
	global_load_dword v173, v186, s[6:7]
	s_add_u32 s6, s6, 0x2000
	s_addc_u32 s7, s7, 0
	global_load_dword v174, v186, s[6:7] offset:-4096
	global_load_dword v175, v186, s[6:7]
	s_add_u32 s6, s6, 0x2000
	s_addc_u32 s7, s7, 0
	s_waitcnt vmcnt(44)
;     ...
;             for (int cc = 0; cc < 2; ++cc) { const int col = F.tid + cc * 512; float acc[16];
; #pragma unroll
;                 for (int p = 0; p < 16; ++p) acc[p] = 0.f;
;                 for (int k = 0; k < 64; ++k) { const float w = w3[k * 1024 + col];
; #pragma unroll
;                     for (int p = 0; p < 16; ++p) acc[p] += f2[p * 64 + k] * w; }
	v_pk_fma_f32 v[32:33], v[56:57], v[128:129], v[32:33] op_sel_hi:[1,0,1]
	v_pk_fma_f32 v[28:29], v[58:59], v[128:129], v[28:29] op_sel_hi:[1,0,1]
	v_pk_fma_f32 v[36:37], v[60:61], v[128:129], v[36:37] op_sel_hi:[1,0,1]
	v_pk_fma_f32 v[34:35], v[62:63], v[128:129], v[34:35] op_sel_hi:[1,0,1]
	v_pk_fma_f32 v[30:31], v[64:65], v[128:129], v[30:31] op_sel_hi:[1,0,1]
	v_pk_fma_f32 v[24:25], v[66:67], v[128:129], v[24:25] op_sel_hi:[1,0,1]
	v_pk_fma_f32 v[22:23], v[68:69], v[128:129], v[22:23] op_sel_hi:[1,0,1]
	v_pk_fma_f32 v[18:19], v[70:71], v[128:129], v[18:19] op_sel_hi:[1,0,1]
	v_pk_fma_f32 v[32:33], v[72:73], v[128:129], v[32:33] op_sel:[0,1,0]
	v_pk_fma_f32 v[28:29], v[74:75], v[128:129], v[28:29] op_sel:[0,1,0]
	v_pk_fma_f32 v[36:37], v[76:77], v[128:129], v[36:37] op_sel:[0,1,0]
	v_pk_fma_f32 v[34:35], v[78:79], v[128:129], v[34:35] op_sel:[0,1,0]
	v_pk_fma_f32 v[30:31], v[80:81], v[128:129], v[30:31] op_sel:[0,1,0]
	v_pk_fma_f32 v[24:25], v[82:83], v[128:129], v[24:25] op_sel:[0,1,0]
	v_pk_fma_f32 v[22:23], v[84:85], v[128:129], v[22:23] op_sel:[0,1,0]
	v_pk_fma_f32 v[18:19], v[86:87], v[128:129], v[18:19] op_sel:[0,1,0]
	s_waitcnt lgkmcnt(0)
	ds_read_b128 v[56:59], v187 offset:768
	ds_read_b128 v[60:63], v187 offset:784
	ds_read_b128 v[64:67], v187 offset:800
	ds_read_b128 v[68:71], v187 offset:816
	ds_read_b128 v[72:75], v187 offset:832
	ds_read_b128 v[76:79], v187 offset:848
	ds_read_b128 v[80:83], v187 offset:864
	ds_read_b128 v[84:87], v187 offset:880
	v_pk_fma_f32 v[32:33], v[88:89], v[130:131], v[32:33] op_sel_hi:[1,0,1]
	v_pk_fma_f32 v[28:29], v[90:91], v[130:131], v[28:29] op_sel_hi:[1,0,1]
	v_pk_fma_f32 v[36:37], v[92:93], v[130:131], v[36:37] op_sel_hi:[1,0,1]
	v_pk_fma_f32 v[34:35], v[94:95], v[130:131], v[34:35] op_sel_hi:[1,0,1]
	v_pk_fma_f32 v[30:31], v[96:97], v[130:131], v[30:31] op_sel_hi:[1,0,1]
	v_pk_fma_f32 v[24:25], v[98:99], v[130:131], v[24:25] op_sel_hi:[1,0,1]
	v_pk_fma_f32 v[22:23], v[100:101], v[130:131], v[22:23] op_sel_hi:[1,0,1]
	v_pk_fma_f32 v[18:19], v[102:103], v[130:131], v[18:19] op_sel_hi:[1,0,1]
	v_pk_fma_f32 v[32:33], v[104:105], v[130:131], v[32:33] op_sel:[0,1,0]
	v_pk_fma_f32 v[28:29], v[106:107], v[130:131], v[28:29] op_sel:[0,1,0]
	v_pk_fma_f32 v[36:37], v[108:109], v[130:131], v[36:37] op_sel:[0,1,0]
	v_pk_fma_f32 v[34:35], v[110:111], v[130:131], v[34:35] op_sel:[0,1,0]
	v_pk_fma_f32 v[30:31], v[112:113], v[130:131], v[30:31] op_sel:[0,1,0]
	v_pk_fma_f32 v[24:25], v[114:115], v[130:131], v[24:25] op_sel:[0,1,0]
	v_pk_fma_f32 v[22:23], v[116:117], v[130:131], v[22:23] op_sel:[0,1,0]
	v_pk_fma_f32 v[18:19], v[118:119], v[130:131], v[18:19] op_sel:[0,1,0]
	s_waitcnt lgkmcnt(0)
	ds_read_b128 v[88:91], v187 offset:896
	ds_read_b128 v[92:95], v187 offset:912
	ds_read_b128 v[96:99], v187 offset:928
	ds_read_b128 v[100:103], v187 offset:944
	ds_read_b128 v[104:107], v187 offset:960
	ds_read_b128 v[108:111], v187 offset:976
	ds_read_b128 v[112:115], v187 offset:992
	ds_read_b128 v[116:119], v187 offset:1008
	s_waitcnt vmcnt(40)
	v_pk_fma_f32 v[32:33], v[56:57], v[132:133], v[32:33] op_sel_hi:[1,0,1]
	v_pk_fma_f32 v[28:29], v[58:59], v[132:133], v[28:29] op_sel_hi:[1,0,1]
	v_pk_fma_f32 v[36:37], v[60:61], v[132:133], v[36:37] op_sel_hi:[1,0,1]
	v_pk_fma_f32 v[34:35], v[62:63], v[132:133], v[34:35] op_sel_hi:[1,0,1]
	v_pk_fma_f32 v[30:31], v[64:65], v[132:133], v[30:31] op_sel_hi:[1,0,1]
	v_pk_fma_f32 v[24:25], v[66:67], v[132:133], v[24:25] op_sel_hi:[1,0,1]
	v_pk_fma_f32 v[22:23], v[68:69], v[132:133], v[22:23] op_sel_hi:[1,0,1]
	v_pk_fma_f32 v[18:19], v[70:71], v[132:133], v[18:19] op_sel_hi:[1,0,1]
	v_pk_fma_f32 v[32:33], v[72:73], v[132:133], v[32:33] op_sel:[0,1,0]
	v_pk_fma_f32 v[28:29], v[74:75], v[132:133], v[28:29] op_sel:[0,1,0]
	v_pk_fma_f32 v[36:37], v[76:77], v[132:133], v[36:37] op_sel:[0,1,0]
	v_pk_fma_f32 v[34:35], v[78:79], v[132:133], v[34:35] op_sel:[0,1,0]
	v_pk_fma_f32 v[30:31], v[80:81], v[132:133], v[30:31] op_sel:[0,1,0]
	v_pk_fma_f32 v[24:25], v[82:83], v[132:133], v[24:25] op_sel:[0,1,0]
	v_pk_fma_f32 v[22:23], v[84:85], v[132:133], v[22:23] op_sel:[0,1,0]
	v_pk_fma_f32 v[18:19], v[86:87], v[132:133], v[18:19] op_sel:[0,1,0]
	s_waitcnt lgkmcnt(0)
	ds_read_b128 v[56:59], v187 offset:1024
	ds_read_b128 v[60:63], v187 offset:1040
	ds_read_b128 v[64:67], v187 offset:1056
	ds_read_b128 v[68:71], v187 offset:1072
	ds_read_b128 v[72:75], v187 offset:1088
	ds_read_b128 v[76:79], v187 offset:1104
	ds_read_b128 v[80:83], v187 offset:1120
	ds_read_b128 v[84:87], v187 offset:1136
	v_pk_fma_f32 v[32:33], v[88:89], v[134:135], v[32:33] op_sel_hi:[1,0,1]
	v_pk_fma_f32 v[28:29], v[90:91], v[134:135], v[28:29] op_sel_hi:[1,0,1]
	v_pk_fma_f32 v[36:37], v[92:93], v[134:135], v[36:37] op_sel_hi:[1,0,1]
	v_pk_fma_f32 v[34:35], v[94:95], v[134:135], v[34:35] op_sel_hi:[1,0,1]
	v_pk_fma_f32 v[30:31], v[96:97], v[134:135], v[30:31] op_sel_hi:[1,0,1]
	v_pk_fma_f32 v[24:25], v[98:99], v[134:135], v[24:25] op_sel_hi:[1,0,1]
	v_pk_fma_f32 v[22:23], v[100:101], v[134:135], v[22:23] op_sel_hi:[1,0,1]
	v_pk_fma_f32 v[18:19], v[102:103], v[134:135], v[18:19] op_sel_hi:[1,0,1]
	v_pk_fma_f32 v[32:33], v[104:105], v[134:135], v[32:33] op_sel:[0,1,0]
	v_pk_fma_f32 v[28:29], v[106:107], v[134:135], v[28:29] op_sel:[0,1,0]
	v_pk_fma_f32 v[36:37], v[108:109], v[134:135], v[36:37] op_sel:[0,1,0]
	v_pk_fma_f32 v[34:35], v[110:111], v[134:135], v[34:35] op_sel:[0,1,0]
	v_pk_fma_f32 v[30:31], v[112:113], v[134:135], v[30:31] op_sel:[0,1,0]
	v_pk_fma_f32 v[24:25], v[114:115], v[134:135], v[24:25] op_sel:[0,1,0]
	v_pk_fma_f32 v[22:23], v[116:117], v[134:135], v[22:23] op_sel:[0,1,0]
	v_pk_fma_f32 v[18:19], v[118:119], v[134:135], v[18:19] op_sel:[0,1,0]
	s_waitcnt lgkmcnt(0)
;     ...
;             for (int cc = 0; cc < 2; ++cc) { const int col = F.tid + cc * 512; float acc[16];
; #pragma unroll
;                 for (int p = 0; p < 16; ++p) acc[p] = 0.f;
;                 for (int k = 0; k < 64; ++k) { const float w = w3[k * 1024 + col];
; #pragma unroll
;                     for (int p = 0; p < 16; ++p) acc[p] += f2[p * 64 + k] * w; }
	ds_read_b128 v[88:91], v187 offset:1152
	ds_read_b128 v[92:95], v187 offset:1168
	ds_read_b128 v[96:99], v187 offset:1184
	ds_read_b128 v[100:103], v187 offset:1200
	ds_read_b128 v[104:107], v187 offset:1216
	ds_read_b128 v[108:111], v187 offset:1232
	ds_read_b128 v[112:115], v187 offset:1248
	ds_read_b128 v[116:119], v187 offset:1264
	global_load_dword v176, v186, s[6:7] offset:-4096
	global_load_dword v177, v186, s[6:7]
	s_add_u32 s6, s6, 0x2000
	s_addc_u32 s7, s7, 0
	global_load_dword v178, v186, s[6:7] offset:-4096
	global_load_dword v179, v186, s[6:7]
	s_add_u32 s6, s6, 0x2000
	s_addc_u32 s7, s7, 0
	global_load_dword v180, v186, s[6:7] offset:-4096
	global_load_dword v182, v186, s[6:7]
	s_add_u32 s6, s6, 0x2000
	s_addc_u32 s7, s7, 0
	global_load_dword v183, v186, s[6:7] offset:-4096
	global_load_dword v184, v186, s[6:7]
	s_waitcnt vmcnt(44)
	v_pk_fma_f32 v[32:33], v[56:57], v[136:137], v[32:33] op_sel_hi:[1,0,1]
	v_pk_fma_f32 v[28:29], v[58:59], v[136:137], v[28:29] op_sel_hi:[1,0,1]
	v_pk_fma_f32 v[36:37], v[60:61], v[136:137], v[36:37] op_sel_hi:[1,0,1]
	v_pk_fma_f32 v[34:35], v[62:63], v[136:137], v[34:35] op_sel_hi:[1,0,1]
	v_pk_fma_f32 v[30:31], v[64:65], v[136:137], v[30:31] op_sel_hi:[1,0,1]
	v_pk_fma_f32 v[24:25], v[66:67], v[136:137], v[24:25] op_sel_hi:[1,0,1]
	v_pk_fma_f32 v[22:23], v[68:69], v[136:137], v[22:23] op_sel_hi:[1,0,1]
	v_pk_fma_f32 v[18:19], v[70:71], v[136:137], v[18:19] op_sel_hi:[1,0,1]
	v_pk_fma_f32 v[32:33], v[72:73], v[136:137], v[32:33] op_sel:[0,1,0]
	v_pk_fma_f32 v[28:29], v[74:75], v[136:137], v[28:29] op_sel:[0,1,0]
	v_pk_fma_f32 v[36:37], v[76:77], v[136:137], v[36:37] op_sel:[0,1,0]
	v_pk_fma_f32 v[34:35], v[78:79], v[136:137], v[34:35] op_sel:[0,1,0]
	v_pk_fma_f32 v[30:31], v[80:81], v[136:137], v[30:31] op_sel:[0,1,0]
	v_pk_fma_f32 v[24:25], v[82:83], v[136:137], v[24:25] op_sel:[0,1,0]
	v_pk_fma_f32 v[22:23], v[84:85], v[136:137], v[22:23] op_sel:[0,1,0]
	v_pk_fma_f32 v[18:19], v[86:87], v[136:137], v[18:19] op_sel:[0,1,0]
	s_waitcnt lgkmcnt(0)
	ds_read_b128 v[56:59], v187 offset:1280
	ds_read_b128 v[60:63], v187 offset:1296
	ds_read_b128 v[64:67], v187 offset:1312
	ds_read_b128 v[68:71], v187 offset:1328
	ds_read_b128 v[72:75], v187 offset:1344
	ds_read_b128 v[76:79], v187 offset:1360
	ds_read_b128 v[80:83], v187 offset:1376
	ds_read_b128 v[84:87], v187 offset:1392
	v_pk_fma_f32 v[32:33], v[88:89], v[138:139], v[32:33] op_sel_hi:[1,0,1]
	v_pk_fma_f32 v[28:29], v[90:91], v[138:139], v[28:29] op_sel_hi:[1,0,1]
	v_pk_fma_f32 v[36:37], v[92:93], v[138:139], v[36:37] op_sel_hi:[1,0,1]
	v_pk_fma_f32 v[34:35], v[94:95], v[138:139], v[34:35] op_sel_hi:[1,0,1]
	v_pk_fma_f32 v[30:31], v[96:97], v[138:139], v[30:31] op_sel_hi:[1,0,1]
	v_pk_fma_f32 v[24:25], v[98:99], v[138:139], v[24:25] op_sel_hi:[1,0,1]
	v_pk_fma_f32 v[22:23], v[100:101], v[138:139], v[22:23] op_sel_hi:[1,0,1]
	v_pk_fma_f32 v[18:19], v[102:103], v[138:139], v[18:19] op_sel_hi:[1,0,1]
	v_pk_fma_f32 v[32:33], v[104:105], v[138:139], v[32:33] op_sel:[0,1,0]
	v_pk_fma_f32 v[28:29], v[106:107], v[138:139], v[28:29] op_sel:[0,1,0]
	v_pk_fma_f32 v[36:37], v[108:109], v[138:139], v[36:37] op_sel:[0,1,0]
	v_pk_fma_f32 v[34:35], v[110:111], v[138:139], v[34:35] op_sel:[0,1,0]
	v_pk_fma_f32 v[30:31], v[112:113], v[138:139], v[30:31] op_sel:[0,1,0]
	v_pk_fma_f32 v[24:25], v[114:115], v[138:139], v[24:25] op_sel:[0,1,0]
	v_pk_fma_f32 v[22:23], v[116:117], v[138:139], v[22:23] op_sel:[0,1,0]
	v_pk_fma_f32 v[18:19], v[118:119], v[138:139], v[18:19] op_sel:[0,1,0]
	s_waitcnt lgkmcnt(0)
	ds_read_b128 v[88:91], v187 offset:1408
	ds_read_b128 v[92:95], v187 offset:1424
	ds_read_b128 v[96:99], v187 offset:1440
	ds_read_b128 v[100:103], v187 offset:1456
	ds_read_b128 v[104:107], v187 offset:1472
	ds_read_b128 v[108:111], v187 offset:1488
	ds_read_b128 v[112:115], v187 offset:1504
	ds_read_b128 v[116:119], v187 offset:1520
	s_waitcnt vmcnt(40)
	v_pk_fma_f32 v[32:33], v[56:57], v[140:141], v[32:33] op_sel_hi:[1,0,1]
	v_pk_fma_f32 v[28:29], v[58:59], v[140:141], v[28:29] op_sel_hi:[1,0,1]
	v_pk_fma_f32 v[36:37], v[60:61], v[140:141], v[36:37] op_sel_hi:[1,0,1]
	v_pk_fma_f32 v[34:35], v[62:63], v[140:141], v[34:35] op_sel_hi:[1,0,1]
	v_pk_fma_f32 v[30:31], v[64:65], v[140:141], v[30:31] op_sel_hi:[1,0,1]
	v_pk_fma_f32 v[24:25], v[66:67], v[140:141], v[24:25] op_sel_hi:[1,0,1]
	v_pk_fma_f32 v[22:23], v[68:69], v[140:141], v[22:23] op_sel_hi:[1,0,1]
	v_pk_fma_f32 v[18:19], v[70:71], v[140:141], v[18:19] op_sel_hi:[1,0,1]
	v_pk_fma_f32 v[32:33], v[72:73], v[140:141], v[32:33] op_sel:[0,1,0]
	v_pk_fma_f32 v[28:29], v[74:75], v[140:141], v[28:29] op_sel:[0,1,0]
	v_pk_fma_f32 v[36:37], v[76:77], v[140:141], v[36:37] op_sel:[0,1,0]
	v_pk_fma_f32 v[34:35], v[78:79], v[140:141], v[34:35] op_sel:[0,1,0]
	v_pk_fma_f32 v[30:31], v[80:81], v[140:141], v[30:31] op_sel:[0,1,0]
	v_pk_fma_f32 v[24:25], v[82:83], v[140:141], v[24:25] op_sel:[0,1,0]
	v_pk_fma_f32 v[22:23], v[84:85], v[140:141], v[22:23] op_sel:[0,1,0]
	v_pk_fma_f32 v[18:19], v[86:87], v[140:141], v[18:19] op_sel:[0,1,0]
	s_waitcnt lgkmcnt(0)
;     ...
;             for (int cc = 0; cc < 2; ++cc) { const int col = F.tid + cc * 512; float acc[16];
; #pragma unroll
;                 for (int p = 0; p < 16; ++p) acc[p] = 0.f;
;                 for (int k = 0; k < 64; ++k) { const float w = w3[k * 1024 + col];
; #pragma unroll
;                     for (int p = 0; p < 16; ++p) acc[p] += f2[p * 64 + k] * w; }
	ds_read_b128 v[56:59], v187 offset:1536
	ds_read_b128 v[60:63], v187 offset:1552
	ds_read_b128 v[64:67], v187 offset:1568
	ds_read_b128 v[68:71], v187 offset:1584
	ds_read_b128 v[72:75], v187 offset:1600
	ds_read_b128 v[76:79], v187 offset:1616
	ds_read_b128 v[80:83], v187 offset:1632
	ds_read_b128 v[84:87], v187 offset:1648
	v_pk_fma_f32 v[32:33], v[88:89], v[142:143], v[32:33] op_sel_hi:[1,0,1]
	v_pk_fma_f32 v[28:29], v[90:91], v[142:143], v[28:29] op_sel_hi:[1,0,1]
	v_pk_fma_f32 v[36:37], v[92:93], v[142:143], v[36:37] op_sel_hi:[1,0,1]
	v_pk_fma_f32 v[34:35], v[94:95], v[142:143], v[34:35] op_sel_hi:[1,0,1]
	v_pk_fma_f32 v[30:31], v[96:97], v[142:143], v[30:31] op_sel_hi:[1,0,1]
	v_pk_fma_f32 v[24:25], v[98:99], v[142:143], v[24:25] op_sel_hi:[1,0,1]
	v_pk_fma_f32 v[22:23], v[100:101], v[142:143], v[22:23] op_sel_hi:[1,0,1]
	v_pk_fma_f32 v[18:19], v[102:103], v[142:143], v[18:19] op_sel_hi:[1,0,1]
	v_pk_fma_f32 v[32:33], v[104:105], v[142:143], v[32:33] op_sel:[0,1,0]
	v_pk_fma_f32 v[28:29], v[106:107], v[142:143], v[28:29] op_sel:[0,1,0]
	v_pk_fma_f32 v[36:37], v[108:109], v[142:143], v[36:37] op_sel:[0,1,0]
	v_pk_fma_f32 v[34:35], v[110:111], v[142:143], v[34:35] op_sel:[0,1,0]
	v_pk_fma_f32 v[30:31], v[112:113], v[142:143], v[30:31] op_sel:[0,1,0]
	v_pk_fma_f32 v[24:25], v[114:115], v[142:143], v[24:25] op_sel:[0,1,0]
	v_pk_fma_f32 v[22:23], v[116:117], v[142:143], v[22:23] op_sel:[0,1,0]
	v_pk_fma_f32 v[18:19], v[118:119], v[142:143], v[18:19] op_sel:[0,1,0]
	s_waitcnt lgkmcnt(0)
	ds_read_b128 v[88:91], v187 offset:1664
	ds_read_b128 v[92:95], v187 offset:1680
	ds_read_b128 v[96:99], v187 offset:1696
	ds_read_b128 v[100:103], v187 offset:1712
	ds_read_b128 v[104:107], v187 offset:1728
	ds_read_b128 v[108:111], v187 offset:1744
	ds_read_b128 v[112:115], v187 offset:1760
	ds_read_b128 v[116:119], v187 offset:1776
	s_waitcnt vmcnt(36)
	v_pk_fma_f32 v[32:33], v[56:57], v[144:145], v[32:33] op_sel_hi:[1,0,1]
	v_pk_fma_f32 v[28:29], v[58:59], v[144:145], v[28:29] op_sel_hi:[1,0,1]
	v_pk_fma_f32 v[36:37], v[60:61], v[144:145], v[36:37] op_sel_hi:[1,0,1]
	v_pk_fma_f32 v[34:35], v[62:63], v[144:145], v[34:35] op_sel_hi:[1,0,1]
	v_pk_fma_f32 v[30:31], v[64:65], v[144:145], v[30:31] op_sel_hi:[1,0,1]
	v_pk_fma_f32 v[24:25], v[66:67], v[144:145], v[24:25] op_sel_hi:[1,0,1]
	v_pk_fma_f32 v[22:23], v[68:69], v[144:145], v[22:23] op_sel_hi:[1,0,1]
	v_pk_fma_f32 v[18:19], v[70:71], v[144:145], v[18:19] op_sel_hi:[1,0,1]
	v_pk_fma_f32 v[32:33], v[72:73], v[144:145], v[32:33] op_sel:[0,1,0]
	v_pk_fma_f32 v[28:29], v[74:75], v[144:145], v[28:29] op_sel:[0,1,0]
	v_pk_fma_f32 v[36:37], v[76:77], v[144:145], v[36:37] op_sel:[0,1,0]
	v_pk_fma_f32 v[34:35], v[78:79], v[144:145], v[34:35] op_sel:[0,1,0]
	v_pk_fma_f32 v[30:31], v[80:81], v[144:145], v[30:31] op_sel:[0,1,0]
	v_pk_fma_f32 v[24:25], v[82:83], v[144:145], v[24:25] op_sel:[0,1,0]
	v_pk_fma_f32 v[22:23], v[84:85], v[144:145], v[22:23] op_sel:[0,1,0]
	v_pk_fma_f32 v[18:19], v[86:87], v[144:145], v[18:19] op_sel:[0,1,0]
	s_waitcnt lgkmcnt(0)
	ds_read_b128 v[56:59], v187 offset:1792
	ds_read_b128 v[60:63], v187 offset:1808
	ds_read_b128 v[64:67], v187 offset:1824
	ds_read_b128 v[68:71], v187 offset:1840
	ds_read_b128 v[72:75], v187 offset:1856
	ds_read_b128 v[76:79], v187 offset:1872
	ds_read_b128 v[80:83], v187 offset:1888
	ds_read_b128 v[84:87], v187 offset:1904
	v_pk_fma_f32 v[32:33], v[88:89], v[146:147], v[32:33] op_sel_hi:[1,0,1]
	v_pk_fma_f32 v[28:29], v[90:91], v[146:147], v[28:29] op_sel_hi:[1,0,1]
	v_pk_fma_f32 v[36:37], v[92:93], v[146:147], v[36:37] op_sel_hi:[1,0,1]
	v_pk_fma_f32 v[34:35], v[94:95], v[146:147], v[34:35] op_sel_hi:[1,0,1]
	v_pk_fma_f32 v[30:31], v[96:97], v[146:147], v[30:31] op_sel_hi:[1,0,1]
	v_pk_fma_f32 v[24:25], v[98:99], v[146:147], v[24:25] op_sel_hi:[1,0,1]
	v_pk_fma_f32 v[22:23], v[100:101], v[146:147], v[22:23] op_sel_hi:[1,0,1]
	v_pk_fma_f32 v[18:19], v[102:103], v[146:147], v[18:19] op_sel_hi:[1,0,1]
	v_pk_fma_f32 v[32:33], v[104:105], v[146:147], v[32:33] op_sel:[0,1,0]
	v_pk_fma_f32 v[28:29], v[106:107], v[146:147], v[28:29] op_sel:[0,1,0]
	v_pk_fma_f32 v[36:37], v[108:109], v[146:147], v[36:37] op_sel:[0,1,0]
	v_pk_fma_f32 v[34:35], v[110:111], v[146:147], v[34:35] op_sel:[0,1,0]
	v_pk_fma_f32 v[30:31], v[112:113], v[146:147], v[30:31] op_sel:[0,1,0]
	v_pk_fma_f32 v[24:25], v[114:115], v[146:147], v[24:25] op_sel:[0,1,0]
	v_pk_fma_f32 v[22:23], v[116:117], v[146:147], v[22:23] op_sel:[0,1,0]
	v_pk_fma_f32 v[18:19], v[118:119], v[146:147], v[18:19] op_sel:[0,1,0]
	s_waitcnt lgkmcnt(0)
	ds_read_b128 v[88:91], v187 offset:1920
	ds_read_b128 v[92:95], v187 offset:1936
	ds_read_b128 v[96:99], v187 offset:1952
	ds_read_b128 v[100:103], v187 offset:1968
	ds_read_b128 v[104:107], v187 offset:1984
	ds_read_b128 v[108:111], v187 offset:2000
	ds_read_b128 v[112:115], v187 offset:2016
	ds_read_b128 v[116:119], v187 offset:2032
	s_waitcnt vmcnt(32)
	v_pk_fma_f32 v[32:33], v[56:57], v[148:149], v[32:33] op_sel_hi:[1,0,1]
	v_pk_fma_f32 v[28:29], v[58:59], v[148:149], v[28:29] op_sel_hi:[1,0,1]
	v_pk_fma_f32 v[36:37], v[60:61], v[148:149], v[36:37] op_sel_hi:[1,0,1]
	v_pk_fma_f32 v[34:35], v[62:63], v[148:149], v[34:35] op_sel_hi:[1,0,1]
	v_pk_fma_f32 v[30:31], v[64:65], v[148:149], v[30:31] op_sel_hi:[1,0,1]
	v_pk_fma_f32 v[24:25], v[66:67], v[148:149], v[24:25] op_sel_hi:[1,0,1]
	v_pk_fma_f32 v[22:23], v[68:69], v[148:149], v[22:23] op_sel_hi:[1,0,1]
	v_pk_fma_f32 v[18:19], v[70:71], v[148:149], v[18:19] op_sel_hi:[1,0,1]
	v_pk_fma_f32 v[32:33], v[72:73], v[148:149], v[32:33] op_sel:[0,1,0]
	v_pk_fma_f32 v[28:29], v[74:75], v[148:149], v[28:29] op_sel:[0,1,0]
	v_pk_fma_f32 v[36:37], v[76:77], v[148:149], v[36:37] op_sel:[0,1,0]
	v_pk_fma_f32 v[34:35], v[78:79], v[148:149], v[34:35] op_sel:[0,1,0]
	v_pk_fma_f32 v[30:31], v[80:81], v[148:149], v[30:31] op_sel:[0,1,0]
	v_pk_fma_f32 v[24:25], v[82:83], v[148:149], v[24:25] op_sel:[0,1,0]
	v_pk_fma_f32 v[22:23], v[84:85], v[148:149], v[22:23] op_sel:[0,1,0]
	v_pk_fma_f32 v[18:19], v[86:87], v[148:149], v[18:19] op_sel:[0,1,0]
	s_waitcnt lgkmcnt(0)
;     ...
;             for (int cc = 0; cc < 2; ++cc) { const int col = F.tid + cc * 512; float acc[16];
; #pragma unroll
;                 for (int p = 0; p < 16; ++p) acc[p] = 0.f;
;                 for (int k = 0; k < 64; ++k) { const float w = w3[k * 1024 + col];
; #pragma unroll
;                     for (int p = 0; p < 16; ++p) acc[p] += f2[p * 64 + k] * w; }
	ds_read_b128 v[56:59], v187 offset:2048
	ds_read_b128 v[60:63], v187 offset:2064
	ds_read_b128 v[64:67], v187 offset:2080
	ds_read_b128 v[68:71], v187 offset:2096
	ds_read_b128 v[72:75], v187 offset:2112
	ds_read_b128 v[76:79], v187 offset:2128
	ds_read_b128 v[80:83], v187 offset:2144
	ds_read_b128 v[84:87], v187 offset:2160
	v_pk_fma_f32 v[32:33], v[88:89], v[150:151], v[32:33] op_sel_hi:[1,0,1]
	v_pk_fma_f32 v[28:29], v[90:91], v[150:151], v[28:29] op_sel_hi:[1,0,1]
	v_pk_fma_f32 v[36:37], v[92:93], v[150:151], v[36:37] op_sel_hi:[1,0,1]
	v_pk_fma_f32 v[34:35], v[94:95], v[150:151], v[34:35] op_sel_hi:[1,0,1]
	v_pk_fma_f32 v[30:31], v[96:97], v[150:151], v[30:31] op_sel_hi:[1,0,1]
	v_pk_fma_f32 v[24:25], v[98:99], v[150:151], v[24:25] op_sel_hi:[1,0,1]
	v_pk_fma_f32 v[22:23], v[100:101], v[150:151], v[22:23] op_sel_hi:[1,0,1]
	v_pk_fma_f32 v[18:19], v[102:103], v[150:151], v[18:19] op_sel_hi:[1,0,1]
	v_pk_fma_f32 v[32:33], v[104:105], v[150:151], v[32:33] op_sel:[0,1,0]
	v_pk_fma_f32 v[28:29], v[106:107], v[150:151], v[28:29] op_sel:[0,1,0]
	v_pk_fma_f32 v[36:37], v[108:109], v[150:151], v[36:37] op_sel:[0,1,0]
	v_pk_fma_f32 v[34:35], v[110:111], v[150:151], v[34:35] op_sel:[0,1,0]
	v_pk_fma_f32 v[30:31], v[112:113], v[150:151], v[30:31] op_sel:[0,1,0]
	v_pk_fma_f32 v[24:25], v[114:115], v[150:151], v[24:25] op_sel:[0,1,0]
	v_pk_fma_f32 v[22:23], v[116:117], v[150:151], v[22:23] op_sel:[0,1,0]
	v_pk_fma_f32 v[18:19], v[118:119], v[150:151], v[18:19] op_sel:[0,1,0]
	s_waitcnt lgkmcnt(0)
	ds_read_b128 v[88:91], v187 offset:2176
	ds_read_b128 v[92:95], v187 offset:2192
	ds_read_b128 v[96:99], v187 offset:2208
	ds_read_b128 v[100:103], v187 offset:2224
	ds_read_b128 v[104:107], v187 offset:2240
	ds_read_b128 v[108:111], v187 offset:2256
	ds_read_b128 v[112:115], v187 offset:2272
	ds_read_b128 v[116:119], v187 offset:2288
	s_waitcnt vmcnt(28)
	v_pk_fma_f32 v[32:33], v[56:57], v[152:153], v[32:33] op_sel_hi:[1,0,1]
	v_pk_fma_f32 v[28:29], v[58:59], v[152:153], v[28:29] op_sel_hi:[1,0,1]
	v_pk_fma_f32 v[36:37], v[60:61], v[152:153], v[36:37] op_sel_hi:[1,0,1]
	v_pk_fma_f32 v[34:35], v[62:63], v[152:153], v[34:35] op_sel_hi:[1,0,1]
	v_pk_fma_f32 v[30:31], v[64:65], v[152:153], v[30:31] op_sel_hi:[1,0,1]
	v_pk_fma_f32 v[24:25], v[66:67], v[152:153], v[24:25] op_sel_hi:[1,0,1]
	v_pk_fma_f32 v[22:23], v[68:69], v[152:153], v[22:23] op_sel_hi:[1,0,1]
	v_pk_fma_f32 v[18:19], v[70:71], v[152:153], v[18:19] op_sel_hi:[1,0,1]
	v_pk_fma_f32 v[32:33], v[72:73], v[152:153], v[32:33] op_sel:[0,1,0]
	v_pk_fma_f32 v[28:29], v[74:75], v[152:153], v[28:29] op_sel:[0,1,0]
	v_pk_fma_f32 v[36:37], v[76:77], v[152:153], v[36:37] op_sel:[0,1,0]
	v_pk_fma_f32 v[34:35], v[78:79], v[152:153], v[34:35] op_sel:[0,1,0]
	v_pk_fma_f32 v[30:31], v[80:81], v[152:153], v[30:31] op_sel:[0,1,0]
	v_pk_fma_f32 v[24:25], v[82:83], v[152:153], v[24:25] op_sel:[0,1,0]
	v_pk_fma_f32 v[22:23], v[84:85], v[152:153], v[22:23] op_sel:[0,1,0]
	v_pk_fma_f32 v[18:19], v[86:87], v[152:153], v[18:19] op_sel:[0,1,0]
	s_waitcnt lgkmcnt(0)
	ds_read_b128 v[56:59], v187 offset:2304
	ds_read_b128 v[60:63], v187 offset:2320
	ds_read_b128 v[64:67], v187 offset:2336
	ds_read_b128 v[68:71], v187 offset:2352
	ds_read_b128 v[72:75], v187 offset:2368
	ds_read_b128 v[76:79], v187 offset:2384
	ds_read_b128 v[80:83], v187 offset:2400
	ds_read_b128 v[84:87], v187 offset:2416
	v_pk_fma_f32 v[32:33], v[88:89], v[154:155], v[32:33] op_sel_hi:[1,0,1]
	v_pk_fma_f32 v[28:29], v[90:91], v[154:155], v[28:29] op_sel_hi:[1,0,1]
	v_pk_fma_f32 v[36:37], v[92:93], v[154:155], v[36:37] op_sel_hi:[1,0,1]
	v_pk_fma_f32 v[34:35], v[94:95], v[154:155], v[34:35] op_sel_hi:[1,0,1]
	v_pk_fma_f32 v[30:31], v[96:97], v[154:155], v[30:31] op_sel_hi:[1,0,1]
	v_pk_fma_f32 v[24:25], v[98:99], v[154:155], v[24:25] op_sel_hi:[1,0,1]
	v_pk_fma_f32 v[22:23], v[100:101], v[154:155], v[22:23] op_sel_hi:[1,0,1]
	v_pk_fma_f32 v[18:19], v[102:103], v[154:155], v[18:19] op_sel_hi:[1,0,1]
	v_pk_fma_f32 v[32:33], v[104:105], v[154:155], v[32:33] op_sel:[0,1,0]
	v_pk_fma_f32 v[28:29], v[106:107], v[154:155], v[28:29] op_sel:[0,1,0]
	v_pk_fma_f32 v[36:37], v[108:109], v[154:155], v[36:37] op_sel:[0,1,0]
	v_pk_fma_f32 v[34:35], v[110:111], v[154:155], v[34:35] op_sel:[0,1,0]
	v_pk_fma_f32 v[30:31], v[112:113], v[154:155], v[30:31] op_sel:[0,1,0]
	v_pk_fma_f32 v[24:25], v[114:115], v[154:155], v[24:25] op_sel:[0,1,0]
	v_pk_fma_f32 v[22:23], v[116:117], v[154:155], v[22:23] op_sel:[0,1,0]
	v_pk_fma_f32 v[18:19], v[118:119], v[154:155], v[18:19] op_sel:[0,1,0]
	s_waitcnt lgkmcnt(0)
	ds_read_b128 v[88:91], v187 offset:2432
	ds_read_b128 v[92:95], v187 offset:2448
	ds_read_b128 v[96:99], v187 offset:2464
	ds_read_b128 v[100:103], v187 offset:2480
	ds_read_b128 v[104:107], v187 offset:2496
	ds_read_b128 v[108:111], v187 offset:2512
	ds_read_b128 v[112:115], v187 offset:2528
	ds_read_b128 v[116:119], v187 offset:2544
	s_waitcnt vmcnt(24)
	v_pk_fma_f32 v[32:33], v[56:57], v[156:157], v[32:33] op_sel_hi:[1,0,1]
	v_pk_fma_f32 v[28:29], v[58:59], v[156:157], v[28:29] op_sel_hi:[1,0,1]
	v_pk_fma_f32 v[36:37], v[60:61], v[156:157], v[36:37] op_sel_hi:[1,0,1]
	v_pk_fma_f32 v[34:35], v[62:63], v[156:157], v[34:35] op_sel_hi:[1,0,1]
	v_pk_fma_f32 v[30:31], v[64:65], v[156:157], v[30:31] op_sel_hi:[1,0,1]
	v_pk_fma_f32 v[24:25], v[66:67], v[156:157], v[24:25] op_sel_hi:[1,0,1]
	v_pk_fma_f32 v[22:23], v[68:69], v[156:157], v[22:23] op_sel_hi:[1,0,1]
	v_pk_fma_f32 v[18:19], v[70:71], v[156:157], v[18:19] op_sel_hi:[1,0,1]
	v_pk_fma_f32 v[32:33], v[72:73], v[156:157], v[32:33] op_sel:[0,1,0]
	v_pk_fma_f32 v[28:29], v[74:75], v[156:157], v[28:29] op_sel:[0,1,0]
	v_pk_fma_f32 v[36:37], v[76:77], v[156:157], v[36:37] op_sel:[0,1,0]
	v_pk_fma_f32 v[34:35], v[78:79], v[156:157], v[34:35] op_sel:[0,1,0]
	v_pk_fma_f32 v[30:31], v[80:81], v[156:157], v[30:31] op_sel:[0,1,0]
	v_pk_fma_f32 v[24:25], v[82:83], v[156:157], v[24:25] op_sel:[0,1,0]
	v_pk_fma_f32 v[22:23], v[84:85], v[156:157], v[22:23] op_sel:[0,1,0]
	v_pk_fma_f32 v[18:19], v[86:87], v[156:157], v[18:19] op_sel:[0,1,0]
	s_waitcnt lgkmcnt(0)
;     ...
;             for (int cc = 0; cc < 2; ++cc) { const int col = F.tid + cc * 512; float acc[16];
; #pragma unroll
;                 for (int p = 0; p < 16; ++p) acc[p] = 0.f;
;                 for (int k = 0; k < 64; ++k) { const float w = w3[k * 1024 + col];
; #pragma unroll
;                     for (int p = 0; p < 16; ++p) acc[p] += f2[p * 64 + k] * w; }
	ds_read_b128 v[56:59], v187 offset:2560
	ds_read_b128 v[60:63], v187 offset:2576
	ds_read_b128 v[64:67], v187 offset:2592
	ds_read_b128 v[68:71], v187 offset:2608
	ds_read_b128 v[72:75], v187 offset:2624
	ds_read_b128 v[76:79], v187 offset:2640
	ds_read_b128 v[80:83], v187 offset:2656
	ds_read_b128 v[84:87], v187 offset:2672
	v_pk_fma_f32 v[32:33], v[88:89], v[158:159], v[32:33] op_sel_hi:[1,0,1]
	v_pk_fma_f32 v[28:29], v[90:91], v[158:159], v[28:29] op_sel_hi:[1,0,1]
	v_pk_fma_f32 v[36:37], v[92:93], v[158:159], v[36:37] op_sel_hi:[1,0,1]
	v_pk_fma_f32 v[34:35], v[94:95], v[158:159], v[34:35] op_sel_hi:[1,0,1]
	v_pk_fma_f32 v[30:31], v[96:97], v[158:159], v[30:31] op_sel_hi:[1,0,1]
	v_pk_fma_f32 v[24:25], v[98:99], v[158:159], v[24:25] op_sel_hi:[1,0,1]
	v_pk_fma_f32 v[22:23], v[100:101], v[158:159], v[22:23] op_sel_hi:[1,0,1]
	v_pk_fma_f32 v[18:19], v[102:103], v[158:159], v[18:19] op_sel_hi:[1,0,1]
	v_pk_fma_f32 v[32:33], v[104:105], v[158:159], v[32:33] op_sel:[0,1,0]
	v_pk_fma_f32 v[28:29], v[106:107], v[158:159], v[28:29] op_sel:[0,1,0]
	v_pk_fma_f32 v[36:37], v[108:109], v[158:159], v[36:37] op_sel:[0,1,0]
	v_pk_fma_f32 v[34:35], v[110:111], v[158:159], v[34:35] op_sel:[0,1,0]
	v_pk_fma_f32 v[30:31], v[112:113], v[158:159], v[30:31] op_sel:[0,1,0]
	v_pk_fma_f32 v[24:25], v[114:115], v[158:159], v[24:25] op_sel:[0,1,0]
	v_pk_fma_f32 v[22:23], v[116:117], v[158:159], v[22:23] op_sel:[0,1,0]
	v_pk_fma_f32 v[18:19], v[118:119], v[158:159], v[18:19] op_sel:[0,1,0]
	s_waitcnt lgkmcnt(0)
	ds_read_b128 v[88:91], v187 offset:2688
	ds_read_b128 v[92:95], v187 offset:2704
	ds_read_b128 v[96:99], v187 offset:2720
	ds_read_b128 v[100:103], v187 offset:2736
	ds_read_b128 v[104:107], v187 offset:2752
	ds_read_b128 v[108:111], v187 offset:2768
	ds_read_b128 v[112:115], v187 offset:2784
	ds_read_b128 v[116:119], v187 offset:2800
	s_waitcnt vmcnt(20)
	v_pk_fma_f32 v[32:33], v[56:57], v[160:161], v[32:33] op_sel_hi:[1,0,1]
	v_pk_fma_f32 v[28:29], v[58:59], v[160:161], v[28:29] op_sel_hi:[1,0,1]
	v_pk_fma_f32 v[36:37], v[60:61], v[160:161], v[36:37] op_sel_hi:[1,0,1]
	v_pk_fma_f32 v[34:35], v[62:63], v[160:161], v[34:35] op_sel_hi:[1,0,1]
	v_pk_fma_f32 v[30:31], v[64:65], v[160:161], v[30:31] op_sel_hi:[1,0,1]
	v_pk_fma_f32 v[24:25], v[66:67], v[160:161], v[24:25] op_sel_hi:[1,0,1]
	v_pk_fma_f32 v[22:23], v[68:69], v[160:161], v[22:23] op_sel_hi:[1,0,1]
	v_pk_fma_f32 v[18:19], v[70:71], v[160:161], v[18:19] op_sel_hi:[1,0,1]
	v_pk_fma_f32 v[32:33], v[72:73], v[160:161], v[32:33] op_sel:[0,1,0]
	v_pk_fma_f32 v[28:29], v[74:75], v[160:161], v[28:29] op_sel:[0,1,0]
	v_pk_fma_f32 v[36:37], v[76:77], v[160:161], v[36:37] op_sel:[0,1,0]
	v_pk_fma_f32 v[34:35], v[78:79], v[160:161], v[34:35] op_sel:[0,1,0]
	v_pk_fma_f32 v[30:31], v[80:81], v[160:161], v[30:31] op_sel:[0,1,0]
	v_pk_fma_f32 v[24:25], v[82:83], v[160:161], v[24:25] op_sel:[0,1,0]
	v_pk_fma_f32 v[22:23], v[84:85], v[160:161], v[22:23] op_sel:[0,1,0]
	v_pk_fma_f32 v[18:19], v[86:87], v[160:161], v[18:19] op_sel:[0,1,0]
	s_waitcnt lgkmcnt(0)
	ds_read_b128 v[56:59], v187 offset:2816
	ds_read_b128 v[60:63], v187 offset:2832
	ds_read_b128 v[64:67], v187 offset:2848
	ds_read_b128 v[68:71], v187 offset:2864
	ds_read_b128 v[72:75], v187 offset:2880
	ds_read_b128 v[76:79], v187 offset:2896
	ds_read_b128 v[80:83], v187 offset:2912
	ds_read_b128 v[84:87], v187 offset:2928
	v_pk_fma_f32 v[32:33], v[88:89], v[162:163], v[32:33] op_sel_hi:[1,0,1]
	v_pk_fma_f32 v[28:29], v[90:91], v[162:163], v[28:29] op_sel_hi:[1,0,1]
	v_pk_fma_f32 v[36:37], v[92:93], v[162:163], v[36:37] op_sel_hi:[1,0,1]
	v_pk_fma_f32 v[34:35], v[94:95], v[162:163], v[34:35] op_sel_hi:[1,0,1]
	v_pk_fma_f32 v[30:31], v[96:97], v[162:163], v[30:31] op_sel_hi:[1,0,1]
	v_pk_fma_f32 v[24:25], v[98:99], v[162:163], v[24:25] op_sel_hi:[1,0,1]
	v_pk_fma_f32 v[22:23], v[100:101], v[162:163], v[22:23] op_sel_hi:[1,0,1]
	v_pk_fma_f32 v[18:19], v[102:103], v[162:163], v[18:19] op_sel_hi:[1,0,1]
	v_pk_fma_f32 v[32:33], v[104:105], v[162:163], v[32:33] op_sel:[0,1,0]
	v_pk_fma_f32 v[28:29], v[106:107], v[162:163], v[28:29] op_sel:[0,1,0]
	v_pk_fma_f32 v[36:37], v[108:109], v[162:163], v[36:37] op_sel:[0,1,0]
	v_pk_fma_f32 v[34:35], v[110:111], v[162:163], v[34:35] op_sel:[0,1,0]
	v_pk_fma_f32 v[30:31], v[112:113], v[162:163], v[30:31] op_sel:[0,1,0]
	v_pk_fma_f32 v[24:25], v[114:115], v[162:163], v[24:25] op_sel:[0,1,0]
	v_pk_fma_f32 v[22:23], v[116:117], v[162:163], v[22:23] op_sel:[0,1,0]
	v_pk_fma_f32 v[18:19], v[118:119], v[162:163], v[18:19] op_sel:[0,1,0]
	s_waitcnt lgkmcnt(0)
	ds_read_b128 v[88:91], v187 offset:2944
	ds_read_b128 v[92:95], v187 offset:2960
	ds_read_b128 v[96:99], v187 offset:2976
	ds_read_b128 v[100:103], v187 offset:2992
	ds_read_b128 v[104:107], v187 offset:3008
	ds_read_b128 v[108:111], v187 offset:3024
	ds_read_b128 v[112:115], v187 offset:3040
	ds_read_b128 v[116:119], v187 offset:3056
	s_waitcnt vmcnt(16)
	v_pk_fma_f32 v[32:33], v[56:57], v[164:165], v[32:33] op_sel_hi:[1,0,1]
	v_pk_fma_f32 v[28:29], v[58:59], v[164:165], v[28:29] op_sel_hi:[1,0,1]
	v_pk_fma_f32 v[36:37], v[60:61], v[164:165], v[36:37] op_sel_hi:[1,0,1]
	v_pk_fma_f32 v[34:35], v[62:63], v[164:165], v[34:35] op_sel_hi:[1,0,1]
	v_pk_fma_f32 v[30:31], v[64:65], v[164:165], v[30:31] op_sel_hi:[1,0,1]
	v_pk_fma_f32 v[24:25], v[66:67], v[164:165], v[24:25] op_sel_hi:[1,0,1]
	v_pk_fma_f32 v[22:23], v[68:69], v[164:165], v[22:23] op_sel_hi:[1,0,1]
	v_pk_fma_f32 v[18:19], v[70:71], v[164:165], v[18:19] op_sel_hi:[1,0,1]
	v_pk_fma_f32 v[32:33], v[72:73], v[164:165], v[32:33] op_sel:[0,1,0]
	v_pk_fma_f32 v[28:29], v[74:75], v[164:165], v[28:29] op_sel:[0,1,0]
	v_pk_fma_f32 v[36:37], v[76:77], v[164:165], v[36:37] op_sel:[0,1,0]
	v_pk_fma_f32 v[34:35], v[78:79], v[164:165], v[34:35] op_sel:[0,1,0]
	v_pk_fma_f32 v[30:31], v[80:81], v[164:165], v[30:31] op_sel:[0,1,0]
	v_pk_fma_f32 v[24:25], v[82:83], v[164:165], v[24:25] op_sel:[0,1,0]
	v_pk_fma_f32 v[22:23], v[84:85], v[164:165], v[22:23] op_sel:[0,1,0]
	v_pk_fma_f32 v[18:19], v[86:87], v[164:165], v[18:19] op_sel:[0,1,0]
	s_waitcnt lgkmcnt(0)
;     ...
;             for (int cc = 0; cc < 2; ++cc) { const int col = F.tid + cc * 512; float acc[16];
; #pragma unroll
;                 for (int p = 0; p < 16; ++p) acc[p] = 0.f;
;                 for (int k = 0; k < 64; ++k) { const float w = w3[k * 1024 + col];
; #pragma unroll
;                     for (int p = 0; p < 16; ++p) acc[p] += f2[p * 64 + k] * w; }
	ds_read_b128 v[56:59], v187 offset:3072
	ds_read_b128 v[60:63], v187 offset:3088
	ds_read_b128 v[64:67], v187 offset:3104
	ds_read_b128 v[68:71], v187 offset:3120
	ds_read_b128 v[72:75], v187 offset:3136
	ds_read_b128 v[76:79], v187 offset:3152
	ds_read_b128 v[80:83], v187 offset:3168
	ds_read_b128 v[84:87], v187 offset:3184
	v_pk_fma_f32 v[32:33], v[88:89], v[166:167], v[32:33] op_sel_hi:[1,0,1]
	v_pk_fma_f32 v[28:29], v[90:91], v[166:167], v[28:29] op_sel_hi:[1,0,1]
	v_pk_fma_f32 v[36:37], v[92:93], v[166:167], v[36:37] op_sel_hi:[1,0,1]
	v_pk_fma_f32 v[34:35], v[94:95], v[166:167], v[34:35] op_sel_hi:[1,0,1]
	v_pk_fma_f32 v[30:31], v[96:97], v[166:167], v[30:31] op_sel_hi:[1,0,1]
	v_pk_fma_f32 v[24:25], v[98:99], v[166:167], v[24:25] op_sel_hi:[1,0,1]
	v_pk_fma_f32 v[22:23], v[100:101], v[166:167], v[22:23] op_sel_hi:[1,0,1]
	v_pk_fma_f32 v[18:19], v[102:103], v[166:167], v[18:19] op_sel_hi:[1,0,1]
	v_pk_fma_f32 v[32:33], v[104:105], v[166:167], v[32:33] op_sel:[0,1,0]
	v_pk_fma_f32 v[28:29], v[106:107], v[166:167], v[28:29] op_sel:[0,1,0]
	v_pk_fma_f32 v[36:37], v[108:109], v[166:167], v[36:37] op_sel:[0,1,0]
	v_pk_fma_f32 v[34:35], v[110:111], v[166:167], v[34:35] op_sel:[0,1,0]
	v_pk_fma_f32 v[30:31], v[112:113], v[166:167], v[30:31] op_sel:[0,1,0]
	v_pk_fma_f32 v[24:25], v[114:115], v[166:167], v[24:25] op_sel:[0,1,0]
	v_pk_fma_f32 v[22:23], v[116:117], v[166:167], v[22:23] op_sel:[0,1,0]
	v_pk_fma_f32 v[18:19], v[118:119], v[166:167], v[18:19] op_sel:[0,1,0]
	s_waitcnt lgkmcnt(0)
	ds_read_b128 v[88:91], v187 offset:3200
	ds_read_b128 v[92:95], v187 offset:3216
	ds_read_b128 v[96:99], v187 offset:3232
	ds_read_b128 v[100:103], v187 offset:3248
	ds_read_b128 v[104:107], v187 offset:3264
	ds_read_b128 v[108:111], v187 offset:3280
	ds_read_b128 v[112:115], v187 offset:3296
	ds_read_b128 v[116:119], v187 offset:3312
	s_waitcnt vmcnt(12)
	v_pk_fma_f32 v[32:33], v[56:57], v[168:169], v[32:33] op_sel_hi:[1,0,1]
	v_pk_fma_f32 v[28:29], v[58:59], v[168:169], v[28:29] op_sel_hi:[1,0,1]
	v_pk_fma_f32 v[36:37], v[60:61], v[168:169], v[36:37] op_sel_hi:[1,0,1]
	v_pk_fma_f32 v[34:35], v[62:63], v[168:169], v[34:35] op_sel_hi:[1,0,1]
	v_pk_fma_f32 v[30:31], v[64:65], v[168:169], v[30:31] op_sel_hi:[1,0,1]
	v_pk_fma_f32 v[24:25], v[66:67], v[168:169], v[24:25] op_sel_hi:[1,0,1]
	v_pk_fma_f32 v[22:23], v[68:69], v[168:169], v[22:23] op_sel_hi:[1,0,1]
	v_pk_fma_f32 v[18:19], v[70:71], v[168:169], v[18:19] op_sel_hi:[1,0,1]
	v_pk_fma_f32 v[32:33], v[72:73], v[168:169], v[32:33] op_sel:[0,1,0]
	v_pk_fma_f32 v[28:29], v[74:75], v[168:169], v[28:29] op_sel:[0,1,0]
	v_pk_fma_f32 v[36:37], v[76:77], v[168:169], v[36:37] op_sel:[0,1,0]
	v_pk_fma_f32 v[34:35], v[78:79], v[168:169], v[34:35] op_sel:[0,1,0]
	v_pk_fma_f32 v[30:31], v[80:81], v[168:169], v[30:31] op_sel:[0,1,0]
	v_pk_fma_f32 v[24:25], v[82:83], v[168:169], v[24:25] op_sel:[0,1,0]
	v_pk_fma_f32 v[22:23], v[84:85], v[168:169], v[22:23] op_sel:[0,1,0]
	v_pk_fma_f32 v[18:19], v[86:87], v[168:169], v[18:19] op_sel:[0,1,0]
	s_waitcnt lgkmcnt(0)
	ds_read_b128 v[56:59], v187 offset:3328
	ds_read_b128 v[60:63], v187 offset:3344
	ds_read_b128 v[64:67], v187 offset:3360
	ds_read_b128 v[68:71], v187 offset:3376
	ds_read_b128 v[72:75], v187 offset:3392
	ds_read_b128 v[76:79], v187 offset:3408
	ds_read_b128 v[80:83], v187 offset:3424
	ds_read_b128 v[84:87], v187 offset:3440
	v_pk_fma_f32 v[32:33], v[88:89], v[170:171], v[32:33] op_sel_hi:[1,0,1]
	v_pk_fma_f32 v[28:29], v[90:91], v[170:171], v[28:29] op_sel_hi:[1,0,1]
	v_pk_fma_f32 v[36:37], v[92:93], v[170:171], v[36:37] op_sel_hi:[1,0,1]
	v_pk_fma_f32 v[34:35], v[94:95], v[170:171], v[34:35] op_sel_hi:[1,0,1]
	v_pk_fma_f32 v[30:31], v[96:97], v[170:171], v[30:31] op_sel_hi:[1,0,1]
	v_pk_fma_f32 v[24:25], v[98:99], v[170:171], v[24:25] op_sel_hi:[1,0,1]
	v_pk_fma_f32 v[22:23], v[100:101], v[170:171], v[22:23] op_sel_hi:[1,0,1]
	v_pk_fma_f32 v[18:19], v[102:103], v[170:171], v[18:19] op_sel_hi:[1,0,1]
	v_pk_fma_f32 v[32:33], v[104:105], v[170:171], v[32:33] op_sel:[0,1,0]
	v_pk_fma_f32 v[28:29], v[106:107], v[170:171], v[28:29] op_sel:[0,1,0]
	v_pk_fma_f32 v[36:37], v[108:109], v[170:171], v[36:37] op_sel:[0,1,0]
	v_pk_fma_f32 v[34:35], v[110:111], v[170:171], v[34:35] op_sel:[0,1,0]
	v_pk_fma_f32 v[30:31], v[112:113], v[170:171], v[30:31] op_sel:[0,1,0]
	v_pk_fma_f32 v[24:25], v[114:115], v[170:171], v[24:25] op_sel:[0,1,0]
	v_pk_fma_f32 v[22:23], v[116:117], v[170:171], v[22:23] op_sel:[0,1,0]
	v_pk_fma_f32 v[18:19], v[118:119], v[170:171], v[18:19] op_sel:[0,1,0]
	s_waitcnt lgkmcnt(0)
	ds_read_b128 v[88:91], v187 offset:3456
	ds_read_b128 v[92:95], v187 offset:3472
	ds_read_b128 v[96:99], v187 offset:3488
	ds_read_b128 v[100:103], v187 offset:3504
	ds_read_b128 v[104:107], v187 offset:3520
	ds_read_b128 v[108:111], v187 offset:3536
	ds_read_b128 v[112:115], v187 offset:3552
	ds_read_b128 v[116:119], v187 offset:3568
	s_waitcnt vmcnt(8)
	v_pk_fma_f32 v[32:33], v[56:57], v[172:173], v[32:33] op_sel_hi:[1,0,1]
	v_pk_fma_f32 v[28:29], v[58:59], v[172:173], v[28:29] op_sel_hi:[1,0,1]
	v_pk_fma_f32 v[36:37], v[60:61], v[172:173], v[36:37] op_sel_hi:[1,0,1]
	v_pk_fma_f32 v[34:35], v[62:63], v[172:173], v[34:35] op_sel_hi:[1,0,1]
	v_pk_fma_f32 v[30:31], v[64:65], v[172:173], v[30:31] op_sel_hi:[1,0,1]
	v_pk_fma_f32 v[24:25], v[66:67], v[172:173], v[24:25] op_sel_hi:[1,0,1]
	v_pk_fma_f32 v[22:23], v[68:69], v[172:173], v[22:23] op_sel_hi:[1,0,1]
	v_pk_fma_f32 v[18:19], v[70:71], v[172:173], v[18:19] op_sel_hi:[1,0,1]
	v_pk_fma_f32 v[32:33], v[72:73], v[172:173], v[32:33] op_sel:[0,1,0]
	v_pk_fma_f32 v[28:29], v[74:75], v[172:173], v[28:29] op_sel:[0,1,0]
	v_pk_fma_f32 v[36:37], v[76:77], v[172:173], v[36:37] op_sel:[0,1,0]
	v_pk_fma_f32 v[34:35], v[78:79], v[172:173], v[34:35] op_sel:[0,1,0]
	v_pk_fma_f32 v[30:31], v[80:81], v[172:173], v[30:31] op_sel:[0,1,0]
	v_pk_fma_f32 v[24:25], v[82:83], v[172:173], v[24:25] op_sel:[0,1,0]
	v_pk_fma_f32 v[22:23], v[84:85], v[172:173], v[22:23] op_sel:[0,1,0]
	v_pk_fma_f32 v[18:19], v[86:87], v[172:173], v[18:19] op_sel:[0,1,0]
	s_waitcnt lgkmcnt(0)
;     ...
;             for (int cc = 0; cc < 2; ++cc) { const int col = F.tid + cc * 512; float acc[16];
; #pragma unroll
;                 for (int p = 0; p < 16; ++p) acc[p] = 0.f;
;                 for (int k = 0; k < 64; ++k) { const float w = w3[k * 1024 + col];
; #pragma unroll
;                     for (int p = 0; p < 16; ++p) acc[p] += f2[p * 64 + k] * w; }
	ds_read_b128 v[56:59], v187 offset:3584
	ds_read_b128 v[60:63], v187 offset:3600
	ds_read_b128 v[64:67], v187 offset:3616
	ds_read_b128 v[68:71], v187 offset:3632
	ds_read_b128 v[72:75], v187 offset:3648
	ds_read_b128 v[76:79], v187 offset:3664
	ds_read_b128 v[80:83], v187 offset:3680
	ds_read_b128 v[84:87], v187 offset:3696
	v_pk_fma_f32 v[32:33], v[88:89], v[174:175], v[32:33] op_sel_hi:[1,0,1]
	v_pk_fma_f32 v[28:29], v[90:91], v[174:175], v[28:29] op_sel_hi:[1,0,1]
	v_pk_fma_f32 v[36:37], v[92:93], v[174:175], v[36:37] op_sel_hi:[1,0,1]
	v_pk_fma_f32 v[34:35], v[94:95], v[174:175], v[34:35] op_sel_hi:[1,0,1]
	v_pk_fma_f32 v[30:31], v[96:97], v[174:175], v[30:31] op_sel_hi:[1,0,1]
	v_pk_fma_f32 v[24:25], v[98:99], v[174:175], v[24:25] op_sel_hi:[1,0,1]
	v_pk_fma_f32 v[22:23], v[100:101], v[174:175], v[22:23] op_sel_hi:[1,0,1]
	v_pk_fma_f32 v[18:19], v[102:103], v[174:175], v[18:19] op_sel_hi:[1,0,1]
	v_pk_fma_f32 v[32:33], v[104:105], v[174:175], v[32:33] op_sel:[0,1,0]
	v_pk_fma_f32 v[28:29], v[106:107], v[174:175], v[28:29] op_sel:[0,1,0]
	v_pk_fma_f32 v[36:37], v[108:109], v[174:175], v[36:37] op_sel:[0,1,0]
	v_pk_fma_f32 v[34:35], v[110:111], v[174:175], v[34:35] op_sel:[0,1,0]
	v_pk_fma_f32 v[30:31], v[112:113], v[174:175], v[30:31] op_sel:[0,1,0]
	v_pk_fma_f32 v[24:25], v[114:115], v[174:175], v[24:25] op_sel:[0,1,0]
	v_pk_fma_f32 v[22:23], v[116:117], v[174:175], v[22:23] op_sel:[0,1,0]
	v_pk_fma_f32 v[18:19], v[118:119], v[174:175], v[18:19] op_sel:[0,1,0]
	s_waitcnt lgkmcnt(0)
	ds_read_b128 v[88:91], v187 offset:3712
	ds_read_b128 v[92:95], v187 offset:3728
	ds_read_b128 v[96:99], v187 offset:3744
	ds_read_b128 v[100:103], v187 offset:3760
	ds_read_b128 v[104:107], v187 offset:3776
	ds_read_b128 v[108:111], v187 offset:3792
	ds_read_b128 v[112:115], v187 offset:3808
	ds_read_b128 v[116:119], v187 offset:3824
	s_waitcnt vmcnt(4)
	v_pk_fma_f32 v[32:33], v[56:57], v[176:177], v[32:33] op_sel_hi:[1,0,1]
	v_pk_fma_f32 v[28:29], v[58:59], v[176:177], v[28:29] op_sel_hi:[1,0,1]
	v_pk_fma_f32 v[36:37], v[60:61], v[176:177], v[36:37] op_sel_hi:[1,0,1]
	v_pk_fma_f32 v[34:35], v[62:63], v[176:177], v[34:35] op_sel_hi:[1,0,1]
	v_pk_fma_f32 v[30:31], v[64:65], v[176:177], v[30:31] op_sel_hi:[1,0,1]
	v_pk_fma_f32 v[24:25], v[66:67], v[176:177], v[24:25] op_sel_hi:[1,0,1]
	v_pk_fma_f32 v[22:23], v[68:69], v[176:177], v[22:23] op_sel_hi:[1,0,1]
	v_pk_fma_f32 v[18:19], v[70:71], v[176:177], v[18:19] op_sel_hi:[1,0,1]
	v_pk_fma_f32 v[32:33], v[72:73], v[176:177], v[32:33] op_sel:[0,1,0]
	v_pk_fma_f32 v[28:29], v[74:75], v[176:177], v[28:29] op_sel:[0,1,0]
	v_pk_fma_f32 v[36:37], v[76:77], v[176:177], v[36:37] op_sel:[0,1,0]
	v_pk_fma_f32 v[34:35], v[78:79], v[176:177], v[34:35] op_sel:[0,1,0]
	v_pk_fma_f32 v[30:31], v[80:81], v[176:177], v[30:31] op_sel:[0,1,0]
	v_pk_fma_f32 v[24:25], v[82:83], v[176:177], v[24:25] op_sel:[0,1,0]
	v_pk_fma_f32 v[22:23], v[84:85], v[176:177], v[22:23] op_sel:[0,1,0]
	v_pk_fma_f32 v[18:19], v[86:87], v[176:177], v[18:19] op_sel:[0,1,0]
	s_waitcnt lgkmcnt(0)
	ds_read_b128 v[56:59], v187 offset:3840
	ds_read_b128 v[60:63], v187 offset:3856
	ds_read_b128 v[64:67], v187 offset:3872
	ds_read_b128 v[68:71], v187 offset:3888
	ds_read_b128 v[72:75], v187 offset:3904
	ds_read_b128 v[76:79], v187 offset:3920
	ds_read_b128 v[80:83], v187 offset:3936
	ds_read_b128 v[84:87], v187 offset:3952
	v_pk_fma_f32 v[32:33], v[88:89], v[178:179], v[32:33] op_sel_hi:[1,0,1]
	v_pk_fma_f32 v[28:29], v[90:91], v[178:179], v[28:29] op_sel_hi:[1,0,1]
	v_pk_fma_f32 v[36:37], v[92:93], v[178:179], v[36:37] op_sel_hi:[1,0,1]
	v_pk_fma_f32 v[34:35], v[94:95], v[178:179], v[34:35] op_sel_hi:[1,0,1]
	v_pk_fma_f32 v[30:31], v[96:97], v[178:179], v[30:31] op_sel_hi:[1,0,1]
	v_pk_fma_f32 v[24:25], v[98:99], v[178:179], v[24:25] op_sel_hi:[1,0,1]
	v_pk_fma_f32 v[22:23], v[100:101], v[178:179], v[22:23] op_sel_hi:[1,0,1]
	v_pk_fma_f32 v[18:19], v[102:103], v[178:179], v[18:19] op_sel_hi:[1,0,1]
	v_pk_fma_f32 v[32:33], v[104:105], v[178:179], v[32:33] op_sel:[0,1,0]
	v_pk_fma_f32 v[28:29], v[106:107], v[178:179], v[28:29] op_sel:[0,1,0]
	v_pk_fma_f32 v[36:37], v[108:109], v[178:179], v[36:37] op_sel:[0,1,0]
	v_pk_fma_f32 v[34:35], v[110:111], v[178:179], v[34:35] op_sel:[0,1,0]
	v_pk_fma_f32 v[30:31], v[112:113], v[178:179], v[30:31] op_sel:[0,1,0]
	v_pk_fma_f32 v[24:25], v[114:115], v[178:179], v[24:25] op_sel:[0,1,0]
	v_pk_fma_f32 v[22:23], v[116:117], v[178:179], v[22:23] op_sel:[0,1,0]
	v_pk_fma_f32 v[18:19], v[118:119], v[178:179], v[18:19] op_sel:[0,1,0]
	s_waitcnt lgkmcnt(0)
	ds_read_b128 v[88:91], v187 offset:3968
	ds_read_b128 v[92:95], v187 offset:3984
	ds_read_b128 v[96:99], v187 offset:4000
	ds_read_b128 v[100:103], v187 offset:4016
	ds_read_b128 v[104:107], v187 offset:4032
	ds_read_b128 v[108:111], v187 offset:4048
	ds_read_b128 v[112:115], v187 offset:4064
	ds_read_b128 v[116:119], v187 offset:4080
	s_waitcnt vmcnt(0)
	v_pk_fma_f32 v[32:33], v[56:57], v[180:181], v[32:33] op_sel_hi:[1,0,1]
	v_pk_fma_f32 v[28:29], v[58:59], v[180:181], v[28:29] op_sel_hi:[1,0,1]
	v_pk_fma_f32 v[36:37], v[60:61], v[180:181], v[36:37] op_sel_hi:[1,0,1]
	v_pk_fma_f32 v[34:35], v[62:63], v[180:181], v[34:35] op_sel_hi:[1,0,1]
	v_pk_fma_f32 v[30:31], v[64:65], v[180:181], v[30:31] op_sel_hi:[1,0,1]
	v_pk_fma_f32 v[24:25], v[66:67], v[180:181], v[24:25] op_sel_hi:[1,0,1]
	v_pk_fma_f32 v[22:23], v[68:69], v[180:181], v[22:23] op_sel_hi:[1,0,1]
	v_pk_fma_f32 v[18:19], v[70:71], v[180:181], v[18:19] op_sel_hi:[1,0,1]
	v_pk_fma_f32 v[32:33], v[72:73], v[182:183], v[32:33] op_sel_hi:[1,0,1]
	v_pk_fma_f32 v[28:29], v[74:75], v[182:183], v[28:29] op_sel_hi:[1,0,1]
	v_pk_fma_f32 v[36:37], v[76:77], v[182:183], v[36:37] op_sel_hi:[1,0,1]
	v_pk_fma_f32 v[34:35], v[78:79], v[182:183], v[34:35] op_sel_hi:[1,0,1]
	v_pk_fma_f32 v[30:31], v[80:81], v[182:183], v[30:31] op_sel_hi:[1,0,1]
	v_pk_fma_f32 v[24:25], v[82:83], v[182:183], v[24:25] op_sel_hi:[1,0,1]
	v_pk_fma_f32 v[22:23], v[84:85], v[182:183], v[22:23] op_sel_hi:[1,0,1]
	v_pk_fma_f32 v[18:19], v[86:87], v[182:183], v[18:19] op_sel_hi:[1,0,1]
	s_waitcnt lgkmcnt(0)
;     ...
;                 for (int k = 0; k < 64; ++k) { const float w = w3[k * 1024 + col];
; #pragma unroll
;                     for (int p = 0; p < 16; ++p) acc[p] += f2[p * 64 + k] * w; }
;                 const int c = col & 255; const float delta = 3.0701134573253945f + (float)c * ((15.350567286626973f - 3.0701134573253945f) / 255.0f);
; #pragma unroll
;                 for (int p4 = 0; p4 < 4; ++p4) { f32x4 o;
; #pragma unroll
;                     for (int q = 0; q < 4; ++q) { const int n = n0 + p4 * 4 + q; const float tt = (float)n / (float)(L - 1); o[q] = acc[p4 * 4 + q] * __expf(-tt * delta); }
;                     *(f32x4*)(FT + (size_t)col * L + n0 + p4 * 4) = o; } }
	v_pk_fma_f32 v[32:33], v[88:89], v[182:183], v[32:33] op_sel:[0,1,0]
	v_pk_fma_f32 v[28:29], v[90:91], v[182:183], v[28:29] op_sel:[0,1,0]
	v_pk_fma_f32 v[36:37], v[92:93], v[182:183], v[36:37] op_sel:[0,1,0]
	v_pk_fma_f32 v[34:35], v[94:95], v[182:183], v[34:35] op_sel:[0,1,0]
	v_pk_fma_f32 v[30:31], v[96:97], v[182:183], v[30:31] op_sel:[0,1,0]
	v_pk_fma_f32 v[24:25], v[98:99], v[182:183], v[24:25] op_sel:[0,1,0]
	v_pk_fma_f32 v[22:23], v[100:101], v[182:183], v[22:23] op_sel:[0,1,0]
	v_pk_fma_f32 v[18:19], v[102:103], v[182:183], v[18:19] op_sel:[0,1,0]
	v_pk_fma_f32 v[32:33], v[104:105], v[184:185], v[32:33] op_sel_hi:[1,0,1]
	v_pk_fma_f32 v[28:29], v[106:107], v[184:185], v[28:29] op_sel_hi:[1,0,1]
	v_pk_fma_f32 v[36:37], v[108:109], v[184:185], v[36:37] op_sel_hi:[1,0,1]
	v_pk_fma_f32 v[34:35], v[110:111], v[184:185], v[34:35] op_sel_hi:[1,0,1]
	v_pk_fma_f32 v[30:31], v[112:113], v[184:185], v[30:31] op_sel_hi:[1,0,1]
	v_pk_fma_f32 v[24:25], v[114:115], v[184:185], v[24:25] op_sel_hi:[1,0,1]
	v_pk_fma_f32 v[22:23], v[116:117], v[184:185], v[22:23] op_sel_hi:[1,0,1]
	v_pk_fma_f32 v[18:19], v[118:119], v[184:185], v[18:19] op_sel_hi:[1,0,1]
	s_nop 0
	s_add_i32 s16, s16, -1
	s_ashr_i32 s27, s26, 31
	s_or_b32 s4, s26, 12
	s_and_b64 s[0:1], s[24:25], exec
	s_mov_b32 s0, 0xd800000
	s_cselect_b32 s0, s0, 0xe800000
	s_add_u32 s5, s28, s0
	v_cvt_f32_u32_e32 v46, s16
	s_addc_u32 s6, s29, 0
	v_cvt_f32_i32_e32 v26, s26
	s_and_b64 s[0:1], s[24:25], exec
	s_cselect_b32 s0, 12, 8
	s_lshl_b64 s[2:3], s[26:27], 2
	s_add_u32 s44, s5, s2
	s_addc_u32 s45, s6, s3
	v_div_scale_f32 v27, s[2:3], v46, v46, -v26
	v_rcp_f32_e32 v38, v27
	v_lshlrev_b64 v[20:21], s0, v[0:1]
	v_lshl_add_u64 v[40:41], v[20:21], 2, s[44:45]
	s_or_b32 s1, s26, 1
	v_fma_f32 v20, -v27, v38, 1.0
	v_fmac_f32_e32 v38, v20, v38
	v_div_scale_f32 v20, vcc, -v26, v46, -v26
	v_mul_f32_e32 v21, v20, v38
	v_fma_f32 v39, -v27, v21, v20
	v_fmac_f32_e32 v21, v39, v38
	v_fma_f32 v20, -v27, v21, v20
	v_cvt_f32_i32_e32 v27, s1
	v_div_fmas_f32 v20, v20, v38, v21
	v_div_fixup_f32 v20, v20, v46, -v26
	s_or_b32 s1, s26, 2
	v_div_scale_f32 v21, s[2:3], v46, v46, -v27
	v_rcp_f32_e32 v26, v21
	v_mul_f32_e32 v20, v53, v20
	v_mul_f32_e32 v20, 0x3fb8aa3b, v20
	v_exp_f32_e32 v20, v20
	v_fma_f32 v38, -v21, v26, 1.0
	v_fmac_f32_e32 v26, v38, v26
	v_div_scale_f32 v38, vcc, -v27, v46, -v27
	v_mul_f32_e32 v39, v38, v26
	v_fma_f32 v42, -v21, v39, v38
	v_fmac_f32_e32 v39, v42, v26
	v_fma_f32 v21, -v21, v39, v38
	v_cvt_f32_i32_e32 v38, s1
	v_div_fmas_f32 v21, v21, v26, v39
	v_div_fixup_f32 v21, v21, v46, -v27
	s_or_b32 s1, s26, 3
	v_div_scale_f32 v26, s[2:3], v46, v46, -v38
	v_rcp_f32_e32 v27, v26
	v_mul_f32_e32 v21, v53, v21
	v_mul_f32_e32 v21, 0x3fb8aa3b, v21
	v_exp_f32_e32 v21, v21
	v_fma_f32 v39, -v26, v27, 1.0
	v_fmac_f32_e32 v27, v39, v27
	v_div_scale_f32 v39, vcc, -v38, v46, -v38
	v_mul_f32_e32 v42, v39, v27
	v_fma_f32 v43, -v26, v42, v39
	v_fmac_f32_e32 v42, v43, v27
	v_fma_f32 v26, -v26, v42, v39
	v_cvt_f32_i32_e32 v39, s1
	v_div_fmas_f32 v26, v26, v27, v42
	v_div_fixup_f32 v26, v26, v46, -v38
	s_or_b32 s1, s26, 4
	v_div_scale_f32 v27, s[2:3], v46, v46, -v39
	v_rcp_f32_e32 v38, v27
	v_mul_f32_e32 v26, v53, v26
	v_mul_f32_e32 v26, 0x3fb8aa3b, v26
	v_exp_f32_e32 v26, v26
	v_fma_f32 v42, -v27, v38, 1.0
	v_fmac_f32_e32 v38, v42, v38
	v_div_scale_f32 v42, vcc, -v39, v46, -v39
	v_mul_f32_e32 v43, v42, v38
	v_fma_f32 v44, -v27, v43, v42
	v_fmac_f32_e32 v43, v44, v38
	v_fma_f32 v27, -v27, v43, v42
	v_div_fmas_f32 v27, v27, v38, v43
	v_cvt_f32_i32_e32 v38, s1
	v_div_fixup_f32 v27, v27, v46, -v39
	v_mul_f32_e32 v27, v53, v27
	v_mul_f32_e32 v27, 0x3fb8aa3b, v27
	v_div_scale_f32 v39, s[2:3], v46, v46, -v38
	v_exp_f32_e32 v27, v27
	v_rcp_f32_e32 v48, v39
	v_pk_mul_f32 v[42:43], v[20:21], v[32:33]
	s_or_b32 s1, s26, 5
	v_pk_mul_f32 v[44:45], v[26:27], v[28:29]
	v_fma_f32 v28, -v39, v48, 1.0
	v_fmac_f32_e32 v48, v28, v48
	v_div_scale_f32 v28, vcc, -v38, v46, -v38
	v_mul_f32_e32 v29, v28, v48
	v_fma_f32 v32, -v39, v29, v28
	v_fmac_f32_e32 v29, v32, v48
	v_cvt_f32_i32_e32 v32, s1
	v_fma_f32 v28, -v39, v29, v28
	v_div_fmas_f32 v28, v28, v48, v29
	v_div_fixup_f32 v28, v28, v46, -v38
	v_div_scale_f32 v29, s[2:3], v46, v46, -v32
	v_rcp_f32_e32 v33, v29
	global_store_dwordx4 v[40:41], v[42:45], off
	s_or_b32 s1, s26, 6
	v_mul_f32_e32 v28, v53, v28
	v_fma_f32 v38, -v29, v33, 1.0
	v_fmac_f32_e32 v33, v38, v33
	v_div_scale_f32 v38, vcc, -v32, v46, -v32
	v_mul_f32_e32 v39, v38, v33
	v_fma_f32 v42, -v29, v39, v38
	v_fmac_f32_e32 v39, v42, v33
	v_fma_f32 v29, -v29, v39, v38
	v_cvt_f32_i32_e32 v38, s1
	v_div_fmas_f32 v29, v29, v33, v39
	v_div_fixup_f32 v29, v29, v46, -v32
	s_or_b32 s1, s26, 7
	v_div_scale_f32 v32, s[2:3], v46, v46, -v38
	v_rcp_f32_e32 v33, v32
	v_mul_f32_e32 v29, v53, v29
	v_mul_f32_e32 v28, 0x3fb8aa3b, v28
	v_mul_f32_e32 v29, 0x3fb8aa3b, v29
	v_fma_f32 v39, -v32, v33, 1.0
	v_fmac_f32_e32 v33, v39, v33
	v_div_scale_f32 v39, vcc, -v38, v46, -v38
	v_mul_f32_e32 v42, v39, v33
	v_fma_f32 v43, -v32, v42, v39
	v_fmac_f32_e32 v42, v43, v33
	v_fma_f32 v32, -v32, v42, v39
	v_cvt_f32_i32_e32 v39, s1
	v_div_fmas_f32 v32, v32, v33, v42
	v_div_fixup_f32 v32, v32, v46, -v38
	s_or_b32 s1, s26, 8
	v_div_scale_f32 v33, s[2:3], v46, v46, -v39
	v_rcp_f32_e32 v38, v33
	v_mul_f32_e32 v32, v53, v32
	v_mul_f32_e32 v32, 0x3fb8aa3b, v32
	v_exp_f32_e32 v32, v32
	v_fma_f32 v42, -v33, v38, 1.0
	v_fmac_f32_e32 v38, v42, v38
	v_div_scale_f32 v42, vcc, -v39, v46, -v39
	v_mul_f32_e32 v43, v42, v38
	v_fma_f32 v44, -v33, v43, v42
	v_fmac_f32_e32 v43, v44, v38
	v_fma_f32 v33, -v33, v43, v42
	v_cvt_f32_i32_e32 v42, s1
	v_div_fmas_f32 v33, v33, v38, v43
;     ...
;             for (int cc = 0; cc < 2; ++cc) { const int col = F.tid + cc * 512; float acc[16];
; #pragma unroll
;                 for (int p = 0; p < 16; ++p) acc[p] = 0.f;
;                 for (int k = 0; k < 64; ++k) { const float w = w3[k * 1024 + col];
;     ...
;                 const int c = col & 255; const float delta = 3.0701134573253945f + (float)c * ((15.350567286626973f - 3.0701134573253945f) / 255.0f);
; #pragma unroll
;                 for (int p4 = 0; p4 < 4; ++p4) { f32x4 o;
; #pragma unroll
;                     for (int q = 0; q < 4; ++q) { const int n = n0 + p4 * 4 + q; const float tt = (float)n / (float)(L - 1); o[q] = acc[p4 * 4 + q] * __expf(-tt * delta); }
;                     *(f32x4*)(FT + (size_t)col * L + n0 + p4 * 4) = o; } }
	v_div_fixup_f32 v33, v33, v46, -v39
	v_mul_f32_e32 v33, v53, v33
	v_mul_f32_e32 v33, 0x3fb8aa3b, v33
	v_div_scale_f32 v43, s[2:3], v46, v46, -v42
	v_exp_f32_e32 v33, v33
	v_rcp_f32_e32 v44, v43
	v_exp_f32_e32 v28, v28
	v_exp_f32_e32 v29, v29
	v_pk_mul_f32 v[38:39], v[32:33], v[34:35]
	v_fma_f32 v34, -v43, v44, 1.0
	v_fmac_f32_e32 v44, v34, v44
	v_div_scale_f32 v34, vcc, -v42, v46, -v42
	v_pk_mul_f32 v[36:37], v[28:29], v[36:37]
	v_mul_f32_e32 v35, v34, v44
	global_store_dwordx4 v[40:41], v[36:39], off offset:16
	s_or_b32 s1, s26, 9
	v_cvt_f32_i32_e32 v47, s4
	v_fma_f32 v36, -v43, v35, v34
	v_fmac_f32_e32 v35, v36, v44
	v_cvt_f32_i32_e32 v36, s1
	v_fma_f32 v34, -v43, v35, v34
	v_div_fmas_f32 v34, v34, v44, v35
	v_div_fixup_f32 v34, v34, v46, -v42
	v_div_scale_f32 v35, s[2:3], v46, v46, -v36
	v_rcp_f32_e32 v37, v35
	s_or_b32 s1, s26, 10
	v_mul_f32_e32 v34, v53, v34
	v_mul_f32_e32 v34, 0x3fb8aa3b, v34
	v_fma_f32 v38, -v35, v37, 1.0
	v_fmac_f32_e32 v37, v38, v37
	v_div_scale_f32 v38, vcc, -v36, v46, -v36
	v_mul_f32_e32 v39, v38, v37
	v_fma_f32 v42, -v35, v39, v38
	v_fmac_f32_e32 v39, v42, v37
	v_fma_f32 v35, -v35, v39, v38
	v_cvt_f32_i32_e32 v38, s1
	v_div_fmas_f32 v35, v35, v37, v39
	v_div_fixup_f32 v35, v35, v46, -v36
	s_or_b32 s1, s26, 11
	v_div_scale_f32 v36, s[2:3], v46, v46, -v38
	v_rcp_f32_e32 v37, v36
	v_mul_f32_e32 v35, v53, v35
	v_mul_f32_e32 v35, 0x3fb8aa3b, v35
	v_exp_f32_e32 v34, v34
	v_fma_f32 v39, -v36, v37, 1.0
	v_fmac_f32_e32 v37, v39, v37
	v_div_scale_f32 v39, vcc, -v38, v46, -v38
	v_mul_f32_e32 v42, v39, v37
	v_fma_f32 v43, -v36, v42, v39
	v_fmac_f32_e32 v42, v43, v37
	v_fma_f32 v36, -v36, v42, v39
	v_cvt_f32_i32_e32 v39, s1
	v_div_fmas_f32 v36, v36, v37, v42
	v_div_fixup_f32 v36, v36, v46, -v38
	v_exp_f32_e32 v35, v35
	v_div_scale_f32 v37, s[2:3], v46, v46, -v39
	v_rcp_f32_e32 v38, v37
	s_or_b32 s1, s26, 13
	v_mul_f32_e32 v36, v53, v36
	v_mul_f32_e32 v36, 0x3fb8aa3b, v36
	v_fma_f32 v42, -v37, v38, 1.0
	v_fmac_f32_e32 v38, v42, v38
	v_div_scale_f32 v42, vcc, -v39, v46, -v39
	v_mul_f32_e32 v43, v42, v38
	v_fma_f32 v44, -v37, v43, v42
	v_fmac_f32_e32 v43, v44, v38
	v_fma_f32 v37, -v37, v43, v42
	v_div_fmas_f32 v37, v37, v38, v43
	v_div_scale_f32 v38, s[2:3], v46, v46, -v47
	v_div_fixup_f32 v37, v37, v46, -v39
	v_rcp_f32_e32 v39, v38
	v_pk_mul_f32 v[42:43], v[34:35], v[30:31]
	v_mul_f32_e32 v37, v53, v37
	v_mul_f32_e32 v37, 0x3fb8aa3b, v37
	v_fma_f32 v30, -v38, v39, 1.0
	v_fmac_f32_e32 v39, v30, v39
	v_div_scale_f32 v30, vcc, -v47, v46, -v47
	v_mul_f32_e32 v31, v30, v39
	v_fma_f32 v44, -v38, v31, v30
	v_fmac_f32_e32 v31, v44, v39
	v_fma_f32 v30, -v38, v31, v30
	v_cvt_f32_i32_e32 v38, s1
	v_div_fmas_f32 v30, v30, v39, v31
	v_div_fixup_f32 v30, v30, v46, -v47
	s_or_b32 s1, s26, 14
	v_div_scale_f32 v31, s[2:3], v46, v46, -v38
	v_rcp_f32_e32 v39, v31
	v_mul_f32_e32 v30, v53, v30
	v_mul_f32_e32 v30, 0x3fb8aa3b, v30
	v_exp_f32_e32 v36, v36
	v_fma_f32 v44, -v31, v39, 1.0
	v_fmac_f32_e32 v39, v44, v39
	v_div_scale_f32 v44, vcc, -v38, v46, -v38
	v_mul_f32_e32 v45, v44, v39
	v_fma_f32 v47, -v31, v45, v44
	v_fmac_f32_e32 v45, v47, v39
	v_fma_f32 v31, -v31, v45, v44
	v_cvt_f32_i32_e32 v44, s1
	v_div_fmas_f32 v31, v31, v39, v45
	v_div_fixup_f32 v31, v31, v46, -v38
	s_or_b32 s1, s26, 15
	v_div_scale_f32 v38, s[2:3], v46, v46, -v44
	v_rcp_f32_e32 v39, v38
	v_mul_f32_e32 v31, v53, v31
	v_mul_f32_e32 v31, 0x3fb8aa3b, v31
	v_exp_f32_e32 v37, v37
	v_fma_f32 v45, -v38, v39, 1.0
	v_fmac_f32_e32 v39, v45, v39
	v_div_scale_f32 v45, vcc, -v44, v46, -v44
	v_mul_f32_e32 v47, v45, v39
	v_fma_f32 v48, -v38, v47, v45
	v_fmac_f32_e32 v47, v48, v39
	v_fma_f32 v38, -v38, v47, v45
	v_cvt_f32_i32_e32 v45, s1
	v_div_fmas_f32 v38, v38, v39, v47
	v_div_fixup_f32 v38, v38, v46, -v44
	v_mul_f32_e32 v38, v53, v38
	v_div_scale_f32 v39, s[2:3], v46, v46, -v45
	v_rcp_f32_e32 v44, v39
	v_mul_f32_e32 v38, 0x3fb8aa3b, v38
	v_exp_f32_e32 v30, v30
	v_exp_f32_e32 v31, v31
	v_fma_f32 v47, -v39, v44, 1.0
	v_fmac_f32_e32 v44, v47, v44
	v_div_scale_f32 v47, vcc, -v45, v46, -v45
	v_mul_f32_e32 v48, v47, v44
	v_fma_f32 v49, -v39, v48, v47
	v_fmac_f32_e32 v48, v49, v44
	v_fma_f32 v39, -v39, v48, v47
	v_div_fmas_f32 v39, v39, v44, v48
	v_div_fixup_f32 v39, v39, v46, -v45
	v_mul_f32_e32 v39, v53, v39
	v_mul_f32_e32 v39, 0x3fb8aa3b, v39
	v_exp_f32_e32 v38, v38
	v_exp_f32_e32 v39, v39
	v_pk_mul_f32 v[44:45], v[36:37], v[24:25]
	v_pk_mul_f32 v[22:23], v[30:31], v[22:23]
	global_store_dwordx4 v[40:41], v[42:45], off offset:32
	v_pk_mul_f32 v[24:25], v[38:39], v[18:19]
	v_mov_b32_e32 v18, 0
	global_store_dwordx4 v[40:41], v[22:25], off offset:48
	s_add_i32 s1, 0, 0x2000
	s_mov_b64 s[26:27], 0
	v_mov_b32_e32 v19, v18
	v_mov_b32_e32 v48, v18
	v_mov_b32_e32 v49, v18
	v_mov_b32_e32 v46, v18
	v_mov_b32_e32 v47, v18
	v_mov_b32_e32 v44, v18
	v_mov_b32_e32 v45, v18
	v_mov_b32_e32 v42, v18
	v_mov_b32_e32 v43, v18
	v_mov_b32_e32 v40, v18
	v_mov_b32_e32 v41, v18
	v_mov_b32_e32 v24, v18
	v_mov_b32_e32 v25, v18
	v_mov_b32_e32 v22, v18
	v_mov_b32_e32 v23, v18
	s_movk_i32 s3, 0x3000
	s_movk_i32 s4, 0x1000
	v_lshlrev_b32_e32 v186, 2, v0
	s_add_u32 s6, s20, 0x1000
	s_addc_u32 s7, s21, 0
	global_load_dword v120, v186, s[6:7] offset:-2048
	global_load_dword v121, v186, s[6:7] offset:2048
	s_add_u32 s6, s6, 0x2000
	s_addc_u32 s7, s7, 0
	global_load_dword v122, v186, s[6:7] offset:-2048
	global_load_dword v123, v186, s[6:7] offset:2048
	s_add_u32 s6, s6, 0x2000
	s_addc_u32 s7, s7, 0
	global_load_dword v124, v186, s[6:7] offset:-2048
	global_load_dword v125, v186, s[6:7] offset:2048
	s_add_u32 s6, s6, 0x2000
	s_addc_u32 s7, s7, 0
	global_load_dword v126, v186, s[6:7] offset:-2048
;     ...
;             for (int cc = 0; cc < 2; ++cc) { const int col = F.tid + cc * 512; float acc[16];
; #pragma unroll
;                 for (int p = 0; p < 16; ++p) acc[p] = 0.f;
;                 for (int k = 0; k < 64; ++k) { const float w = w3[k * 1024 + col];
; #pragma unroll
;                     for (int p = 0; p < 16; ++p) acc[p] += f2[p * 64 + k] * w; }
	global_load_dword v127, v186, s[6:7] offset:2048
	s_add_u32 s6, s6, 0x2000
	s_addc_u32 s7, s7, 0
	global_load_dword v128, v186, s[6:7] offset:-2048
	global_load_dword v129, v186, s[6:7] offset:2048
	s_add_u32 s6, s6, 0x2000
	s_addc_u32 s7, s7, 0
	global_load_dword v130, v186, s[6:7] offset:-2048
	global_load_dword v131, v186, s[6:7] offset:2048
	s_add_u32 s6, s6, 0x2000
	s_addc_u32 s7, s7, 0
	global_load_dword v132, v186, s[6:7] offset:-2048
	global_load_dword v133, v186, s[6:7] offset:2048
	s_add_u32 s6, s6, 0x2000
	s_addc_u32 s7, s7, 0
	global_load_dword v134, v186, s[6:7] offset:-2048
	global_load_dword v135, v186, s[6:7] offset:2048
	s_add_u32 s6, s6, 0x2000
	s_addc_u32 s7, s7, 0
	global_load_dword v136, v186, s[6:7] offset:-2048
	global_load_dword v137, v186, s[6:7] offset:2048
	s_add_u32 s6, s6, 0x2000
	s_addc_u32 s7, s7, 0
	global_load_dword v138, v186, s[6:7] offset:-2048
	global_load_dword v139, v186, s[6:7] offset:2048
	s_add_u32 s6, s6, 0x2000
	s_addc_u32 s7, s7, 0
	global_load_dword v140, v186, s[6:7] offset:-2048
	global_load_dword v141, v186, s[6:7] offset:2048
	s_add_u32 s6, s6, 0x2000
	s_addc_u32 s7, s7, 0
	global_load_dword v142, v186, s[6:7] offset:-2048
	global_load_dword v143, v186, s[6:7] offset:2048
	s_add_u32 s6, s6, 0x2000
	s_addc_u32 s7, s7, 0
	global_load_dword v144, v186, s[6:7] offset:-2048
	global_load_dword v145, v186, s[6:7] offset:2048
	s_add_u32 s6, s6, 0x2000
	s_addc_u32 s7, s7, 0
	global_load_dword v146, v186, s[6:7] offset:-2048
	global_load_dword v147, v186, s[6:7] offset:2048
	s_add_u32 s6, s6, 0x2000
	s_addc_u32 s7, s7, 0
	global_load_dword v148, v186, s[6:7] offset:-2048
	global_load_dword v149, v186, s[6:7] offset:2048
	s_add_u32 s6, s6, 0x2000
	s_addc_u32 s7, s7, 0
	global_load_dword v150, v186, s[6:7] offset:-2048
	global_load_dword v151, v186, s[6:7] offset:2048
	s_add_u32 s6, s6, 0x2000
	s_addc_u32 s7, s7, 0
	global_load_dword v152, v186, s[6:7] offset:-2048
	global_load_dword v153, v186, s[6:7] offset:2048
	s_add_u32 s6, s6, 0x2000
	s_addc_u32 s7, s7, 0
	global_load_dword v154, v186, s[6:7] offset:-2048
	global_load_dword v155, v186, s[6:7] offset:2048
	s_add_u32 s6, s6, 0x2000
	s_addc_u32 s7, s7, 0
	global_load_dword v156, v186, s[6:7] offset:-2048
	global_load_dword v157, v186, s[6:7] offset:2048
	s_add_u32 s6, s6, 0x2000
	s_addc_u32 s7, s7, 0
	global_load_dword v158, v186, s[6:7] offset:-2048
	global_load_dword v159, v186, s[6:7] offset:2048
	s_add_u32 s6, s6, 0x2000
	s_addc_u32 s7, s7, 0
	global_load_dword v160, v186, s[6:7] offset:-2048
	global_load_dword v161, v186, s[6:7] offset:2048
	s_add_u32 s6, s6, 0x2000
	s_addc_u32 s7, s7, 0
	global_load_dword v162, v186, s[6:7] offset:-2048
	global_load_dword v163, v186, s[6:7] offset:2048
	s_add_u32 s6, s6, 0x2000
	s_addc_u32 s7, s7, 0
	global_load_dword v164, v186, s[6:7] offset:-2048
	global_load_dword v165, v186, s[6:7] offset:2048
	s_add_u32 s6, s6, 0x2000
	s_addc_u32 s7, s7, 0
	global_load_dword v166, v186, s[6:7] offset:-2048
	global_load_dword v167, v186, s[6:7] offset:2048
	s_add_u32 s6, s6, 0x2000
	s_addc_u32 s7, s7, 0
	v_mov_b32_e32 v187, 0x2000
	ds_read_b128 v[56:59], v187
	ds_read_b128 v[60:63], v187 offset:16
	ds_read_b128 v[64:67], v187 offset:32
	ds_read_b128 v[68:71], v187 offset:48
	ds_read_b128 v[72:75], v187 offset:64
	ds_read_b128 v[76:79], v187 offset:80
	ds_read_b128 v[80:83], v187 offset:96
	ds_read_b128 v[84:87], v187 offset:112
	s_waitcnt lgkmcnt(0)
	ds_read_b128 v[88:91], v187 offset:128
	ds_read_b128 v[92:95], v187 offset:144
	ds_read_b128 v[96:99], v187 offset:160
	ds_read_b128 v[100:103], v187 offset:176
	ds_read_b128 v[104:107], v187 offset:192
	ds_read_b128 v[108:111], v187 offset:208
	ds_read_b128 v[112:115], v187 offset:224
	ds_read_b128 v[116:119], v187 offset:240
	s_waitcnt vmcnt(44)
	v_pk_fma_f32 v[48:49], v[56:57], v[120:121], v[48:49] op_sel_hi:[1,0,1]
	v_pk_fma_f32 v[46:47], v[58:59], v[120:121], v[46:47] op_sel_hi:[1,0,1]
	v_pk_fma_f32 v[44:45], v[60:61], v[120:121], v[44:45] op_sel_hi:[1,0,1]
	v_pk_fma_f32 v[42:43], v[62:63], v[120:121], v[42:43] op_sel_hi:[1,0,1]
	v_pk_fma_f32 v[40:41], v[64:65], v[120:121], v[40:41] op_sel_hi:[1,0,1]
	v_pk_fma_f32 v[24:25], v[66:67], v[120:121], v[24:25] op_sel_hi:[1,0,1]
	v_pk_fma_f32 v[22:23], v[68:69], v[120:121], v[22:23] op_sel_hi:[1,0,1]
	v_pk_fma_f32 v[18:19], v[70:71], v[120:121], v[18:19] op_sel_hi:[1,0,1]
	v_pk_fma_f32 v[48:49], v[72:73], v[120:121], v[48:49] op_sel:[0,1,0]
	v_pk_fma_f32 v[46:47], v[74:75], v[120:121], v[46:47] op_sel:[0,1,0]
	v_pk_fma_f32 v[44:45], v[76:77], v[120:121], v[44:45] op_sel:[0,1,0]
	v_pk_fma_f32 v[42:43], v[78:79], v[120:121], v[42:43] op_sel:[0,1,0]
	v_pk_fma_f32 v[40:41], v[80:81], v[120:121], v[40:41] op_sel:[0,1,0]
	v_pk_fma_f32 v[24:25], v[82:83], v[120:121], v[24:25] op_sel:[0,1,0]
	v_pk_fma_f32 v[22:23], v[84:85], v[120:121], v[22:23] op_sel:[0,1,0]
	v_pk_fma_f32 v[18:19], v[86:87], v[120:121], v[18:19] op_sel:[0,1,0]
	s_waitcnt lgkmcnt(0)
;     ...
;             for (int cc = 0; cc < 2; ++cc) { const int col = F.tid + cc * 512; float acc[16];
; #pragma unroll
;                 for (int p = 0; p < 16; ++p) acc[p] = 0.f;
;                 for (int k = 0; k < 64; ++k) { const float w = w3[k * 1024 + col];
; #pragma unroll
;                     for (int p = 0; p < 16; ++p) acc[p] += f2[p * 64 + k] * w; }
	ds_read_b128 v[56:59], v187 offset:256
	ds_read_b128 v[60:63], v187 offset:272
	ds_read_b128 v[64:67], v187 offset:288
	ds_read_b128 v[68:71], v187 offset:304
	ds_read_b128 v[72:75], v187 offset:320
	ds_read_b128 v[76:79], v187 offset:336
	ds_read_b128 v[80:83], v187 offset:352
	ds_read_b128 v[84:87], v187 offset:368
	v_pk_fma_f32 v[48:49], v[88:89], v[122:123], v[48:49] op_sel_hi:[1,0,1]
	v_pk_fma_f32 v[46:47], v[90:91], v[122:123], v[46:47] op_sel_hi:[1,0,1]
	v_pk_fma_f32 v[44:45], v[92:93], v[122:123], v[44:45] op_sel_hi:[1,0,1]
	v_pk_fma_f32 v[42:43], v[94:95], v[122:123], v[42:43] op_sel_hi:[1,0,1]
	v_pk_fma_f32 v[40:41], v[96:97], v[122:123], v[40:41] op_sel_hi:[1,0,1]
	v_pk_fma_f32 v[24:25], v[98:99], v[122:123], v[24:25] op_sel_hi:[1,0,1]
	v_pk_fma_f32 v[22:23], v[100:101], v[122:123], v[22:23] op_sel_hi:[1,0,1]
	v_pk_fma_f32 v[18:19], v[102:103], v[122:123], v[18:19] op_sel_hi:[1,0,1]
	v_pk_fma_f32 v[48:49], v[104:105], v[122:123], v[48:49] op_sel:[0,1,0]
	v_pk_fma_f32 v[46:47], v[106:107], v[122:123], v[46:47] op_sel:[0,1,0]
	v_pk_fma_f32 v[44:45], v[108:109], v[122:123], v[44:45] op_sel:[0,1,0]
	v_pk_fma_f32 v[42:43], v[110:111], v[122:123], v[42:43] op_sel:[0,1,0]
	v_pk_fma_f32 v[40:41], v[112:113], v[122:123], v[40:41] op_sel:[0,1,0]
	v_pk_fma_f32 v[24:25], v[114:115], v[122:123], v[24:25] op_sel:[0,1,0]
	v_pk_fma_f32 v[22:23], v[116:117], v[122:123], v[22:23] op_sel:[0,1,0]
	v_pk_fma_f32 v[18:19], v[118:119], v[122:123], v[18:19] op_sel:[0,1,0]
	s_waitcnt lgkmcnt(0)
	ds_read_b128 v[88:91], v187 offset:384
	ds_read_b128 v[92:95], v187 offset:400
	ds_read_b128 v[96:99], v187 offset:416
	ds_read_b128 v[100:103], v187 offset:432
	ds_read_b128 v[104:107], v187 offset:448
	ds_read_b128 v[108:111], v187 offset:464
	ds_read_b128 v[112:115], v187 offset:480
	ds_read_b128 v[116:119], v187 offset:496
	s_waitcnt vmcnt(40)
	v_pk_fma_f32 v[48:49], v[56:57], v[124:125], v[48:49] op_sel_hi:[1,0,1]
	v_pk_fma_f32 v[46:47], v[58:59], v[124:125], v[46:47] op_sel_hi:[1,0,1]
	v_pk_fma_f32 v[44:45], v[60:61], v[124:125], v[44:45] op_sel_hi:[1,0,1]
	v_pk_fma_f32 v[42:43], v[62:63], v[124:125], v[42:43] op_sel_hi:[1,0,1]
	v_pk_fma_f32 v[40:41], v[64:65], v[124:125], v[40:41] op_sel_hi:[1,0,1]
	v_pk_fma_f32 v[24:25], v[66:67], v[124:125], v[24:25] op_sel_hi:[1,0,1]
	v_pk_fma_f32 v[22:23], v[68:69], v[124:125], v[22:23] op_sel_hi:[1,0,1]
	v_pk_fma_f32 v[18:19], v[70:71], v[124:125], v[18:19] op_sel_hi:[1,0,1]
	v_pk_fma_f32 v[48:49], v[72:73], v[124:125], v[48:49] op_sel:[0,1,0]
	v_pk_fma_f32 v[46:47], v[74:75], v[124:125], v[46:47] op_sel:[0,1,0]
	v_pk_fma_f32 v[44:45], v[76:77], v[124:125], v[44:45] op_sel:[0,1,0]
	v_pk_fma_f32 v[42:43], v[78:79], v[124:125], v[42:43] op_sel:[0,1,0]
	v_pk_fma_f32 v[40:41], v[80:81], v[124:125], v[40:41] op_sel:[0,1,0]
	v_pk_fma_f32 v[24:25], v[82:83], v[124:125], v[24:25] op_sel:[0,1,0]
	v_pk_fma_f32 v[22:23], v[84:85], v[124:125], v[22:23] op_sel:[0,1,0]
	v_pk_fma_f32 v[18:19], v[86:87], v[124:125], v[18:19] op_sel:[0,1,0]
	s_waitcnt lgkmcnt(0)
	ds_read_b128 v[56:59], v187 offset:512
	ds_read_b128 v[60:63], v187 offset:528
	ds_read_b128 v[64:67], v187 offset:544
	ds_read_b128 v[68:71], v187 offset:560
	ds_read_b128 v[72:75], v187 offset:576
	ds_read_b128 v[76:79], v187 offset:592
	ds_read_b128 v[80:83], v187 offset:608
	ds_read_b128 v[84:87], v187 offset:624
	v_pk_fma_f32 v[48:49], v[88:89], v[126:127], v[48:49] op_sel_hi:[1,0,1]
	v_pk_fma_f32 v[46:47], v[90:91], v[126:127], v[46:47] op_sel_hi:[1,0,1]
	v_pk_fma_f32 v[44:45], v[92:93], v[126:127], v[44:45] op_sel_hi:[1,0,1]
	v_pk_fma_f32 v[42:43], v[94:95], v[126:127], v[42:43] op_sel_hi:[1,0,1]
	v_pk_fma_f32 v[40:41], v[96:97], v[126:127], v[40:41] op_sel_hi:[1,0,1]
	v_pk_fma_f32 v[24:25], v[98:99], v[126:127], v[24:25] op_sel_hi:[1,0,1]
	v_pk_fma_f32 v[22:23], v[100:101], v[126:127], v[22:23] op_sel_hi:[1,0,1]
	v_pk_fma_f32 v[18:19], v[102:103], v[126:127], v[18:19] op_sel_hi:[1,0,1]
	v_pk_fma_f32 v[48:49], v[104:105], v[126:127], v[48:49] op_sel:[0,1,0]
	v_pk_fma_f32 v[46:47], v[106:107], v[126:127], v[46:47] op_sel:[0,1,0]
	v_pk_fma_f32 v[44:45], v[108:109], v[126:127], v[44:45] op_sel:[0,1,0]
	v_pk_fma_f32 v[42:43], v[110:111], v[126:127], v[42:43] op_sel:[0,1,0]
	v_pk_fma_f32 v[40:41], v[112:113], v[126:127], v[40:41] op_sel:[0,1,0]
	v_pk_fma_f32 v[24:25], v[114:115], v[126:127], v[24:25] op_sel:[0,1,0]
	v_pk_fma_f32 v[22:23], v[116:117], v[126:127], v[22:23] op_sel:[0,1,0]
	v_pk_fma_f32 v[18:19], v[118:119], v[126:127], v[18:19] op_sel:[0,1,0]
	s_waitcnt lgkmcnt(0)
	ds_read_b128 v[88:91], v187 offset:640
	ds_read_b128 v[92:95], v187 offset:656
	ds_read_b128 v[96:99], v187 offset:672
	ds_read_b128 v[100:103], v187 offset:688
	ds_read_b128 v[104:107], v187 offset:704
	ds_read_b128 v[108:111], v187 offset:720
	ds_read_b128 v[112:115], v187 offset:736
	ds_read_b128 v[116:119], v187 offset:752
	global_load_dword v168, v186, s[6:7] offset:-2048
	global_load_dword v169, v186, s[6:7] offset:2048
	s_add_u32 s6, s6, 0x2000
	s_addc_u32 s7, s7, 0
	global_load_dword v170, v186, s[6:7] offset:-2048
	global_load_dword v171, v186, s[6:7] offset:2048
	s_add_u32 s6, s6, 0x2000
	s_addc_u32 s7, s7, 0
	global_load_dword v172, v186, s[6:7] offset:-2048
	global_load_dword v173, v186, s[6:7] offset:2048
	s_add_u32 s6, s6, 0x2000
	s_addc_u32 s7, s7, 0
	global_load_dword v174, v186, s[6:7] offset:-2048
	global_load_dword v175, v186, s[6:7] offset:2048
	s_add_u32 s6, s6, 0x2000
	s_addc_u32 s7, s7, 0
	s_waitcnt vmcnt(44)
;     ...
;             for (int cc = 0; cc < 2; ++cc) { const int col = F.tid + cc * 512; float acc[16];
; #pragma unroll
;                 for (int p = 0; p < 16; ++p) acc[p] = 0.f;
;                 for (int k = 0; k < 64; ++k) { const float w = w3[k * 1024 + col];
; #pragma unroll
;                     for (int p = 0; p < 16; ++p) acc[p] += f2[p * 64 + k] * w; }
	v_pk_fma_f32 v[48:49], v[56:57], v[128:129], v[48:49] op_sel_hi:[1,0,1]
	v_pk_fma_f32 v[46:47], v[58:59], v[128:129], v[46:47] op_sel_hi:[1,0,1]
	v_pk_fma_f32 v[44:45], v[60:61], v[128:129], v[44:45] op_sel_hi:[1,0,1]
	v_pk_fma_f32 v[42:43], v[62:63], v[128:129], v[42:43] op_sel_hi:[1,0,1]
	v_pk_fma_f32 v[40:41], v[64:65], v[128:129], v[40:41] op_sel_hi:[1,0,1]
	v_pk_fma_f32 v[24:25], v[66:67], v[128:129], v[24:25] op_sel_hi:[1,0,1]
	v_pk_fma_f32 v[22:23], v[68:69], v[128:129], v[22:23] op_sel_hi:[1,0,1]
	v_pk_fma_f32 v[18:19], v[70:71], v[128:129], v[18:19] op_sel_hi:[1,0,1]
	v_pk_fma_f32 v[48:49], v[72:73], v[128:129], v[48:49] op_sel:[0,1,0]
	v_pk_fma_f32 v[46:47], v[74:75], v[128:129], v[46:47] op_sel:[0,1,0]
	v_pk_fma_f32 v[44:45], v[76:77], v[128:129], v[44:45] op_sel:[0,1,0]
	v_pk_fma_f32 v[42:43], v[78:79], v[128:129], v[42:43] op_sel:[0,1,0]
	v_pk_fma_f32 v[40:41], v[80:81], v[128:129], v[40:41] op_sel:[0,1,0]
	v_pk_fma_f32 v[24:25], v[82:83], v[128:129], v[24:25] op_sel:[0,1,0]
	v_pk_fma_f32 v[22:23], v[84:85], v[128:129], v[22:23] op_sel:[0,1,0]
	v_pk_fma_f32 v[18:19], v[86:87], v[128:129], v[18:19] op_sel:[0,1,0]
	s_waitcnt lgkmcnt(0)
	ds_read_b128 v[56:59], v187 offset:768
	ds_read_b128 v[60:63], v187 offset:784
	ds_read_b128 v[64:67], v187 offset:800
	ds_read_b128 v[68:71], v187 offset:816
	ds_read_b128 v[72:75], v187 offset:832
	ds_read_b128 v[76:79], v187 offset:848
	ds_read_b128 v[80:83], v187 offset:864
	ds_read_b128 v[84:87], v187 offset:880
	v_pk_fma_f32 v[48:49], v[88:89], v[130:131], v[48:49] op_sel_hi:[1,0,1]
	v_pk_fma_f32 v[46:47], v[90:91], v[130:131], v[46:47] op_sel_hi:[1,0,1]
	v_pk_fma_f32 v[44:45], v[92:93], v[130:131], v[44:45] op_sel_hi:[1,0,1]
	v_pk_fma_f32 v[42:43], v[94:95], v[130:131], v[42:43] op_sel_hi:[1,0,1]
	v_pk_fma_f32 v[40:41], v[96:97], v[130:131], v[40:41] op_sel_hi:[1,0,1]
	v_pk_fma_f32 v[24:25], v[98:99], v[130:131], v[24:25] op_sel_hi:[1,0,1]
	v_pk_fma_f32 v[22:23], v[100:101], v[130:131], v[22:23] op_sel_hi:[1,0,1]
	v_pk_fma_f32 v[18:19], v[102:103], v[130:131], v[18:19] op_sel_hi:[1,0,1]
	v_pk_fma_f32 v[48:49], v[104:105], v[130:131], v[48:49] op_sel:[0,1,0]
	v_pk_fma_f32 v[46:47], v[106:107], v[130:131], v[46:47] op_sel:[0,1,0]
	v_pk_fma_f32 v[44:45], v[108:109], v[130:131], v[44:45] op_sel:[0,1,0]
	v_pk_fma_f32 v[42:43], v[110:111], v[130:131], v[42:43] op_sel:[0,1,0]
	v_pk_fma_f32 v[40:41], v[112:113], v[130:131], v[40:41] op_sel:[0,1,0]
	v_pk_fma_f32 v[24:25], v[114:115], v[130:131], v[24:25] op_sel:[0,1,0]
	v_pk_fma_f32 v[22:23], v[116:117], v[130:131], v[22:23] op_sel:[0,1,0]
	v_pk_fma_f32 v[18:19], v[118:119], v[130:131], v[18:19] op_sel:[0,1,0]
	s_waitcnt lgkmcnt(0)
	ds_read_b128 v[88:91], v187 offset:896
	ds_read_b128 v[92:95], v187 offset:912
	ds_read_b128 v[96:99], v187 offset:928
	ds_read_b128 v[100:103], v187 offset:944
	ds_read_b128 v[104:107], v187 offset:960
	ds_read_b128 v[108:111], v187 offset:976
	ds_read_b128 v[112:115], v187 offset:992
	ds_read_b128 v[116:119], v187 offset:1008
	s_waitcnt vmcnt(40)
	v_pk_fma_f32 v[48:49], v[56:57], v[132:133], v[48:49] op_sel_hi:[1,0,1]
	v_pk_fma_f32 v[46:47], v[58:59], v[132:133], v[46:47] op_sel_hi:[1,0,1]
	v_pk_fma_f32 v[44:45], v[60:61], v[132:133], v[44:45] op_sel_hi:[1,0,1]
	v_pk_fma_f32 v[42:43], v[62:63], v[132:133], v[42:43] op_sel_hi:[1,0,1]
	v_pk_fma_f32 v[40:41], v[64:65], v[132:133], v[40:41] op_sel_hi:[1,0,1]
	v_pk_fma_f32 v[24:25], v[66:67], v[132:133], v[24:25] op_sel_hi:[1,0,1]
	v_pk_fma_f32 v[22:23], v[68:69], v[132:133], v[22:23] op_sel_hi:[1,0,1]
	v_pk_fma_f32 v[18:19], v[70:71], v[132:133], v[18:19] op_sel_hi:[1,0,1]
	v_pk_fma_f32 v[48:49], v[72:73], v[132:133], v[48:49] op_sel:[0,1,0]
	v_pk_fma_f32 v[46:47], v[74:75], v[132:133], v[46:47] op_sel:[0,1,0]
	v_pk_fma_f32 v[44:45], v[76:77], v[132:133], v[44:45] op_sel:[0,1,0]
	v_pk_fma_f32 v[42:43], v[78:79], v[132:133], v[42:43] op_sel:[0,1,0]
	v_pk_fma_f32 v[40:41], v[80:81], v[132:133], v[40:41] op_sel:[0,1,0]
	v_pk_fma_f32 v[24:25], v[82:83], v[132:133], v[24:25] op_sel:[0,1,0]
	v_pk_fma_f32 v[22:23], v[84:85], v[132:133], v[22:23] op_sel:[0,1,0]
	v_pk_fma_f32 v[18:19], v[86:87], v[132:133], v[18:19] op_sel:[0,1,0]
	s_waitcnt lgkmcnt(0)
	ds_read_b128 v[56:59], v187 offset:1024
	ds_read_b128 v[60:63], v187 offset:1040
	ds_read_b128 v[64:67], v187 offset:1056
	ds_read_b128 v[68:71], v187 offset:1072
	ds_read_b128 v[72:75], v187 offset:1088
	ds_read_b128 v[76:79], v187 offset:1104
	ds_read_b128 v[80:83], v187 offset:1120
	ds_read_b128 v[84:87], v187 offset:1136
	v_pk_fma_f32 v[48:49], v[88:89], v[134:135], v[48:49] op_sel_hi:[1,0,1]
	v_pk_fma_f32 v[46:47], v[90:91], v[134:135], v[46:47] op_sel_hi:[1,0,1]
	v_pk_fma_f32 v[44:45], v[92:93], v[134:135], v[44:45] op_sel_hi:[1,0,1]
	v_pk_fma_f32 v[42:43], v[94:95], v[134:135], v[42:43] op_sel_hi:[1,0,1]
	v_pk_fma_f32 v[40:41], v[96:97], v[134:135], v[40:41] op_sel_hi:[1,0,1]
	v_pk_fma_f32 v[24:25], v[98:99], v[134:135], v[24:25] op_sel_hi:[1,0,1]
	v_pk_fma_f32 v[22:23], v[100:101], v[134:135], v[22:23] op_sel_hi:[1,0,1]
	v_pk_fma_f32 v[18:19], v[102:103], v[134:135], v[18:19] op_sel_hi:[1,0,1]
	v_pk_fma_f32 v[48:49], v[104:105], v[134:135], v[48:49] op_sel:[0,1,0]
	v_pk_fma_f32 v[46:47], v[106:107], v[134:135], v[46:47] op_sel:[0,1,0]
	v_pk_fma_f32 v[44:45], v[108:109], v[134:135], v[44:45] op_sel:[0,1,0]
	v_pk_fma_f32 v[42:43], v[110:111], v[134:135], v[42:43] op_sel:[0,1,0]
	v_pk_fma_f32 v[40:41], v[112:113], v[134:135], v[40:41] op_sel:[0,1,0]
	v_pk_fma_f32 v[24:25], v[114:115], v[134:135], v[24:25] op_sel:[0,1,0]
	v_pk_fma_f32 v[22:23], v[116:117], v[134:135], v[22:23] op_sel:[0,1,0]
	v_pk_fma_f32 v[18:19], v[118:119], v[134:135], v[18:19] op_sel:[0,1,0]
	s_waitcnt lgkmcnt(0)
;     ...
;             for (int cc = 0; cc < 2; ++cc) { const int col = F.tid + cc * 512; float acc[16];
; #pragma unroll
;                 for (int p = 0; p < 16; ++p) acc[p] = 0.f;
;                 for (int k = 0; k < 64; ++k) { const float w = w3[k * 1024 + col];
; #pragma unroll
;                     for (int p = 0; p < 16; ++p) acc[p] += f2[p * 64 + k] * w; }
	ds_read_b128 v[88:91], v187 offset:1152
	ds_read_b128 v[92:95], v187 offset:1168
	ds_read_b128 v[96:99], v187 offset:1184
	ds_read_b128 v[100:103], v187 offset:1200
	ds_read_b128 v[104:107], v187 offset:1216
	ds_read_b128 v[108:111], v187 offset:1232
	ds_read_b128 v[112:115], v187 offset:1248
	ds_read_b128 v[116:119], v187 offset:1264
	global_load_dword v176, v186, s[6:7] offset:-2048
	global_load_dword v177, v186, s[6:7] offset:2048
	s_add_u32 s6, s6, 0x2000
	s_addc_u32 s7, s7, 0
	global_load_dword v178, v186, s[6:7] offset:-2048
	global_load_dword v179, v186, s[6:7] offset:2048
	s_add_u32 s6, s6, 0x2000
	s_addc_u32 s7, s7, 0
	global_load_dword v180, v186, s[6:7] offset:-2048
	global_load_dword v182, v186, s[6:7] offset:2048
	s_add_u32 s6, s6, 0x2000
	s_addc_u32 s7, s7, 0
	global_load_dword v183, v186, s[6:7] offset:-2048
	global_load_dword v184, v186, s[6:7] offset:2048
	s_waitcnt vmcnt(44)
	v_pk_fma_f32 v[48:49], v[56:57], v[136:137], v[48:49] op_sel_hi:[1,0,1]
	v_pk_fma_f32 v[46:47], v[58:59], v[136:137], v[46:47] op_sel_hi:[1,0,1]
	v_pk_fma_f32 v[44:45], v[60:61], v[136:137], v[44:45] op_sel_hi:[1,0,1]
	v_pk_fma_f32 v[42:43], v[62:63], v[136:137], v[42:43] op_sel_hi:[1,0,1]
	v_pk_fma_f32 v[40:41], v[64:65], v[136:137], v[40:41] op_sel_hi:[1,0,1]
	v_pk_fma_f32 v[24:25], v[66:67], v[136:137], v[24:25] op_sel_hi:[1,0,1]
	v_pk_fma_f32 v[22:23], v[68:69], v[136:137], v[22:23] op_sel_hi:[1,0,1]
	v_pk_fma_f32 v[18:19], v[70:71], v[136:137], v[18:19] op_sel_hi:[1,0,1]
	v_pk_fma_f32 v[48:49], v[72:73], v[136:137], v[48:49] op_sel:[0,1,0]
	v_pk_fma_f32 v[46:47], v[74:75], v[136:137], v[46:47] op_sel:[0,1,0]
	v_pk_fma_f32 v[44:45], v[76:77], v[136:137], v[44:45] op_sel:[0,1,0]
	v_pk_fma_f32 v[42:43], v[78:79], v[136:137], v[42:43] op_sel:[0,1,0]
	v_pk_fma_f32 v[40:41], v[80:81], v[136:137], v[40:41] op_sel:[0,1,0]
	v_pk_fma_f32 v[24:25], v[82:83], v[136:137], v[24:25] op_sel:[0,1,0]
	v_pk_fma_f32 v[22:23], v[84:85], v[136:137], v[22:23] op_sel:[0,1,0]
	v_pk_fma_f32 v[18:19], v[86:87], v[136:137], v[18:19] op_sel:[0,1,0]
	s_waitcnt lgkmcnt(0)
	ds_read_b128 v[56:59], v187 offset:1280
	ds_read_b128 v[60:63], v187 offset:1296
	ds_read_b128 v[64:67], v187 offset:1312
	ds_read_b128 v[68:71], v187 offset:1328
	ds_read_b128 v[72:75], v187 offset:1344
	ds_read_b128 v[76:79], v187 offset:1360
	ds_read_b128 v[80:83], v187 offset:1376
	ds_read_b128 v[84:87], v187 offset:1392
	v_pk_fma_f32 v[48:49], v[88:89], v[138:139], v[48:49] op_sel_hi:[1,0,1]
	v_pk_fma_f32 v[46:47], v[90:91], v[138:139], v[46:47] op_sel_hi:[1,0,1]
	v_pk_fma_f32 v[44:45], v[92:93], v[138:139], v[44:45] op_sel_hi:[1,0,1]
	v_pk_fma_f32 v[42:43], v[94:95], v[138:139], v[42:43] op_sel_hi:[1,0,1]
	v_pk_fma_f32 v[40:41], v[96:97], v[138:139], v[40:41] op_sel_hi:[1,0,1]
	v_pk_fma_f32 v[24:25], v[98:99], v[138:139], v[24:25] op_sel_hi:[1,0,1]
	v_pk_fma_f32 v[22:23], v[100:101], v[138:139], v[22:23] op_sel_hi:[1,0,1]
	v_pk_fma_f32 v[18:19], v[102:103], v[138:139], v[18:19] op_sel_hi:[1,0,1]
	v_pk_fma_f32 v[48:49], v[104:105], v[138:139], v[48:49] op_sel:[0,1,0]
	v_pk_fma_f32 v[46:47], v[106:107], v[138:139], v[46:47] op_sel:[0,1,0]
	v_pk_fma_f32 v[44:45], v[108:109], v[138:139], v[44:45] op_sel:[0,1,0]
	v_pk_fma_f32 v[42:43], v[110:111], v[138:139], v[42:43] op_sel:[0,1,0]
	v_pk_fma_f32 v[40:41], v[112:113], v[138:139], v[40:41] op_sel:[0,1,0]
	v_pk_fma_f32 v[24:25], v[114:115], v[138:139], v[24:25] op_sel:[0,1,0]
	v_pk_fma_f32 v[22:23], v[116:117], v[138:139], v[22:23] op_sel:[0,1,0]
	v_pk_fma_f32 v[18:19], v[118:119], v[138:139], v[18:19] op_sel:[0,1,0]
	s_waitcnt lgkmcnt(0)
	ds_read_b128 v[88:91], v187 offset:1408
	ds_read_b128 v[92:95], v187 offset:1424
	ds_read_b128 v[96:99], v187 offset:1440
	ds_read_b128 v[100:103], v187 offset:1456
	ds_read_b128 v[104:107], v187 offset:1472
	ds_read_b128 v[108:111], v187 offset:1488
	ds_read_b128 v[112:115], v187 offset:1504
	ds_read_b128 v[116:119], v187 offset:1520
	s_waitcnt vmcnt(40)
	v_pk_fma_f32 v[48:49], v[56:57], v[140:141], v[48:49] op_sel_hi:[1,0,1]
	v_pk_fma_f32 v[46:47], v[58:59], v[140:141], v[46:47] op_sel_hi:[1,0,1]
	v_pk_fma_f32 v[44:45], v[60:61], v[140:141], v[44:45] op_sel_hi:[1,0,1]
	v_pk_fma_f32 v[42:43], v[62:63], v[140:141], v[42:43] op_sel_hi:[1,0,1]
	v_pk_fma_f32 v[40:41], v[64:65], v[140:141], v[40:41] op_sel_hi:[1,0,1]
	v_pk_fma_f32 v[24:25], v[66:67], v[140:141], v[24:25] op_sel_hi:[1,0,1]
	v_pk_fma_f32 v[22:23], v[68:69], v[140:141], v[22:23] op_sel_hi:[1,0,1]
	v_pk_fma_f32 v[18:19], v[70:71], v[140:141], v[18:19] op_sel_hi:[1,0,1]
	v_pk_fma_f32 v[48:49], v[72:73], v[140:141], v[48:49] op_sel:[0,1,0]
	v_pk_fma_f32 v[46:47], v[74:75], v[140:141], v[46:47] op_sel:[0,1,0]
	v_pk_fma_f32 v[44:45], v[76:77], v[140:141], v[44:45] op_sel:[0,1,0]
	v_pk_fma_f32 v[42:43], v[78:79], v[140:141], v[42:43] op_sel:[0,1,0]
	v_pk_fma_f32 v[40:41], v[80:81], v[140:141], v[40:41] op_sel:[0,1,0]
	v_pk_fma_f32 v[24:25], v[82:83], v[140:141], v[24:25] op_sel:[0,1,0]
	v_pk_fma_f32 v[22:23], v[84:85], v[140:141], v[22:23] op_sel:[0,1,0]
	v_pk_fma_f32 v[18:19], v[86:87], v[140:141], v[18:19] op_sel:[0,1,0]
	s_waitcnt lgkmcnt(0)
;     ...
;             for (int cc = 0; cc < 2; ++cc) { const int col = F.tid + cc * 512; float acc[16];
; #pragma unroll
;                 for (int p = 0; p < 16; ++p) acc[p] = 0.f;
;                 for (int k = 0; k < 64; ++k) { const float w = w3[k * 1024 + col];
; #pragma unroll
;                     for (int p = 0; p < 16; ++p) acc[p] += f2[p * 64 + k] * w; }
;                 const int c = col & 255; const float delta = 3.0701134573253945f + (float)c * ((15.350567286626973f - 3.0701134573253945f) / 255.0f);
; #pragma unroll
;                 for (int p4 = 0; p4 < 4; ++p4) { f32x4 o;
; #pragma unroll
;                     for (int q = 0; q < 4; ++q) { const int n = n0 + p4 * 4 + q; const float tt = (float)n / (float)(L - 1); o[q] = acc[p4 * 4 + q] * __expf(-tt * delta); }
;                     *(f32x4*)(FT + (size_t)col * L + n0 + p4 * 4) = o; } }
	ds_read_b128 v[56:59], v187 offset:1536
	ds_read_b128 v[60:63], v187 offset:1552
	ds_read_b128 v[64:67], v187 offset:1568
	ds_read_b128 v[68:71], v187 offset:1584
	ds_read_b128 v[72:75], v187 offset:1600
	ds_read_b128 v[76:79], v187 offset:1616
	ds_read_b128 v[80:83], v187 offset:1632
	ds_read_b128 v[84:87], v187 offset:1648
	v_pk_fma_f32 v[48:49], v[88:89], v[142:143], v[48:49] op_sel_hi:[1,0,1]
	v_pk_fma_f32 v[46:47], v[90:91], v[142:143], v[46:47] op_sel_hi:[1,0,1]
	v_pk_fma_f32 v[44:45], v[92:93], v[142:143], v[44:45] op_sel_hi:[1,0,1]
	v_pk_fma_f32 v[42:43], v[94:95], v[142:143], v[42:43] op_sel_hi:[1,0,1]
	v_pk_fma_f32 v[40:41], v[96:97], v[142:143], v[40:41] op_sel_hi:[1,0,1]
	v_pk_fma_f32 v[24:25], v[98:99], v[142:143], v[24:25] op_sel_hi:[1,0,1]
	v_pk_fma_f32 v[22:23], v[100:101], v[142:143], v[22:23] op_sel_hi:[1,0,1]
	v_pk_fma_f32 v[18:19], v[102:103], v[142:143], v[18:19] op_sel_hi:[1,0,1]
	v_pk_fma_f32 v[48:49], v[104:105], v[142:143], v[48:49] op_sel:[0,1,0]
	v_pk_fma_f32 v[46:47], v[106:107], v[142:143], v[46:47] op_sel:[0,1,0]
	v_pk_fma_f32 v[44:45], v[108:109], v[142:143], v[44:45] op_sel:[0,1,0]
	v_pk_fma_f32 v[42:43], v[110:111], v[142:143], v[42:43] op_sel:[0,1,0]
	v_pk_fma_f32 v[40:41], v[112:113], v[142:143], v[40:41] op_sel:[0,1,0]
	v_pk_fma_f32 v[24:25], v[114:115], v[142:143], v[24:25] op_sel:[0,1,0]
	v_pk_fma_f32 v[22:23], v[116:117], v[142:143], v[22:23] op_sel:[0,1,0]
	v_pk_fma_f32 v[18:19], v[118:119], v[142:143], v[18:19] op_sel:[0,1,0]
	s_waitcnt lgkmcnt(0)
	ds_read_b128 v[88:91], v187 offset:1664
	ds_read_b128 v[92:95], v187 offset:1680
	ds_read_b128 v[96:99], v187 offset:1696
	ds_read_b128 v[100:103], v187 offset:1712
	ds_read_b128 v[104:107], v187 offset:1728
	ds_read_b128 v[108:111], v187 offset:1744
	ds_read_b128 v[112:115], v187 offset:1760
	ds_read_b128 v[116:119], v187 offset:1776
	s_waitcnt vmcnt(36)
	v_pk_fma_f32 v[48:49], v[56:57], v[144:145], v[48:49] op_sel_hi:[1,0,1]
	v_pk_fma_f32 v[46:47], v[58:59], v[144:145], v[46:47] op_sel_hi:[1,0,1]
	v_pk_fma_f32 v[44:45], v[60:61], v[144:145], v[44:45] op_sel_hi:[1,0,1]
	v_pk_fma_f32 v[42:43], v[62:63], v[144:145], v[42:43] op_sel_hi:[1,0,1]
	v_pk_fma_f32 v[40:41], v[64:65], v[144:145], v[40:41] op_sel_hi:[1,0,1]
	v_pk_fma_f32 v[24:25], v[66:67], v[144:145], v[24:25] op_sel_hi:[1,0,1]
	v_pk_fma_f32 v[22:23], v[68:69], v[144:145], v[22:23] op_sel_hi:[1,0,1]
	v_pk_fma_f32 v[18:19], v[70:71], v[144:145], v[18:19] op_sel_hi:[1,0,1]
	v_pk_fma_f32 v[48:49], v[72:73], v[144:145], v[48:49] op_sel:[0,1,0]
	v_pk_fma_f32 v[46:47], v[74:75], v[144:145], v[46:47] op_sel:[0,1,0]
	v_pk_fma_f32 v[44:45], v[76:77], v[144:145], v[44:45] op_sel:[0,1,0]
	v_pk_fma_f32 v[42:43], v[78:79], v[144:145], v[42:43] op_sel:[0,1,0]
	v_pk_fma_f32 v[40:41], v[80:81], v[144:145], v[40:41] op_sel:[0,1,0]
	v_pk_fma_f32 v[24:25], v[82:83], v[144:145], v[24:25] op_sel:[0,1,0]
	v_pk_fma_f32 v[22:23], v[84:85], v[144:145], v[22:23] op_sel:[0,1,0]
	v_pk_fma_f32 v[18:19], v[86:87], v[144:145], v[18:19] op_sel:[0,1,0]
	s_waitcnt lgkmcnt(0)
	ds_read_b128 v[56:59], v187 offset:1792
	ds_read_b128 v[60:63], v187 offset:1808
	ds_read_b128 v[64:67], v187 offset:1824
	ds_read_b128 v[68:71], v187 offset:1840
	ds_read_b128 v[72:75], v187 offset:1856
	ds_read_b128 v[76:79], v187 offset:1872
	ds_read_b128 v[80:83], v187 offset:1888
	ds_read_b128 v[84:87], v187 offset:1904
	v_pk_fma_f32 v[48:49], v[88:89], v[146:147], v[48:49] op_sel_hi:[1,0,1]
	v_pk_fma_f32 v[46:47], v[90:91], v[146:147], v[46:47] op_sel_hi:[1,0,1]
	v_pk_fma_f32 v[44:45], v[92:93], v[146:147], v[44:45] op_sel_hi:[1,0,1]
	v_pk_fma_f32 v[42:43], v[94:95], v[146:147], v[42:43] op_sel_hi:[1,0,1]
	v_pk_fma_f32 v[40:41], v[96:97], v[146:147], v[40:41] op_sel_hi:[1,0,1]
	v_pk_fma_f32 v[24:25], v[98:99], v[146:147], v[24:25] op_sel_hi:[1,0,1]
	v_pk_fma_f32 v[22:23], v[100:101], v[146:147], v[22:23] op_sel_hi:[1,0,1]
	v_pk_fma_f32 v[18:19], v[102:103], v[146:147], v[18:19] op_sel_hi:[1,0,1]
	v_pk_fma_f32 v[48:49], v[104:105], v[146:147], v[48:49] op_sel:[0,1,0]
	v_pk_fma_f32 v[46:47], v[106:107], v[146:147], v[46:47] op_sel:[0,1,0]
	v_pk_fma_f32 v[44:45], v[108:109], v[146:147], v[44:45] op_sel:[0,1,0]
	v_pk_fma_f32 v[42:43], v[110:111], v[146:147], v[42:43] op_sel:[0,1,0]
	v_pk_fma_f32 v[40:41], v[112:113], v[146:147], v[40:41] op_sel:[0,1,0]
	v_pk_fma_f32 v[24:25], v[114:115], v[146:147], v[24:25] op_sel:[0,1,0]
	v_pk_fma_f32 v[22:23], v[116:117], v[146:147], v[22:23] op_sel:[0,1,0]
	v_pk_fma_f32 v[18:19], v[118:119], v[146:147], v[18:19] op_sel:[0,1,0]
	s_waitcnt lgkmcnt(0)
	ds_read_b128 v[88:91], v187 offset:1920
	ds_read_b128 v[92:95], v187 offset:1936
	ds_read_b128 v[96:99], v187 offset:1952
	ds_read_b128 v[100:103], v187 offset:1968
	ds_read_b128 v[104:107], v187 offset:1984
	ds_read_b128 v[108:111], v187 offset:2000
	ds_read_b128 v[112:115], v187 offset:2016
	ds_read_b128 v[116:119], v187 offset:2032
	s_waitcnt vmcnt(32)
	v_pk_fma_f32 v[48:49], v[56:57], v[148:149], v[48:49] op_sel_hi:[1,0,1]
	v_pk_fma_f32 v[46:47], v[58:59], v[148:149], v[46:47] op_sel_hi:[1,0,1]
	v_pk_fma_f32 v[44:45], v[60:61], v[148:149], v[44:45] op_sel_hi:[1,0,1]
	v_pk_fma_f32 v[42:43], v[62:63], v[148:149], v[42:43] op_sel_hi:[1,0,1]
	v_pk_fma_f32 v[40:41], v[64:65], v[148:149], v[40:41] op_sel_hi:[1,0,1]
	v_pk_fma_f32 v[24:25], v[66:67], v[148:149], v[24:25] op_sel_hi:[1,0,1]
	v_pk_fma_f32 v[22:23], v[68:69], v[148:149], v[22:23] op_sel_hi:[1,0,1]
	v_pk_fma_f32 v[18:19], v[70:71], v[148:149], v[18:19] op_sel_hi:[1,0,1]
	v_pk_fma_f32 v[48:49], v[72:73], v[148:149], v[48:49] op_sel:[0,1,0]
	v_pk_fma_f32 v[46:47], v[74:75], v[148:149], v[46:47] op_sel:[0,1,0]
	v_pk_fma_f32 v[44:45], v[76:77], v[148:149], v[44:45] op_sel:[0,1,0]
	v_pk_fma_f32 v[42:43], v[78:79], v[148:149], v[42:43] op_sel:[0,1,0]
	v_pk_fma_f32 v[40:41], v[80:81], v[148:149], v[40:41] op_sel:[0,1,0]
	v_pk_fma_f32 v[24:25], v[82:83], v[148:149], v[24:25] op_sel:[0,1,0]
	v_pk_fma_f32 v[22:23], v[84:85], v[148:149], v[22:23] op_sel:[0,1,0]
	v_pk_fma_f32 v[18:19], v[86:87], v[148:149], v[18:19] op_sel:[0,1,0]
	s_waitcnt lgkmcnt(0)
;     ...
;             for (int cc = 0; cc < 2; ++cc) { const int col = F.tid + cc * 512; float acc[16];
; #pragma unroll
;                 for (int p = 0; p < 16; ++p) acc[p] = 0.f;
;                 for (int k = 0; k < 64; ++k) { const float w = w3[k * 1024 + col];
; #pragma unroll
;                     for (int p = 0; p < 16; ++p) acc[p] += f2[p * 64 + k] * w; }
;                 const int c = col & 255; const float delta = 3.0701134573253945f + (float)c * ((15.350567286626973f - 3.0701134573253945f) / 255.0f);
; #pragma unroll
;                 for (int p4 = 0; p4 < 4; ++p4) { f32x4 o;
; #pragma unroll
;                     for (int q = 0; q < 4; ++q) { const int n = n0 + p4 * 4 + q; const float tt = (float)n / (float)(L - 1); o[q] = acc[p4 * 4 + q] * __expf(-tt * delta); }
;                     *(f32x4*)(FT + (size_t)col * L + n0 + p4 * 4) = o; } }
	ds_read_b128 v[56:59], v187 offset:2048
	ds_read_b128 v[60:63], v187 offset:2064
	ds_read_b128 v[64:67], v187 offset:2080
	ds_read_b128 v[68:71], v187 offset:2096
	ds_read_b128 v[72:75], v187 offset:2112
	ds_read_b128 v[76:79], v187 offset:2128
	ds_read_b128 v[80:83], v187 offset:2144
	ds_read_b128 v[84:87], v187 offset:2160
	v_pk_fma_f32 v[48:49], v[88:89], v[150:151], v[48:49] op_sel_hi:[1,0,1]
	v_pk_fma_f32 v[46:47], v[90:91], v[150:151], v[46:47] op_sel_hi:[1,0,1]
	v_pk_fma_f32 v[44:45], v[92:93], v[150:151], v[44:45] op_sel_hi:[1,0,1]
	v_pk_fma_f32 v[42:43], v[94:95], v[150:151], v[42:43] op_sel_hi:[1,0,1]
	v_pk_fma_f32 v[40:41], v[96:97], v[150:151], v[40:41] op_sel_hi:[1,0,1]
	v_pk_fma_f32 v[24:25], v[98:99], v[150:151], v[24:25] op_sel_hi:[1,0,1]
	v_pk_fma_f32 v[22:23], v[100:101], v[150:151], v[22:23] op_sel_hi:[1,0,1]
	v_pk_fma_f32 v[18:19], v[102:103], v[150:151], v[18:19] op_sel_hi:[1,0,1]
	v_pk_fma_f32 v[48:49], v[104:105], v[150:151], v[48:49] op_sel:[0,1,0]
	v_pk_fma_f32 v[46:47], v[106:107], v[150:151], v[46:47] op_sel:[0,1,0]
	v_pk_fma_f32 v[44:45], v[108:109], v[150:151], v[44:45] op_sel:[0,1,0]
	v_pk_fma_f32 v[42:43], v[110:111], v[150:151], v[42:43] op_sel:[0,1,0]
	v_pk_fma_f32 v[40:41], v[112:113], v[150:151], v[40:41] op_sel:[0,1,0]
	v_pk_fma_f32 v[24:25], v[114:115], v[150:151], v[24:25] op_sel:[0,1,0]
	v_pk_fma_f32 v[22:23], v[116:117], v[150:151], v[22:23] op_sel:[0,1,0]
	v_pk_fma_f32 v[18:19], v[118:119], v[150:151], v[18:19] op_sel:[0,1,0]
	s_waitcnt lgkmcnt(0)
	ds_read_b128 v[88:91], v187 offset:2176
	ds_read_b128 v[92:95], v187 offset:2192
	ds_read_b128 v[96:99], v187 offset:2208
	ds_read_b128 v[100:103], v187 offset:2224
	ds_read_b128 v[104:107], v187 offset:2240
	ds_read_b128 v[108:111], v187 offset:2256
	ds_read_b128 v[112:115], v187 offset:2272
	ds_read_b128 v[116:119], v187 offset:2288
	s_waitcnt vmcnt(28)
	v_pk_fma_f32 v[48:49], v[56:57], v[152:153], v[48:49] op_sel_hi:[1,0,1]
	v_pk_fma_f32 v[46:47], v[58:59], v[152:153], v[46:47] op_sel_hi:[1,0,1]
	v_pk_fma_f32 v[44:45], v[60:61], v[152:153], v[44:45] op_sel_hi:[1,0,1]
	v_pk_fma_f32 v[42:43], v[62:63], v[152:153], v[42:43] op_sel_hi:[1,0,1]
	v_pk_fma_f32 v[40:41], v[64:65], v[152:153], v[40:41] op_sel_hi:[1,0,1]
	v_pk_fma_f32 v[24:25], v[66:67], v[152:153], v[24:25] op_sel_hi:[1,0,1]
	v_pk_fma_f32 v[22:23], v[68:69], v[152:153], v[22:23] op_sel_hi:[1,0,1]
	v_pk_fma_f32 v[18:19], v[70:71], v[152:153], v[18:19] op_sel_hi:[1,0,1]
	v_pk_fma_f32 v[48:49], v[72:73], v[152:153], v[48:49] op_sel:[0,1,0]
	v_pk_fma_f32 v[46:47], v[74:75], v[152:153], v[46:47] op_sel:[0,1,0]
	v_pk_fma_f32 v[44:45], v[76:77], v[152:153], v[44:45] op_sel:[0,1,0]
	v_pk_fma_f32 v[42:43], v[78:79], v[152:153], v[42:43] op_sel:[0,1,0]
	v_pk_fma_f32 v[40:41], v[80:81], v[152:153], v[40:41] op_sel:[0,1,0]
	v_pk_fma_f32 v[24:25], v[82:83], v[152:153], v[24:25] op_sel:[0,1,0]
	v_pk_fma_f32 v[22:23], v[84:85], v[152:153], v[22:23] op_sel:[0,1,0]
	v_pk_fma_f32 v[18:19], v[86:87], v[152:153], v[18:19] op_sel:[0,1,0]
	s_waitcnt lgkmcnt(0)
	ds_read_b128 v[56:59], v187 offset:2304
	ds_read_b128 v[60:63], v187 offset:2320
	ds_read_b128 v[64:67], v187 offset:2336
	ds_read_b128 v[68:71], v187 offset:2352
	ds_read_b128 v[72:75], v187 offset:2368
	ds_read_b128 v[76:79], v187 offset:2384
	ds_read_b128 v[80:83], v187 offset:2400
	ds_read_b128 v[84:87], v187 offset:2416
	v_pk_fma_f32 v[48:49], v[88:89], v[154:155], v[48:49] op_sel_hi:[1,0,1]
	v_pk_fma_f32 v[46:47], v[90:91], v[154:155], v[46:47] op_sel_hi:[1,0,1]
	v_pk_fma_f32 v[44:45], v[92:93], v[154:155], v[44:45] op_sel_hi:[1,0,1]
	v_pk_fma_f32 v[42:43], v[94:95], v[154:155], v[42:43] op_sel_hi:[1,0,1]
	v_pk_fma_f32 v[40:41], v[96:97], v[154:155], v[40:41] op_sel_hi:[1,0,1]
	v_pk_fma_f32 v[24:25], v[98:99], v[154:155], v[24:25] op_sel_hi:[1,0,1]
	v_pk_fma_f32 v[22:23], v[100:101], v[154:155], v[22:23] op_sel_hi:[1,0,1]
	v_pk_fma_f32 v[18:19], v[102:103], v[154:155], v[18:19] op_sel_hi:[1,0,1]
	v_pk_fma_f32 v[48:49], v[104:105], v[154:155], v[48:49] op_sel:[0,1,0]
	v_pk_fma_f32 v[46:47], v[106:107], v[154:155], v[46:47] op_sel:[0,1,0]
	v_pk_fma_f32 v[44:45], v[108:109], v[154:155], v[44:45] op_sel:[0,1,0]
	v_pk_fma_f32 v[42:43], v[110:111], v[154:155], v[42:43] op_sel:[0,1,0]
	v_pk_fma_f32 v[40:41], v[112:113], v[154:155], v[40:41] op_sel:[0,1,0]
	v_pk_fma_f32 v[24:25], v[114:115], v[154:155], v[24:25] op_sel:[0,1,0]
	v_pk_fma_f32 v[22:23], v[116:117], v[154:155], v[22:23] op_sel:[0,1,0]
	v_pk_fma_f32 v[18:19], v[118:119], v[154:155], v[18:19] op_sel:[0,1,0]
	s_waitcnt lgkmcnt(0)
	ds_read_b128 v[88:91], v187 offset:2432
	ds_read_b128 v[92:95], v187 offset:2448
	ds_read_b128 v[96:99], v187 offset:2464
	ds_read_b128 v[100:103], v187 offset:2480
	ds_read_b128 v[104:107], v187 offset:2496
	ds_read_b128 v[108:111], v187 offset:2512
	ds_read_b128 v[112:115], v187 offset:2528
	ds_read_b128 v[116:119], v187 offset:2544
	s_waitcnt vmcnt(24)
	v_pk_fma_f32 v[48:49], v[56:57], v[156:157], v[48:49] op_sel_hi:[1,0,1]
	v_pk_fma_f32 v[46:47], v[58:59], v[156:157], v[46:47] op_sel_hi:[1,0,1]
	v_pk_fma_f32 v[44:45], v[60:61], v[156:157], v[44:45] op_sel_hi:[1,0,1]
	v_pk_fma_f32 v[42:43], v[62:63], v[156:157], v[42:43] op_sel_hi:[1,0,1]
	v_pk_fma_f32 v[40:41], v[64:65], v[156:157], v[40:41] op_sel_hi:[1,0,1]
	v_pk_fma_f32 v[24:25], v[66:67], v[156:157], v[24:25] op_sel_hi:[1,0,1]
	v_pk_fma_f32 v[22:23], v[68:69], v[156:157], v[22:23] op_sel_hi:[1,0,1]
	v_pk_fma_f32 v[18:19], v[70:71], v[156:157], v[18:19] op_sel_hi:[1,0,1]
	v_pk_fma_f32 v[48:49], v[72:73], v[156:157], v[48:49] op_sel:[0,1,0]
	v_pk_fma_f32 v[46:47], v[74:75], v[156:157], v[46:47] op_sel:[0,1,0]
	v_pk_fma_f32 v[44:45], v[76:77], v[156:157], v[44:45] op_sel:[0,1,0]
	v_pk_fma_f32 v[42:43], v[78:79], v[156:157], v[42:43] op_sel:[0,1,0]
	v_pk_fma_f32 v[40:41], v[80:81], v[156:157], v[40:41] op_sel:[0,1,0]
	v_pk_fma_f32 v[24:25], v[82:83], v[156:157], v[24:25] op_sel:[0,1,0]
	v_pk_fma_f32 v[22:23], v[84:85], v[156:157], v[22:23] op_sel:[0,1,0]
	v_pk_fma_f32 v[18:19], v[86:87], v[156:157], v[18:19] op_sel:[0,1,0]
	s_waitcnt lgkmcnt(0)
;     ...
;             for (int cc = 0; cc < 2; ++cc) { const int col = F.tid + cc * 512; float acc[16];
; #pragma unroll
;                 for (int p = 0; p < 16; ++p) acc[p] = 0.f;
;                 for (int k = 0; k < 64; ++k) { const float w = w3[k * 1024 + col];
; #pragma unroll
;                     for (int p = 0; p < 16; ++p) acc[p] += f2[p * 64 + k] * w; }
;                 const int c = col & 255; const float delta = 3.0701134573253945f + (float)c * ((15.350567286626973f - 3.0701134573253945f) / 255.0f);
; #pragma unroll
;                 for (int p4 = 0; p4 < 4; ++p4) { f32x4 o;
; #pragma unroll
;                     for (int q = 0; q < 4; ++q) { const int n = n0 + p4 * 4 + q; const float tt = (float)n / (float)(L - 1); o[q] = acc[p4 * 4 + q] * __expf(-tt * delta); }
;                     *(f32x4*)(FT + (size_t)col * L + n0 + p4 * 4) = o; } }
	ds_read_b128 v[56:59], v187 offset:2560
	ds_read_b128 v[60:63], v187 offset:2576
	ds_read_b128 v[64:67], v187 offset:2592
	ds_read_b128 v[68:71], v187 offset:2608
	ds_read_b128 v[72:75], v187 offset:2624
	ds_read_b128 v[76:79], v187 offset:2640
	ds_read_b128 v[80:83], v187 offset:2656
	ds_read_b128 v[84:87], v187 offset:2672
	v_pk_fma_f32 v[48:49], v[88:89], v[158:159], v[48:49] op_sel_hi:[1,0,1]
	v_pk_fma_f32 v[46:47], v[90:91], v[158:159], v[46:47] op_sel_hi:[1,0,1]
	v_pk_fma_f32 v[44:45], v[92:93], v[158:159], v[44:45] op_sel_hi:[1,0,1]
	v_pk_fma_f32 v[42:43], v[94:95], v[158:159], v[42:43] op_sel_hi:[1,0,1]
	v_pk_fma_f32 v[40:41], v[96:97], v[158:159], v[40:41] op_sel_hi:[1,0,1]
	v_pk_fma_f32 v[24:25], v[98:99], v[158:159], v[24:25] op_sel_hi:[1,0,1]
	v_pk_fma_f32 v[22:23], v[100:101], v[158:159], v[22:23] op_sel_hi:[1,0,1]
	v_pk_fma_f32 v[18:19], v[102:103], v[158:159], v[18:19] op_sel_hi:[1,0,1]
	v_pk_fma_f32 v[48:49], v[104:105], v[158:159], v[48:49] op_sel:[0,1,0]
	v_pk_fma_f32 v[46:47], v[106:107], v[158:159], v[46:47] op_sel:[0,1,0]
	v_pk_fma_f32 v[44:45], v[108:109], v[158:159], v[44:45] op_sel:[0,1,0]
	v_pk_fma_f32 v[42:43], v[110:111], v[158:159], v[42:43] op_sel:[0,1,0]
	v_pk_fma_f32 v[40:41], v[112:113], v[158:159], v[40:41] op_sel:[0,1,0]
	v_pk_fma_f32 v[24:25], v[114:115], v[158:159], v[24:25] op_sel:[0,1,0]
	v_pk_fma_f32 v[22:23], v[116:117], v[158:159], v[22:23] op_sel:[0,1,0]
	v_pk_fma_f32 v[18:19], v[118:119], v[158:159], v[18:19] op_sel:[0,1,0]
	s_waitcnt lgkmcnt(0)
	ds_read_b128 v[88:91], v187 offset:2688
	ds_read_b128 v[92:95], v187 offset:2704
	ds_read_b128 v[96:99], v187 offset:2720
	ds_read_b128 v[100:103], v187 offset:2736
	ds_read_b128 v[104:107], v187 offset:2752
	ds_read_b128 v[108:111], v187 offset:2768
	ds_read_b128 v[112:115], v187 offset:2784
	ds_read_b128 v[116:119], v187 offset:2800
	s_waitcnt vmcnt(20)
	v_pk_fma_f32 v[48:49], v[56:57], v[160:161], v[48:49] op_sel_hi:[1,0,1]
	v_pk_fma_f32 v[46:47], v[58:59], v[160:161], v[46:47] op_sel_hi:[1,0,1]
	v_pk_fma_f32 v[44:45], v[60:61], v[160:161], v[44:45] op_sel_hi:[1,0,1]
	v_pk_fma_f32 v[42:43], v[62:63], v[160:161], v[42:43] op_sel_hi:[1,0,1]
	v_pk_fma_f32 v[40:41], v[64:65], v[160:161], v[40:41] op_sel_hi:[1,0,1]
	v_pk_fma_f32 v[24:25], v[66:67], v[160:161], v[24:25] op_sel_hi:[1,0,1]
	v_pk_fma_f32 v[22:23], v[68:69], v[160:161], v[22:23] op_sel_hi:[1,0,1]
	v_pk_fma_f32 v[18:19], v[70:71], v[160:161], v[18:19] op_sel_hi:[1,0,1]
	v_pk_fma_f32 v[48:49], v[72:73], v[160:161], v[48:49] op_sel:[0,1,0]
	v_pk_fma_f32 v[46:47], v[74:75], v[160:161], v[46:47] op_sel:[0,1,0]
	v_pk_fma_f32 v[44:45], v[76:77], v[160:161], v[44:45] op_sel:[0,1,0]
	v_pk_fma_f32 v[42:43], v[78:79], v[160:161], v[42:43] op_sel:[0,1,0]
	v_pk_fma_f32 v[40:41], v[80:81], v[160:161], v[40:41] op_sel:[0,1,0]
	v_pk_fma_f32 v[24:25], v[82:83], v[160:161], v[24:25] op_sel:[0,1,0]
	v_pk_fma_f32 v[22:23], v[84:85], v[160:161], v[22:23] op_sel:[0,1,0]
	v_pk_fma_f32 v[18:19], v[86:87], v[160:161], v[18:19] op_sel:[0,1,0]
	s_waitcnt lgkmcnt(0)
	ds_read_b128 v[56:59], v187 offset:2816
	ds_read_b128 v[60:63], v187 offset:2832
	ds_read_b128 v[64:67], v187 offset:2848
	ds_read_b128 v[68:71], v187 offset:2864
	ds_read_b128 v[72:75], v187 offset:2880
	ds_read_b128 v[76:79], v187 offset:2896
	ds_read_b128 v[80:83], v187 offset:2912
	ds_read_b128 v[84:87], v187 offset:2928
	v_pk_fma_f32 v[48:49], v[88:89], v[162:163], v[48:49] op_sel_hi:[1,0,1]
	v_pk_fma_f32 v[46:47], v[90:91], v[162:163], v[46:47] op_sel_hi:[1,0,1]
	v_pk_fma_f32 v[44:45], v[92:93], v[162:163], v[44:45] op_sel_hi:[1,0,1]
	v_pk_fma_f32 v[42:43], v[94:95], v[162:163], v[42:43] op_sel_hi:[1,0,1]
	v_pk_fma_f32 v[40:41], v[96:97], v[162:163], v[40:41] op_sel_hi:[1,0,1]
	v_pk_fma_f32 v[24:25], v[98:99], v[162:163], v[24:25] op_sel_hi:[1,0,1]
	v_pk_fma_f32 v[22:23], v[100:101], v[162:163], v[22:23] op_sel_hi:[1,0,1]
	v_pk_fma_f32 v[18:19], v[102:103], v[162:163], v[18:19] op_sel_hi:[1,0,1]
	v_pk_fma_f32 v[48:49], v[104:105], v[162:163], v[48:49] op_sel:[0,1,0]
	v_pk_fma_f32 v[46:47], v[106:107], v[162:163], v[46:47] op_sel:[0,1,0]
	v_pk_fma_f32 v[44:45], v[108:109], v[162:163], v[44:45] op_sel:[0,1,0]
	v_pk_fma_f32 v[42:43], v[110:111], v[162:163], v[42:43] op_sel:[0,1,0]
	v_pk_fma_f32 v[40:41], v[112:113], v[162:163], v[40:41] op_sel:[0,1,0]
	v_pk_fma_f32 v[24:25], v[114:115], v[162:163], v[24:25] op_sel:[0,1,0]
	v_pk_fma_f32 v[22:23], v[116:117], v[162:163], v[22:23] op_sel:[0,1,0]
	v_pk_fma_f32 v[18:19], v[118:119], v[162:163], v[18:19] op_sel:[0,1,0]
	s_waitcnt lgkmcnt(0)
	ds_read_b128 v[88:91], v187 offset:2944
	ds_read_b128 v[92:95], v187 offset:2960
	ds_read_b128 v[96:99], v187 offset:2976
	ds_read_b128 v[100:103], v187 offset:2992
	ds_read_b128 v[104:107], v187 offset:3008
	ds_read_b128 v[108:111], v187 offset:3024
	ds_read_b128 v[112:115], v187 offset:3040
	ds_read_b128 v[116:119], v187 offset:3056
	s_waitcnt vmcnt(16)
	v_pk_fma_f32 v[48:49], v[56:57], v[164:165], v[48:49] op_sel_hi:[1,0,1]
	v_pk_fma_f32 v[46:47], v[58:59], v[164:165], v[46:47] op_sel_hi:[1,0,1]
	v_pk_fma_f32 v[44:45], v[60:61], v[164:165], v[44:45] op_sel_hi:[1,0,1]
	v_pk_fma_f32 v[42:43], v[62:63], v[164:165], v[42:43] op_sel_hi:[1,0,1]
	v_pk_fma_f32 v[40:41], v[64:65], v[164:165], v[40:41] op_sel_hi:[1,0,1]
	v_pk_fma_f32 v[24:25], v[66:67], v[164:165], v[24:25] op_sel_hi:[1,0,1]
	v_pk_fma_f32 v[22:23], v[68:69], v[164:165], v[22:23] op_sel_hi:[1,0,1]
	v_pk_fma_f32 v[18:19], v[70:71], v[164:165], v[18:19] op_sel_hi:[1,0,1]
	v_pk_fma_f32 v[48:49], v[72:73], v[164:165], v[48:49] op_sel:[0,1,0]
	v_pk_fma_f32 v[46:47], v[74:75], v[164:165], v[46:47] op_sel:[0,1,0]
	v_pk_fma_f32 v[44:45], v[76:77], v[164:165], v[44:45] op_sel:[0,1,0]
	v_pk_fma_f32 v[42:43], v[78:79], v[164:165], v[42:43] op_sel:[0,1,0]
	v_pk_fma_f32 v[40:41], v[80:81], v[164:165], v[40:41] op_sel:[0,1,0]
	v_pk_fma_f32 v[24:25], v[82:83], v[164:165], v[24:25] op_sel:[0,1,0]
	v_pk_fma_f32 v[22:23], v[84:85], v[164:165], v[22:23] op_sel:[0,1,0]
	v_pk_fma_f32 v[18:19], v[86:87], v[164:165], v[18:19] op_sel:[0,1,0]
	s_waitcnt lgkmcnt(0)
;     ...
;             for (int cc = 0; cc < 2; ++cc) { const int col = F.tid + cc * 512; float acc[16];
; #pragma unroll
;                 for (int p = 0; p < 16; ++p) acc[p] = 0.f;
;                 for (int k = 0; k < 64; ++k) { const float w = w3[k * 1024 + col];
; #pragma unroll
;                     for (int p = 0; p < 16; ++p) acc[p] += f2[p * 64 + k] * w; }
;                 const int c = col & 255; const float delta = 3.0701134573253945f + (float)c * ((15.350567286626973f - 3.0701134573253945f) / 255.0f);
; #pragma unroll
;                 for (int p4 = 0; p4 < 4; ++p4) { f32x4 o;
; #pragma unroll
;                     for (int q = 0; q < 4; ++q) { const int n = n0 + p4 * 4 + q; const float tt = (float)n / (float)(L - 1); o[q] = acc[p4 * 4 + q] * __expf(-tt * delta); }
;                     *(f32x4*)(FT + (size_t)col * L + n0 + p4 * 4) = o; } }
	ds_read_b128 v[56:59], v187 offset:3072
	ds_read_b128 v[60:63], v187 offset:3088
	ds_read_b128 v[64:67], v187 offset:3104
	ds_read_b128 v[68:71], v187 offset:3120
	ds_read_b128 v[72:75], v187 offset:3136
	ds_read_b128 v[76:79], v187 offset:3152
	ds_read_b128 v[80:83], v187 offset:3168
	ds_read_b128 v[84:87], v187 offset:3184
	v_pk_fma_f32 v[48:49], v[88:89], v[166:167], v[48:49] op_sel_hi:[1,0,1]
	v_pk_fma_f32 v[46:47], v[90:91], v[166:167], v[46:47] op_sel_hi:[1,0,1]
	v_pk_fma_f32 v[44:45], v[92:93], v[166:167], v[44:45] op_sel_hi:[1,0,1]
	v_pk_fma_f32 v[42:43], v[94:95], v[166:167], v[42:43] op_sel_hi:[1,0,1]
	v_pk_fma_f32 v[40:41], v[96:97], v[166:167], v[40:41] op_sel_hi:[1,0,1]
	v_pk_fma_f32 v[24:25], v[98:99], v[166:167], v[24:25] op_sel_hi:[1,0,1]
	v_pk_fma_f32 v[22:23], v[100:101], v[166:167], v[22:23] op_sel_hi:[1,0,1]
	v_pk_fma_f32 v[18:19], v[102:103], v[166:167], v[18:19] op_sel_hi:[1,0,1]
	v_pk_fma_f32 v[48:49], v[104:105], v[166:167], v[48:49] op_sel:[0,1,0]
	v_pk_fma_f32 v[46:47], v[106:107], v[166:167], v[46:47] op_sel:[0,1,0]
	v_pk_fma_f32 v[44:45], v[108:109], v[166:167], v[44:45] op_sel:[0,1,0]
	v_pk_fma_f32 v[42:43], v[110:111], v[166:167], v[42:43] op_sel:[0,1,0]
	v_pk_fma_f32 v[40:41], v[112:113], v[166:167], v[40:41] op_sel:[0,1,0]
	v_pk_fma_f32 v[24:25], v[114:115], v[166:167], v[24:25] op_sel:[0,1,0]
	v_pk_fma_f32 v[22:23], v[116:117], v[166:167], v[22:23] op_sel:[0,1,0]
	v_pk_fma_f32 v[18:19], v[118:119], v[166:167], v[18:19] op_sel:[0,1,0]
	s_waitcnt lgkmcnt(0)
	ds_read_b128 v[88:91], v187 offset:3200
	ds_read_b128 v[92:95], v187 offset:3216
	ds_read_b128 v[96:99], v187 offset:3232
	ds_read_b128 v[100:103], v187 offset:3248
	ds_read_b128 v[104:107], v187 offset:3264
	ds_read_b128 v[108:111], v187 offset:3280
	ds_read_b128 v[112:115], v187 offset:3296
	ds_read_b128 v[116:119], v187 offset:3312
	s_waitcnt vmcnt(12)
	v_pk_fma_f32 v[48:49], v[56:57], v[168:169], v[48:49] op_sel_hi:[1,0,1]
	v_pk_fma_f32 v[46:47], v[58:59], v[168:169], v[46:47] op_sel_hi:[1,0,1]
	v_pk_fma_f32 v[44:45], v[60:61], v[168:169], v[44:45] op_sel_hi:[1,0,1]
	v_pk_fma_f32 v[42:43], v[62:63], v[168:169], v[42:43] op_sel_hi:[1,0,1]
	v_pk_fma_f32 v[40:41], v[64:65], v[168:169], v[40:41] op_sel_hi:[1,0,1]
	v_pk_fma_f32 v[24:25], v[66:67], v[168:169], v[24:25] op_sel_hi:[1,0,1]
	v_pk_fma_f32 v[22:23], v[68:69], v[168:169], v[22:23] op_sel_hi:[1,0,1]
	v_pk_fma_f32 v[18:19], v[70:71], v[168:169], v[18:19] op_sel_hi:[1,0,1]
	v_pk_fma_f32 v[48:49], v[72:73], v[168:169], v[48:49] op_sel:[0,1,0]
	v_pk_fma_f32 v[46:47], v[74:75], v[168:169], v[46:47] op_sel:[0,1,0]
	v_pk_fma_f32 v[44:45], v[76:77], v[168:169], v[44:45] op_sel:[0,1,0]
	v_pk_fma_f32 v[42:43], v[78:79], v[168:169], v[42:43] op_sel:[0,1,0]
	v_pk_fma_f32 v[40:41], v[80:81], v[168:169], v[40:41] op_sel:[0,1,0]
	v_pk_fma_f32 v[24:25], v[82:83], v[168:169], v[24:25] op_sel:[0,1,0]
	v_pk_fma_f32 v[22:23], v[84:85], v[168:169], v[22:23] op_sel:[0,1,0]
	v_pk_fma_f32 v[18:19], v[86:87], v[168:169], v[18:19] op_sel:[0,1,0]
	s_waitcnt lgkmcnt(0)
	ds_read_b128 v[56:59], v187 offset:3328
	ds_read_b128 v[60:63], v187 offset:3344
	ds_read_b128 v[64:67], v187 offset:3360
	ds_read_b128 v[68:71], v187 offset:3376
	ds_read_b128 v[72:75], v187 offset:3392
	ds_read_b128 v[76:79], v187 offset:3408
	ds_read_b128 v[80:83], v187 offset:3424
	ds_read_b128 v[84:87], v187 offset:3440
	v_pk_fma_f32 v[48:49], v[88:89], v[170:171], v[48:49] op_sel_hi:[1,0,1]
	v_pk_fma_f32 v[46:47], v[90:91], v[170:171], v[46:47] op_sel_hi:[1,0,1]
	v_pk_fma_f32 v[44:45], v[92:93], v[170:171], v[44:45] op_sel_hi:[1,0,1]
	v_pk_fma_f32 v[42:43], v[94:95], v[170:171], v[42:43] op_sel_hi:[1,0,1]
	v_pk_fma_f32 v[40:41], v[96:97], v[170:171], v[40:41] op_sel_hi:[1,0,1]
	v_pk_fma_f32 v[24:25], v[98:99], v[170:171], v[24:25] op_sel_hi:[1,0,1]
	v_pk_fma_f32 v[22:23], v[100:101], v[170:171], v[22:23] op_sel_hi:[1,0,1]
	v_pk_fma_f32 v[18:19], v[102:103], v[170:171], v[18:19] op_sel_hi:[1,0,1]
	v_pk_fma_f32 v[48:49], v[104:105], v[170:171], v[48:49] op_sel:[0,1,0]
	v_pk_fma_f32 v[46:47], v[106:107], v[170:171], v[46:47] op_sel:[0,1,0]
	v_pk_fma_f32 v[44:45], v[108:109], v[170:171], v[44:45] op_sel:[0,1,0]
	v_pk_fma_f32 v[42:43], v[110:111], v[170:171], v[42:43] op_sel:[0,1,0]
	v_pk_fma_f32 v[40:41], v[112:113], v[170:171], v[40:41] op_sel:[0,1,0]
	v_pk_fma_f32 v[24:25], v[114:115], v[170:171], v[24:25] op_sel:[0,1,0]
	v_pk_fma_f32 v[22:23], v[116:117], v[170:171], v[22:23] op_sel:[0,1,0]
	v_pk_fma_f32 v[18:19], v[118:119], v[170:171], v[18:19] op_sel:[0,1,0]
	s_waitcnt lgkmcnt(0)
	ds_read_b128 v[88:91], v187 offset:3456
	ds_read_b128 v[92:95], v187 offset:3472
	ds_read_b128 v[96:99], v187 offset:3488
	ds_read_b128 v[100:103], v187 offset:3504
	ds_read_b128 v[104:107], v187 offset:3520
	ds_read_b128 v[108:111], v187 offset:3536
	ds_read_b128 v[112:115], v187 offset:3552
	ds_read_b128 v[116:119], v187 offset:3568
	s_waitcnt vmcnt(8)
	v_pk_fma_f32 v[48:49], v[56:57], v[172:173], v[48:49] op_sel_hi:[1,0,1]
	v_pk_fma_f32 v[46:47], v[58:59], v[172:173], v[46:47] op_sel_hi:[1,0,1]
	v_pk_fma_f32 v[44:45], v[60:61], v[172:173], v[44:45] op_sel_hi:[1,0,1]
	v_pk_fma_f32 v[42:43], v[62:63], v[172:173], v[42:43] op_sel_hi:[1,0,1]
	v_pk_fma_f32 v[40:41], v[64:65], v[172:173], v[40:41] op_sel_hi:[1,0,1]
	v_pk_fma_f32 v[24:25], v[66:67], v[172:173], v[24:25] op_sel_hi:[1,0,1]
	v_pk_fma_f32 v[22:23], v[68:69], v[172:173], v[22:23] op_sel_hi:[1,0,1]
	v_pk_fma_f32 v[18:19], v[70:71], v[172:173], v[18:19] op_sel_hi:[1,0,1]
	v_pk_fma_f32 v[48:49], v[72:73], v[172:173], v[48:49] op_sel:[0,1,0]
	v_pk_fma_f32 v[46:47], v[74:75], v[172:173], v[46:47] op_sel:[0,1,0]
	v_pk_fma_f32 v[44:45], v[76:77], v[172:173], v[44:45] op_sel:[0,1,0]
	v_pk_fma_f32 v[42:43], v[78:79], v[172:173], v[42:43] op_sel:[0,1,0]
	v_pk_fma_f32 v[40:41], v[80:81], v[172:173], v[40:41] op_sel:[0,1,0]
	v_pk_fma_f32 v[24:25], v[82:83], v[172:173], v[24:25] op_sel:[0,1,0]
	v_pk_fma_f32 v[22:23], v[84:85], v[172:173], v[22:23] op_sel:[0,1,0]
	v_pk_fma_f32 v[18:19], v[86:87], v[172:173], v[18:19] op_sel:[0,1,0]
	s_waitcnt lgkmcnt(0)
;     ...
;             for (int cc = 0; cc < 2; ++cc) { const int col = F.tid + cc * 512; float acc[16];
; #pragma unroll
;                 for (int p = 0; p < 16; ++p) acc[p] = 0.f;
;                 for (int k = 0; k < 64; ++k) { const float w = w3[k * 1024 + col];
; #pragma unroll
;                     for (int p = 0; p < 16; ++p) acc[p] += f2[p * 64 + k] * w; }
;                 const int c = col & 255; const float delta = 3.0701134573253945f + (float)c * ((15.350567286626973f - 3.0701134573253945f) / 255.0f);
; #pragma unroll
;                 for (int p4 = 0; p4 < 4; ++p4) { f32x4 o;
; #pragma unroll
;                     for (int q = 0; q < 4; ++q) { const int n = n0 + p4 * 4 + q; const float tt = (float)n / (float)(L - 1); o[q] = acc[p4 * 4 + q] * __expf(-tt * delta); }
;                     *(f32x4*)(FT + (size_t)col * L + n0 + p4 * 4) = o; } }
	ds_read_b128 v[56:59], v187 offset:3584
	ds_read_b128 v[60:63], v187 offset:3600
	ds_read_b128 v[64:67], v187 offset:3616
	ds_read_b128 v[68:71], v187 offset:3632
	ds_read_b128 v[72:75], v187 offset:3648
	ds_read_b128 v[76:79], v187 offset:3664
	ds_read_b128 v[80:83], v187 offset:3680
	ds_read_b128 v[84:87], v187 offset:3696
	v_pk_fma_f32 v[48:49], v[88:89], v[174:175], v[48:49] op_sel_hi:[1,0,1]
	v_pk_fma_f32 v[46:47], v[90:91], v[174:175], v[46:47] op_sel_hi:[1,0,1]
	v_pk_fma_f32 v[44:45], v[92:93], v[174:175], v[44:45] op_sel_hi:[1,0,1]
	v_pk_fma_f32 v[42:43], v[94:95], v[174:175], v[42:43] op_sel_hi:[1,0,1]
	v_pk_fma_f32 v[40:41], v[96:97], v[174:175], v[40:41] op_sel_hi:[1,0,1]
	v_pk_fma_f32 v[24:25], v[98:99], v[174:175], v[24:25] op_sel_hi:[1,0,1]
	v_pk_fma_f32 v[22:23], v[100:101], v[174:175], v[22:23] op_sel_hi:[1,0,1]
	v_pk_fma_f32 v[18:19], v[102:103], v[174:175], v[18:19] op_sel_hi:[1,0,1]
	v_pk_fma_f32 v[48:49], v[104:105], v[174:175], v[48:49] op_sel:[0,1,0]
	v_pk_fma_f32 v[46:47], v[106:107], v[174:175], v[46:47] op_sel:[0,1,0]
	v_pk_fma_f32 v[44:45], v[108:109], v[174:175], v[44:45] op_sel:[0,1,0]
	v_pk_fma_f32 v[42:43], v[110:111], v[174:175], v[42:43] op_sel:[0,1,0]
	v_pk_fma_f32 v[40:41], v[112:113], v[174:175], v[40:41] op_sel:[0,1,0]
	v_pk_fma_f32 v[24:25], v[114:115], v[174:175], v[24:25] op_sel:[0,1,0]
	v_pk_fma_f32 v[22:23], v[116:117], v[174:175], v[22:23] op_sel:[0,1,0]
	v_pk_fma_f32 v[18:19], v[118:119], v[174:175], v[18:19] op_sel:[0,1,0]
	s_waitcnt lgkmcnt(0)
	ds_read_b128 v[88:91], v187 offset:3712
	ds_read_b128 v[92:95], v187 offset:3728
	ds_read_b128 v[96:99], v187 offset:3744
	ds_read_b128 v[100:103], v187 offset:3760
	ds_read_b128 v[104:107], v187 offset:3776
	ds_read_b128 v[108:111], v187 offset:3792
	ds_read_b128 v[112:115], v187 offset:3808
	ds_read_b128 v[116:119], v187 offset:3824
	s_waitcnt vmcnt(4)
	v_pk_fma_f32 v[48:49], v[56:57], v[176:177], v[48:49] op_sel_hi:[1,0,1]
	v_pk_fma_f32 v[46:47], v[58:59], v[176:177], v[46:47] op_sel_hi:[1,0,1]
	v_pk_fma_f32 v[44:45], v[60:61], v[176:177], v[44:45] op_sel_hi:[1,0,1]
	v_pk_fma_f32 v[42:43], v[62:63], v[176:177], v[42:43] op_sel_hi:[1,0,1]
	v_pk_fma_f32 v[40:41], v[64:65], v[176:177], v[40:41] op_sel_hi:[1,0,1]
	v_pk_fma_f32 v[24:25], v[66:67], v[176:177], v[24:25] op_sel_hi:[1,0,1]
	v_pk_fma_f32 v[22:23], v[68:69], v[176:177], v[22:23] op_sel_hi:[1,0,1]
	v_pk_fma_f32 v[18:19], v[70:71], v[176:177], v[18:19] op_sel_hi:[1,0,1]
	v_pk_fma_f32 v[48:49], v[72:73], v[176:177], v[48:49] op_sel:[0,1,0]
	v_pk_fma_f32 v[46:47], v[74:75], v[176:177], v[46:47] op_sel:[0,1,0]
	v_pk_fma_f32 v[44:45], v[76:77], v[176:177], v[44:45] op_sel:[0,1,0]
	v_pk_fma_f32 v[42:43], v[78:79], v[176:177], v[42:43] op_sel:[0,1,0]
	v_pk_fma_f32 v[40:41], v[80:81], v[176:177], v[40:41] op_sel:[0,1,0]
	v_pk_fma_f32 v[24:25], v[82:83], v[176:177], v[24:25] op_sel:[0,1,0]
	v_pk_fma_f32 v[22:23], v[84:85], v[176:177], v[22:23] op_sel:[0,1,0]
	v_pk_fma_f32 v[18:19], v[86:87], v[176:177], v[18:19] op_sel:[0,1,0]
	s_waitcnt lgkmcnt(0)
	ds_read_b128 v[56:59], v187 offset:3840
	ds_read_b128 v[60:63], v187 offset:3856
	ds_read_b128 v[64:67], v187 offset:3872
	ds_read_b128 v[68:71], v187 offset:3888
	ds_read_b128 v[72:75], v187 offset:3904
	ds_read_b128 v[76:79], v187 offset:3920
	ds_read_b128 v[80:83], v187 offset:3936
	ds_read_b128 v[84:87], v187 offset:3952
	v_pk_fma_f32 v[48:49], v[88:89], v[178:179], v[48:49] op_sel_hi:[1,0,1]
	v_pk_fma_f32 v[46:47], v[90:91], v[178:179], v[46:47] op_sel_hi:[1,0,1]
	v_pk_fma_f32 v[44:45], v[92:93], v[178:179], v[44:45] op_sel_hi:[1,0,1]
	v_pk_fma_f32 v[42:43], v[94:95], v[178:179], v[42:43] op_sel_hi:[1,0,1]
	v_pk_fma_f32 v[40:41], v[96:97], v[178:179], v[40:41] op_sel_hi:[1,0,1]
	v_pk_fma_f32 v[24:25], v[98:99], v[178:179], v[24:25] op_sel_hi:[1,0,1]
	v_pk_fma_f32 v[22:23], v[100:101], v[178:179], v[22:23] op_sel_hi:[1,0,1]
	v_pk_fma_f32 v[18:19], v[102:103], v[178:179], v[18:19] op_sel_hi:[1,0,1]
	v_pk_fma_f32 v[48:49], v[104:105], v[178:179], v[48:49] op_sel:[0,1,0]
	v_pk_fma_f32 v[46:47], v[106:107], v[178:179], v[46:47] op_sel:[0,1,0]
	v_pk_fma_f32 v[44:45], v[108:109], v[178:179], v[44:45] op_sel:[0,1,0]
	v_pk_fma_f32 v[42:43], v[110:111], v[178:179], v[42:43] op_sel:[0,1,0]
	v_pk_fma_f32 v[40:41], v[112:113], v[178:179], v[40:41] op_sel:[0,1,0]
	v_pk_fma_f32 v[24:25], v[114:115], v[178:179], v[24:25] op_sel:[0,1,0]
	v_pk_fma_f32 v[22:23], v[116:117], v[178:179], v[22:23] op_sel:[0,1,0]
	v_pk_fma_f32 v[18:19], v[118:119], v[178:179], v[18:19] op_sel:[0,1,0]
	s_waitcnt lgkmcnt(0)
;     ...
;             for (int cc = 0; cc < 2; ++cc) { const int col = F.tid + cc * 512; float acc[16];
; #pragma unroll
;                 for (int p = 0; p < 16; ++p) acc[p] = 0.f;
;                 for (int k = 0; k < 64; ++k) { const float w = w3[k * 1024 + col];
; #pragma unroll
;                     for (int p = 0; p < 16; ++p) acc[p] += f2[p * 64 + k] * w; }
;                 const int c = col & 255; const float delta = 3.0701134573253945f + (float)c * ((15.350567286626973f - 3.0701134573253945f) / 255.0f);
; #pragma unroll
;                 for (int p4 = 0; p4 < 4; ++p4) { f32x4 o;
; #pragma unroll
;                     for (int q = 0; q < 4; ++q) { const int n = n0 + p4 * 4 + q; const float tt = (float)n / (float)(L - 1); o[q] = acc[p4 * 4 + q] * __expf(-tt * delta); }
;                     *(f32x4*)(FT + (size_t)col * L + n0 + p4 * 4) = o; } }
	ds_read_b128 v[88:91], v187 offset:3968
	ds_read_b128 v[92:95], v187 offset:3984
	ds_read_b128 v[96:99], v187 offset:4000
	ds_read_b128 v[100:103], v187 offset:4016
	ds_read_b128 v[104:107], v187 offset:4032
	ds_read_b128 v[108:111], v187 offset:4048
	ds_read_b128 v[112:115], v187 offset:4064
	ds_read_b128 v[116:119], v187 offset:4080
	s_waitcnt vmcnt(0)
	v_pk_fma_f32 v[48:49], v[56:57], v[180:181], v[48:49] op_sel_hi:[1,0,1]
	v_pk_fma_f32 v[46:47], v[58:59], v[180:181], v[46:47] op_sel_hi:[1,0,1]
	v_pk_fma_f32 v[44:45], v[60:61], v[180:181], v[44:45] op_sel_hi:[1,0,1]
	v_pk_fma_f32 v[42:43], v[62:63], v[180:181], v[42:43] op_sel_hi:[1,0,1]
	v_pk_fma_f32 v[40:41], v[64:65], v[180:181], v[40:41] op_sel_hi:[1,0,1]
	v_pk_fma_f32 v[24:25], v[66:67], v[180:181], v[24:25] op_sel_hi:[1,0,1]
	v_pk_fma_f32 v[22:23], v[68:69], v[180:181], v[22:23] op_sel_hi:[1,0,1]
	v_pk_fma_f32 v[18:19], v[70:71], v[180:181], v[18:19] op_sel_hi:[1,0,1]
	v_pk_fma_f32 v[48:49], v[72:73], v[182:183], v[48:49] op_sel_hi:[1,0,1]
	v_pk_fma_f32 v[46:47], v[74:75], v[182:183], v[46:47] op_sel_hi:[1,0,1]
	v_pk_fma_f32 v[44:45], v[76:77], v[182:183], v[44:45] op_sel_hi:[1,0,1]
	v_pk_fma_f32 v[42:43], v[78:79], v[182:183], v[42:43] op_sel_hi:[1,0,1]
	v_pk_fma_f32 v[40:41], v[80:81], v[182:183], v[40:41] op_sel_hi:[1,0,1]
	v_pk_fma_f32 v[24:25], v[82:83], v[182:183], v[24:25] op_sel_hi:[1,0,1]
	v_pk_fma_f32 v[22:23], v[84:85], v[182:183], v[22:23] op_sel_hi:[1,0,1]
	v_pk_fma_f32 v[18:19], v[86:87], v[182:183], v[18:19] op_sel_hi:[1,0,1]
	s_waitcnt lgkmcnt(0)
	v_pk_fma_f32 v[48:49], v[88:89], v[182:183], v[48:49] op_sel:[0,1,0]
	v_pk_fma_f32 v[46:47], v[90:91], v[182:183], v[46:47] op_sel:[0,1,0]
	v_pk_fma_f32 v[44:45], v[92:93], v[182:183], v[44:45] op_sel:[0,1,0]
	v_pk_fma_f32 v[42:43], v[94:95], v[182:183], v[42:43] op_sel:[0,1,0]
	v_pk_fma_f32 v[40:41], v[96:97], v[182:183], v[40:41] op_sel:[0,1,0]
	v_pk_fma_f32 v[24:25], v[98:99], v[182:183], v[24:25] op_sel:[0,1,0]
	v_pk_fma_f32 v[22:23], v[100:101], v[182:183], v[22:23] op_sel:[0,1,0]
	v_pk_fma_f32 v[18:19], v[102:103], v[182:183], v[18:19] op_sel:[0,1,0]
	v_pk_fma_f32 v[48:49], v[104:105], v[184:185], v[48:49] op_sel_hi:[1,0,1]
	v_pk_fma_f32 v[46:47], v[106:107], v[184:185], v[46:47] op_sel_hi:[1,0,1]
	v_pk_fma_f32 v[44:45], v[108:109], v[184:185], v[44:45] op_sel_hi:[1,0,1]
	v_pk_fma_f32 v[42:43], v[110:111], v[184:185], v[42:43] op_sel_hi:[1,0,1]
	v_pk_fma_f32 v[40:41], v[112:113], v[184:185], v[40:41] op_sel_hi:[1,0,1]
	v_pk_fma_f32 v[24:25], v[114:115], v[184:185], v[24:25] op_sel_hi:[1,0,1]
	v_pk_fma_f32 v[22:23], v[116:117], v[184:185], v[22:23] op_sel_hi:[1,0,1]
	v_pk_fma_f32 v[18:19], v[118:119], v[184:185], v[18:19] op_sel_hi:[1,0,1]
	s_nop 0
	s_mov_b32 s26, 0x40000
	s_mov_b32 s27, 0
	v_lshlrev_b64 v[56:57], s0, v[12:13]
	v_readlane_b32 s0, v252, 56
	v_readlane_b32 s1, v252, 57
	s_and_b64 s[0:1], s[0:1], s[24:25]
	s_add_i32 s2, s15, s70
	s_and_b64 s[0:1], s[0:1], s[22:23]
	s_and_b64 s[0:1], s[0:1], exec
	v_readlane_b32 s0, v253, 0
	s_cselect_b32 s3, s0, -1
	v_readlane_b32 s0, v252, 58
	v_readlane_b32 s1, v252, 59
	s_and_b64 s[0:1], s[0:1], exec
	v_lshl_add_u64 v[60:61], v[56:57], 2, s[44:45]
	v_pk_mul_f32 v[58:59], v[26:27], v[46:47]
	v_pk_mul_f32 v[26:27], v[28:29], v[44:45]
	v_pk_mul_f32 v[28:29], v[32:33], v[42:43]
	s_cselect_b32 s15, s3, s2
	v_pk_mul_f32 v[56:57], v[20:21], v[48:49]
	global_store_dwordx4 v[60:61], v[26:29], off offset:16
	v_pk_mul_f32 v[20:21], v[30:31], v[22:23]
	v_pk_mul_f32 v[22:23], v[38:39], v[18:19]
	v_pk_mul_f32 v[26:27], v[34:35], v[40:41]
	v_pk_mul_f32 v[28:29], v[36:37], v[24:25]
	s_cmp_gt_i32 s15, -1
	global_store_dwordx4 v[60:61], v[56:59], off
	global_store_dwordx4 v[60:61], v[26:29], off offset:32
	global_store_dwordx4 v[60:61], v[20:23], off offset:48
	s_cselect_b64 s[0:1], -1, 0
	s_cmp_lt_i32 s15, s14
	s_waitcnt lgkmcnt(0)
	s_barrier
	s_cselect_b64 s[2:3], -1, 0
	s_and_b64 s[0:1], s[0:1], s[2:3]
	s_and_b64 vcc, exec, s[0:1]
	s_movk_i32 s26, 0x1000
	s_cbranch_vccnz .LBB0_224
	s_branch .LBB0_263

; #define LAS __attribute__((address_space(3)))
; __device__ __forceinline__ float fsigmoid(float x) { return __builtin_amdgcn_rcpf(1.0f + __expf(-x)); }
; template <int PASS, bool REV> ...
;     ...
;         for (int kk = 0; kk < 2; ++kk) { const bf16x8 wa = wcur[0][kk], wx = wcur[1][kk]; bf16x8 uf[4][2];
; #pragma unroll
;             for (int tg = 0; tg < 4; ++tg) uf[tg][kk] = *(const LAS bf16x8*)(UB + (tg * 16 + fr) * 264 + blk * 64 + kk * 32 + fq * 8);
; #pragma unroll
;             for (int tg = 0; tg < 4; ++tg) { aa[tg] = __builtin_amdgcn_mfma_f32_16x16x32_bf16(wa, uf[tg][kk], aa[tg], 0, 0, 0); ax[tg] = __builtin_amdgcn_mfma_f32_16x16x32_bf16(wx, uf[tg][kk], ax[tg], 0, 0, 0); } }
;         { const int ng1 = (ng + 1 < ng_hi) ? ng + 1 : ng_lo;
; #pragma unroll
;             for (int gt = 0; gt < 2; ++gt)
; #pragma unroll
;                 for (int kk = 0; kk < 2; ++kk) wcur[gt][kk] = *(const bf16x8*)(Wg + ((size_t)(gt * 4 + blk) * 64 + ng1 * 16 + fr) * 64 + kk * 32 + fq * 8); }
;         if (PASS == 2 && REV && emit) {
; #pragma unroll
;             for (int tg = 0; tg < 4; ++tg) gwv[tg] = *(const v2u*)(P + (size_t)(R0 + tg * 16 + fr) * PROJ + C_RGG + blk * 64 + ng * 16 + fq * 4); }
;         const int ch = blk * 64 + ng * 16 + fq * 4; const f32x4 sp = *(const LAS f32x4*)(cst + ch), bav = *(const LAS f32x4*)(cst + 256 + ch), bxv = *(const LAS f32x4*)(cst + 512 + ch);
; #pragma unroll
;         for (int tg = 0; tg < 4; ++tg) { const v2u uw = *(const LAS v2u*)(UB + (tg * 16 + fr) * 264 + ch); const float uv[4] = {bflo(uw.x), bfhi(uw.x), bflo(uw.y), bfhi(uw.y)};
; #pragma unroll
;             for (int j = 0; j < 4; ++j) { const float r = fsigmoid(aa[tg][j] + bav[j]), ig = fsigmoid(ax[tg][j] + bxv[j]); const float la = -8.0f * r * sp[j];
;                 float Av = __expf(la); const float om = __builtin_fmaf(-Av, Av, 1.0f);
;                 float Bv = __builtin_amdgcn_sqrtf(om) * (ig * uv[j]);
;                 rg_scan_step<REV, 1>(Av, Bv); rg_scan_step<REV, 2>(Av, Bv); rg_scan_step<REV, 4>(Av, Bv); rg_scan_step<REV, 8>(Av, Bv);
;                 aa[tg][j] = Av; ax[tg][j] = Bv; } }
.LBB0_553:
	s_add_i32 s0, s9, s13
	s_waitcnt vmcnt(0) lgkmcnt(7)
	v_mfma_f32_16x16x32_bf16 v[48:51], v[40:43], v[0:3], 0
	s_add_i32 s0, s0, 1
	s_cmp_lt_u32 s0, s8
	s_cselect_b32 s0, s0, s9
	v_mfma_f32_16x16x32_bf16 v[52:55], v[44:47], v[0:3], 0
	v_lshl_add_u32 v180, s0, 4, v99
	v_add_u32_e32 v118, 0, v116
	s_waitcnt lgkmcnt(5)
	v_mfma_f32_16x16x32_bf16 v[56:59], v[40:43], v[8:11], 0
	s_waitcnt lgkmcnt(3)
	v_mfma_f32_16x16x32_bf16 v[64:67], v[40:43], v[16:19], 0
	s_waitcnt lgkmcnt(1)
	v_mfma_f32_16x16x32_bf16 v[40:43], v[40:43], v[24:27], 0
	v_mfma_f32_16x16x32_bf16 v[60:63], v[44:47], v[8:11], 0
	v_mfma_f32_16x16x32_bf16 v[68:71], v[44:47], v[16:19], 0
	v_mfma_f32_16x16x32_bf16 v[44:47], v[44:47], v[24:27], 0
	v_mfma_f32_16x16x32_bf16 v[88:91], v[32:35], v[4:7], v[48:51]
	v_mfma_f32_16x16x32_bf16 v[84:87], v[36:39], v[4:7], v[52:55]
	v_mfma_f32_16x16x32_bf16 v[80:83], v[32:35], v[12:15], v[56:59]
	v_mfma_f32_16x16x32_bf16 v[72:75], v[32:35], v[20:23], v[64:67]
	s_waitcnt lgkmcnt(0)
	v_mfma_f32_16x16x32_bf16 v[52:55], v[32:35], v[28:31], v[40:43]
	v_lshlrev_b64 v[32:33], 7, v[180:181]
	v_add_u32_e32 v180, 0x100, v180
	v_lshl_add_u64 v[32:33], v[94:95], 0, v[32:33]
	v_mfma_f32_16x16x32_bf16 v[76:79], v[36:39], v[12:15], v[60:63]
	global_load_dwordx4 v[40:43], v[32:33], off
	s_nop 0
	global_load_dwordx4 v[32:35], v[32:33], off offset:64
	v_add_u32_e32 v60, 0, v117
	v_add_u32_e32 v61, 0x12000, v60
	v_mfma_f32_16x16x32_bf16 v[68:71], v[36:39], v[20:23], v[68:71]
	v_add_u32_e32 v56, 0x11c00, v60
	v_add_u32_e32 v60, 0x12400, v60
	v_mfma_f32_16x16x32_bf16 v[48:51], v[36:39], v[28:31], v[44:47]
	v_lshlrev_b64 v[36:37], 7, v[180:181]
	v_lshl_add_u64 v[36:37], v[94:95], 0, v[36:37]
	s_nop 0
	global_load_dwordx4 v[44:47], v[36:37], off
	s_nop 0
	global_load_dwordx4 v[36:39], v[36:37], off offset:64
	ds_read_b128 v[64:67], v61
	ds_read_b64 v[120:121], v118
	ds_read_b128 v[56:59], v56
	ds_read_b128 v[60:63], v60
	s_waitcnt lgkmcnt(3)
	v_add_f32_e32 v88, v88, v64
	v_mul_f32_e32 v88, 0xbfb8aa3b, v88
	v_exp_f32_e32 v88, v88
	s_waitcnt lgkmcnt(0)
	v_add_f32_e32 v84, v84, v60
	v_mul_f32_e32 v84, 0xbfb8aa3b, v84
	v_exp_f32_e32 v84, v84
	v_add_f32_e32 v88, 1.0, v88
	v_rcp_f32_e32 v88, v88
	v_add_f32_e32 v89, v89, v65
	v_mul_f32_e32 v89, 0xbfb8aa3b, v89
	v_exp_f32_e32 v89, v89
	v_mul_f32_e32 v88, 0xc1000000, v88
	v_mul_f32_e32 v88, v56, v88
	v_mul_f32_e32 v88, 0x3fb8aa3b, v88
	v_exp_f32_e32 v88, v88
	v_add_f32_e32 v84, 1.0, v84
	v_rcp_f32_e32 v84, v84
	v_add_f32_e32 v89, 1.0, v89
	v_fma_f32 v123, -v88, v88, 1.0
	v_sqrt_f32_e32 v123, v123
	v_rcp_f32_e32 v89, v89
	v_lshlrev_b32_e32 v119, 16, v120
	v_mul_f32_e32 v84, v84, v119
	v_mul_f32_e32 v84, v84, v123
	v_mov_b32_e32 v119, 1.0
	v_mov_b32_e32 v123, v181
	v_add_f32_e32 v85, v85, v61
	v_mov_b32_dpp v119, v88 row_shl:1 row_mask:0xf bank_mask:0xf
	v_mov_b32_dpp v123, v84 row_shl:1 row_mask:0xf bank_mask:0xf
	v_mul_f32_e32 v89, 0xc1000000, v89
	v_fmac_f32_e32 v84, v88, v123
	v_mul_f32_e32 v88, v88, v119
	v_mov_b32_e32 v119, 1.0
	v_mov_b32_e32 v123, v181
	v_mul_f32_e32 v85, 0xbfb8aa3b, v85
	v_mul_f32_e32 v89, v57, v89
	v_mov_b32_dpp v119, v88 row_shl:2 row_mask:0xf bank_mask:0xf
	v_mov_b32_dpp v123, v84 row_shl:2 row_mask:0xf bank_mask:0xf
	v_exp_f32_e32 v85, v85
	v_mul_f32_e32 v89, 0x3fb8aa3b, v89
	v_add_f32_e32 v90, v90, v66
	v_fmac_f32_e32 v84, v88, v123
	v_mul_f32_e32 v88, v88, v119
	v_mov_b32_e32 v119, 1.0
	v_mov_b32_e32 v123, v181
	v_exp_f32_e32 v89, v89
	v_mul_f32_e32 v90, 0xbfb8aa3b, v90
	v_mov_b32_dpp v119, v88 row_shl:4 row_mask:0xf bank_mask:0xf
	v_mov_b32_dpp v123, v84 row_shl:4 row_mask:0xf bank_mask:0xf
	v_exp_f32_e32 v90, v90
	v_fmac_f32_e32 v84, v88, v123
	v_mul_f32_e32 v88, v88, v119
	v_mov_b32_e32 v119, 1.0
	v_mov_b32_e32 v123, v181
	v_add_f32_e32 v85, 1.0, v85
	v_mov_b32_dpp v119, v88 row_shl:8 row_mask:0xf bank_mask:0xf
	v_mov_b32_dpp v123, v84 row_shl:8 row_mask:0xf bank_mask:0xf
	v_fmac_f32_e32 v84, v88, v123
	v_mul_f32_e32 v88, v88, v119
	v_rcp_f32_e32 v85, v85
	v_fma_f32 v119, -v89, v89, 1.0
	v_sqrt_f32_e32 v119, v119
	v_add_f32_e32 v90, 1.0, v90
	v_rcp_f32_e32 v90, v90
	v_and_b32_e32 v120, 0xffff0000, v120
	v_mul_f32_e32 v85, v85, v120
	v_mul_f32_e32 v85, v85, v119
	v_mov_b32_e32 v119, 1.0
	v_mov_b32_e32 v120, v181
	v_add_f32_e32 v86, v86, v62
	v_mov_b32_dpp v119, v89 row_shl:1 row_mask:0xf bank_mask:0xf
	v_mov_b32_dpp v120, v85 row_shl:1 row_mask:0xf bank_mask:0xf
	v_mul_f32_e32 v90, 0xc1000000, v90
	v_fmac_f32_e32 v85, v89, v120
	v_mul_f32_e32 v89, v89, v119
	v_mov_b32_e32 v119, 1.0
	v_mov_b32_e32 v120, v181
	v_mul_f32_e32 v86, 0xbfb8aa3b, v86
	v_mul_f32_e32 v90, v58, v90
	v_mov_b32_dpp v119, v89 row_shl:2 row_mask:0xf bank_mask:0xf
	v_mov_b32_dpp v120, v85 row_shl:2 row_mask:0xf bank_mask:0xf
	v_exp_f32_e32 v86, v86
	v_mul_f32_e32 v90, 0x3fb8aa3b, v90
	v_add_f32_e32 v91, v91, v67
	v_fmac_f32_e32 v85, v89, v120
	v_mul_f32_e32 v89, v89, v119
	v_mov_b32_e32 v119, 1.0
	v_mov_b32_e32 v120, v181
	v_exp_f32_e32 v90, v90
	v_mul_f32_e32 v91, 0xbfb8aa3b, v91
	v_mov_b32_dpp v119, v89 row_shl:4 row_mask:0xf bank_mask:0xf
	v_mov_b32_dpp v120, v85 row_shl:4 row_mask:0xf bank_mask:0xf
	v_exp_f32_e32 v91, v91
	v_fmac_f32_e32 v85, v89, v120
	v_mul_f32_e32 v89, v89, v119
	v_mov_b32_e32 v119, 1.0
	v_mov_b32_e32 v120, v181
	v_add_f32_e32 v86, 1.0, v86
	v_mov_b32_dpp v119, v89 row_shl:8 row_mask:0xf bank_mask:0xf
	v_mov_b32_dpp v120, v85 row_shl:8 row_mask:0xf bank_mask:0xf
	v_fmac_f32_e32 v85, v89, v120
	v_mul_f32_e32 v89, v89, v119
	v_rcp_f32_e32 v86, v86
	v_fma_f32 v119, -v90, v90, 1.0
	v_sqrt_f32_e32 v119, v119
	v_add_f32_e32 v91, 1.0, v91
	v_rcp_f32_e32 v91, v91
	v_lshlrev_b32_e32 v122, 16, v121
; #define LAS __attribute__((address_space(3)))
; __device__ __forceinline__ float fsigmoid(float x) { return __builtin_amdgcn_rcpf(1.0f + __expf(-x)); }
; template <int PASS, bool REV> ...
;     ...
;         for (int tg = 0; tg < 4; ++tg) { const v2u uw = *(const LAS v2u*)(UB + (tg * 16 + fr) * 264 + ch); const float uv[4] = {bflo(uw.x), bfhi(uw.x), bflo(uw.y), bfhi(uw.y)};
; #pragma unroll
;             for (int j = 0; j < 4; ++j) { const float r = fsigmoid(aa[tg][j] + bav[j]), ig = fsigmoid(ax[tg][j] + bxv[j]); const float la = -8.0f * r * sp[j];
;                 float Av = __expf(la); const float om = __builtin_fmaf(-Av, Av, 1.0f);
;                 float Bv = __builtin_amdgcn_sqrtf(om) * (ig * uv[j]);
;                 rg_scan_step<REV, 1>(Av, Bv); rg_scan_step<REV, 2>(Av, Bv); rg_scan_step<REV, 4>(Av, Bv); rg_scan_step<REV, 8>(Av, Bv);
;                 aa[tg][j] = Av; ax[tg][j] = Bv; } }
	v_mul_f32_e32 v86, v86, v122
	v_mul_f32_e32 v86, v86, v119
	v_mov_b32_e32 v119, 1.0
	v_mov_b32_e32 v120, v181
	v_add_f32_e32 v87, v87, v63
	v_mov_b32_dpp v119, v90 row_shl:1 row_mask:0xf bank_mask:0xf
	v_mov_b32_dpp v120, v86 row_shl:1 row_mask:0xf bank_mask:0xf
	v_mul_f32_e32 v91, 0xc1000000, v91
	v_fmac_f32_e32 v86, v90, v120
	v_mul_f32_e32 v90, v90, v119
	v_mov_b32_e32 v119, 1.0
	v_mov_b32_e32 v120, v181
	v_mul_f32_e32 v87, 0xbfb8aa3b, v87
	v_mul_f32_e32 v91, v59, v91
	v_mov_b32_dpp v119, v90 row_shl:2 row_mask:0xf bank_mask:0xf
	v_mov_b32_dpp v120, v86 row_shl:2 row_mask:0xf bank_mask:0xf
	v_exp_f32_e32 v87, v87
	v_mul_f32_e32 v91, 0x3fb8aa3b, v91
	v_fmac_f32_e32 v86, v90, v120
	v_mul_f32_e32 v90, v90, v119
	v_mov_b32_e32 v119, 1.0
	v_mov_b32_e32 v120, v181
	v_exp_f32_e32 v91, v91
	v_mov_b32_dpp v119, v90 row_shl:4 row_mask:0xf bank_mask:0xf
	v_mov_b32_dpp v120, v86 row_shl:4 row_mask:0xf bank_mask:0xf
	v_add_f32_e32 v80, v80, v64
	v_fmac_f32_e32 v86, v90, v120
	v_mul_f32_e32 v90, v90, v119
	v_mov_b32_e32 v119, 1.0
	v_mov_b32_e32 v120, v181
	v_mul_f32_e32 v80, 0xbfb8aa3b, v80
	v_mov_b32_dpp v119, v90 row_shl:8 row_mask:0xf bank_mask:0xf
	v_mov_b32_dpp v120, v86 row_shl:8 row_mask:0xf bank_mask:0xf
	v_add_f32_e32 v87, 1.0, v87
	v_exp_f32_e32 v80, v80
	v_fmac_f32_e32 v86, v90, v120
	v_mul_f32_e32 v90, v90, v119
	v_rcp_f32_e32 v87, v87
	v_fma_f32 v119, -v91, v91, 1.0
	v_sqrt_f32_e32 v119, v119
	v_and_b32_e32 v121, 0xffff0000, v121
	v_add_f32_e32 v80, 1.0, v80
	v_mul_f32_e32 v87, v87, v121
	v_rcp_f32_e32 v80, v80
	v_mul_f32_e32 v87, v87, v119
	v_mov_b32_e32 v120, v181
	v_mov_b32_e32 v119, 1.0
	v_add_f32_e32 v76, v76, v60
	v_mov_b32_dpp v120, v87 row_shl:1 row_mask:0xf bank_mask:0xf
	v_mov_b32_dpp v119, v91 row_shl:1 row_mask:0xf bank_mask:0xf
	v_fmac_f32_e32 v87, v91, v120
	v_mov_b32_e32 v120, v181
	v_mul_f32_e32 v91, v91, v119
	v_mov_b32_e32 v119, 1.0
	v_mov_b32_dpp v120, v87 row_shl:2 row_mask:0xf bank_mask:0xf
	v_mul_f32_e32 v80, 0xc1000000, v80
	v_mov_b32_dpp v119, v91 row_shl:2 row_mask:0xf bank_mask:0xf
	v_fmac_f32_e32 v87, v91, v120
	v_mov_b32_e32 v120, v181
	v_mul_f32_e32 v76, 0xbfb8aa3b, v76
	v_mul_f32_e32 v80, v56, v80
	v_mul_f32_e32 v91, v91, v119
	v_mov_b32_e32 v119, 1.0
	v_mov_b32_dpp v120, v87 row_shl:4 row_mask:0xf bank_mask:0xf
	v_exp_f32_e32 v76, v76
	v_mul_f32_e32 v80, 0x3fb8aa3b, v80
	v_add_f32_e32 v81, v81, v65
	v_mov_b32_dpp v119, v91 row_shl:4 row_mask:0xf bank_mask:0xf
	v_fmac_f32_e32 v87, v91, v120
	v_mov_b32_e32 v120, v181
	v_exp_f32_e32 v80, v80
	v_mul_f32_e32 v81, 0xbfb8aa3b, v81
	v_mul_f32_e32 v91, v91, v119
	v_mov_b32_dpp v120, v87 row_shl:8 row_mask:0xf bank_mask:0xf
	v_exp_f32_e32 v81, v81
	v_fmac_f32_e32 v87, v91, v120
	ds_read_b64 v[120:121], v118 offset:8448
	v_add_f32_e32 v76, 1.0, v76
	v_rcp_f32_e32 v76, v76
	v_fma_f32 v123, -v80, v80, 1.0
	v_mov_b32_e32 v119, 1.0
	v_sqrt_f32_e32 v123, v123
	v_add_f32_e32 v81, 1.0, v81
	v_mov_b32_dpp v119, v91 row_shl:8 row_mask:0xf bank_mask:0xf
	v_rcp_f32_e32 v81, v81
	v_mul_f32_e32 v91, v91, v119
	s_waitcnt lgkmcnt(0)
	v_lshlrev_b32_e32 v119, 16, v120
	v_mul_f32_e32 v76, v76, v119
	v_mul_f32_e32 v76, v123, v76
	v_mov_b32_e32 v119, 1.0
	v_mov_b32_e32 v123, v181
	v_add_f32_e32 v77, v77, v61
	v_mov_b32_dpp v119, v80 row_shl:1 row_mask:0xf bank_mask:0xf
	v_mov_b32_dpp v123, v76 row_shl:1 row_mask:0xf bank_mask:0xf
	v_mul_f32_e32 v81, 0xc1000000, v81
	v_fmac_f32_e32 v76, v80, v123
	v_mul_f32_e32 v80, v80, v119
	v_mov_b32_e32 v119, 1.0
	v_mov_b32_e32 v123, v181
	v_mul_f32_e32 v77, 0xbfb8aa3b, v77
	v_mul_f32_e32 v81, v57, v81
	v_mov_b32_dpp v119, v80 row_shl:2 row_mask:0xf bank_mask:0xf
	v_mov_b32_dpp v123, v76 row_shl:2 row_mask:0xf bank_mask:0xf
	v_exp_f32_e32 v77, v77
	v_mul_f32_e32 v81, 0x3fb8aa3b, v81
	v_add_f32_e32 v82, v82, v66
	v_fmac_f32_e32 v76, v80, v123
	v_mul_f32_e32 v80, v80, v119
	v_mov_b32_e32 v119, 1.0
	v_mov_b32_e32 v123, v181
	v_exp_f32_e32 v81, v81
	v_mul_f32_e32 v82, 0xbfb8aa3b, v82
	v_mov_b32_dpp v119, v80 row_shl:4 row_mask:0xf bank_mask:0xf
	v_mov_b32_dpp v123, v76 row_shl:4 row_mask:0xf bank_mask:0xf
	v_exp_f32_e32 v82, v82
	v_fmac_f32_e32 v76, v80, v123
	v_mul_f32_e32 v80, v80, v119
	v_mov_b32_e32 v119, 1.0
	v_mov_b32_e32 v123, v181
	v_add_f32_e32 v77, 1.0, v77
	v_mov_b32_dpp v119, v80 row_shl:8 row_mask:0xf bank_mask:0xf
	v_mov_b32_dpp v123, v76 row_shl:8 row_mask:0xf bank_mask:0xf
	v_fmac_f32_e32 v76, v80, v123
	v_mul_f32_e32 v80, v80, v119
	v_rcp_f32_e32 v77, v77
	v_fma_f32 v119, -v81, v81, 1.0
	v_sqrt_f32_e32 v119, v119
	v_add_f32_e32 v82, 1.0, v82
	v_rcp_f32_e32 v82, v82
	v_and_b32_e32 v120, 0xffff0000, v120
	v_mul_f32_e32 v77, v77, v120
	v_mul_f32_e32 v77, v119, v77
	v_mov_b32_e32 v119, 1.0
	v_mov_b32_e32 v120, v181
	v_add_f32_e32 v78, v78, v62
	v_mov_b32_dpp v119, v81 row_shl:1 row_mask:0xf bank_mask:0xf
	v_mov_b32_dpp v120, v77 row_shl:1 row_mask:0xf bank_mask:0xf
	v_mul_f32_e32 v82, 0xc1000000, v82
	v_fmac_f32_e32 v77, v81, v120
	v_mul_f32_e32 v81, v81, v119
	v_mov_b32_e32 v119, 1.0
	v_mov_b32_e32 v120, v181
	v_mul_f32_e32 v78, 0xbfb8aa3b, v78
	v_mul_f32_e32 v82, v58, v82
	v_mov_b32_dpp v119, v81 row_shl:2 row_mask:0xf bank_mask:0xf
	v_mov_b32_dpp v120, v77 row_shl:2 row_mask:0xf bank_mask:0xf
	v_exp_f32_e32 v78, v78
	v_mul_f32_e32 v82, 0x3fb8aa3b, v82
	v_add_f32_e32 v83, v83, v67
	v_fmac_f32_e32 v77, v81, v120
	v_mul_f32_e32 v81, v81, v119
	v_mov_b32_e32 v119, 1.0
	v_mov_b32_e32 v120, v181
	v_exp_f32_e32 v82, v82
	v_mul_f32_e32 v83, 0xbfb8aa3b, v83
	v_mov_b32_dpp v119, v81 row_shl:4 row_mask:0xf bank_mask:0xf
	v_mov_b32_dpp v120, v77 row_shl:4 row_mask:0xf bank_mask:0xf
	v_exp_f32_e32 v83, v83
	v_fmac_f32_e32 v77, v81, v120
; #define LAS __attribute__((address_space(3)))
; __device__ __forceinline__ float fsigmoid(float x) { return __builtin_amdgcn_rcpf(1.0f + __expf(-x)); }
; template <int PASS, bool REV> ...
;     ...
;         for (int tg = 0; tg < 4; ++tg) { const v2u uw = *(const LAS v2u*)(UB + (tg * 16 + fr) * 264 + ch); const float uv[4] = {bflo(uw.x), bfhi(uw.x), bflo(uw.y), bfhi(uw.y)};
; #pragma unroll
;             for (int j = 0; j < 4; ++j) { const float r = fsigmoid(aa[tg][j] + bav[j]), ig = fsigmoid(ax[tg][j] + bxv[j]); const float la = -8.0f * r * sp[j];
;                 float Av = __expf(la); const float om = __builtin_fmaf(-Av, Av, 1.0f);
;                 float Bv = __builtin_amdgcn_sqrtf(om) * (ig * uv[j]);
;                 rg_scan_step<REV, 1>(Av, Bv); rg_scan_step<REV, 2>(Av, Bv); rg_scan_step<REV, 4>(Av, Bv); rg_scan_step<REV, 8>(Av, Bv);
;                 aa[tg][j] = Av; ax[tg][j] = Bv; } }
	v_mul_f32_e32 v81, v81, v119
	v_mov_b32_e32 v119, 1.0
	v_mov_b32_e32 v120, v181
	v_add_f32_e32 v78, 1.0, v78
	v_mov_b32_dpp v119, v81 row_shl:8 row_mask:0xf bank_mask:0xf
	v_mov_b32_dpp v120, v77 row_shl:8 row_mask:0xf bank_mask:0xf
	v_fmac_f32_e32 v77, v81, v120
	v_mul_f32_e32 v81, v81, v119
	v_rcp_f32_e32 v78, v78
	v_fma_f32 v119, -v82, v82, 1.0
	v_sqrt_f32_e32 v119, v119
	v_add_f32_e32 v83, 1.0, v83
	v_rcp_f32_e32 v83, v83
	v_lshlrev_b32_e32 v122, 16, v121
	v_mul_f32_e32 v78, v78, v122
	v_mul_f32_e32 v78, v119, v78
	v_mov_b32_e32 v119, 1.0
	v_mov_b32_e32 v120, v181
	v_add_f32_e32 v79, v79, v63
	v_mov_b32_dpp v119, v82 row_shl:1 row_mask:0xf bank_mask:0xf
	v_mov_b32_dpp v120, v78 row_shl:1 row_mask:0xf bank_mask:0xf
	v_mul_f32_e32 v83, 0xc1000000, v83
	v_fmac_f32_e32 v78, v82, v120
	v_mul_f32_e32 v82, v82, v119
	v_mov_b32_e32 v119, 1.0
	v_mov_b32_e32 v120, v181
	v_mul_f32_e32 v79, 0xbfb8aa3b, v79
	v_mul_f32_e32 v83, v59, v83
	v_mov_b32_dpp v119, v82 row_shl:2 row_mask:0xf bank_mask:0xf
	v_mov_b32_dpp v120, v78 row_shl:2 row_mask:0xf bank_mask:0xf
	v_exp_f32_e32 v79, v79
	v_mul_f32_e32 v83, 0x3fb8aa3b, v83
	v_fmac_f32_e32 v78, v82, v120
	v_mul_f32_e32 v82, v82, v119
	v_mov_b32_e32 v119, 1.0
	v_mov_b32_e32 v120, v181
	v_exp_f32_e32 v83, v83
	v_mov_b32_dpp v119, v82 row_shl:4 row_mask:0xf bank_mask:0xf
	v_mov_b32_dpp v120, v78 row_shl:4 row_mask:0xf bank_mask:0xf
	v_add_f32_e32 v72, v72, v64
	v_fmac_f32_e32 v78, v82, v120
	v_mul_f32_e32 v82, v82, v119
	v_mov_b32_e32 v119, 1.0
	v_mov_b32_e32 v120, v181
	v_mul_f32_e32 v72, 0xbfb8aa3b, v72
	v_mov_b32_dpp v119, v82 row_shl:8 row_mask:0xf bank_mask:0xf
	v_mov_b32_dpp v120, v78 row_shl:8 row_mask:0xf bank_mask:0xf
	v_add_f32_e32 v79, 1.0, v79
	v_exp_f32_e32 v72, v72
	v_fmac_f32_e32 v78, v82, v120
	v_mul_f32_e32 v82, v82, v119
	v_rcp_f32_e32 v79, v79
	v_fma_f32 v119, -v83, v83, 1.0
	v_sqrt_f32_e32 v119, v119
	v_and_b32_e32 v121, 0xffff0000, v121
	v_add_f32_e32 v72, 1.0, v72
	v_mul_f32_e32 v79, v79, v121
	v_rcp_f32_e32 v72, v72
	v_mul_f32_e32 v79, v119, v79
	v_mov_b32_e32 v120, v181
	v_mov_b32_e32 v119, 1.0
	v_add_f32_e32 v68, v68, v60
	v_mov_b32_dpp v120, v79 row_shl:1 row_mask:0xf bank_mask:0xf
	v_mov_b32_dpp v119, v83 row_shl:1 row_mask:0xf bank_mask:0xf
	v_fmac_f32_e32 v79, v83, v120
	v_mov_b32_e32 v120, v181
	v_mul_f32_e32 v83, v83, v119
	v_mov_b32_e32 v119, 1.0
	v_mov_b32_dpp v120, v79 row_shl:2 row_mask:0xf bank_mask:0xf
	v_mul_f32_e32 v72, 0xc1000000, v72
	v_mov_b32_dpp v119, v83 row_shl:2 row_mask:0xf bank_mask:0xf
	v_fmac_f32_e32 v79, v83, v120
	v_mov_b32_e32 v120, v181
	v_mul_f32_e32 v68, 0xbfb8aa3b, v68
	v_mul_f32_e32 v72, v56, v72
	v_mul_f32_e32 v83, v83, v119
	v_mov_b32_e32 v119, 1.0
	v_mov_b32_dpp v120, v79 row_shl:4 row_mask:0xf bank_mask:0xf
	v_exp_f32_e32 v68, v68
	v_mul_f32_e32 v72, 0x3fb8aa3b, v72
	v_add_f32_e32 v73, v73, v65
	v_mov_b32_dpp v119, v83 row_shl:4 row_mask:0xf bank_mask:0xf
	v_fmac_f32_e32 v79, v83, v120
	v_mov_b32_e32 v120, v181
	v_exp_f32_e32 v72, v72
	v_mul_f32_e32 v73, 0xbfb8aa3b, v73
	v_mul_f32_e32 v83, v83, v119
	v_mov_b32_dpp v120, v79 row_shl:8 row_mask:0xf bank_mask:0xf
	v_exp_f32_e32 v73, v73
	v_fmac_f32_e32 v79, v83, v120
	ds_read_b64 v[120:121], v118 offset:16896
	v_add_f32_e32 v68, 1.0, v68
	v_rcp_f32_e32 v68, v68
	v_fma_f32 v123, -v72, v72, 1.0
	v_add_f32_e32 v52, v52, v64
	v_sqrt_f32_e32 v123, v123
	v_add_f32_e32 v73, 1.0, v73
	v_mul_f32_e32 v52, 0xbfb8aa3b, v52
	v_rcp_f32_e32 v73, v73
	v_exp_f32_e32 v52, v52
	v_mul_f32_dpp v83, v83, v83 row_shl:8 row_mask:0xf bank_mask:0xf
	s_waitcnt lgkmcnt(0)
	v_lshlrev_b32_e32 v119, 16, v120
	v_mul_f32_e32 v68, v68, v119
	v_mul_f32_e32 v68, v123, v68
	v_add_f32_e32 v70, v70, v62
	v_add_f32_e32 v69, v69, v61
	v_mul_f32_e32 v73, 0xc1000000, v73
	v_mul_f32_e32 v70, 0xbfb8aa3b, v70
	v_add_f32_e32 v52, 1.0, v52
	v_fmac_f32_dpp v68, v68, v72 row_shl:1 row_mask:0xf bank_mask:0xf bound_ctrl:1
	v_mul_f32_dpp v72, v72, v72 row_shl:1 row_mask:0xf bank_mask:0xf
	v_mul_f32_e32 v69, 0xbfb8aa3b, v69
	v_mul_f32_e32 v73, v57, v73
	v_exp_f32_e32 v70, v70
	v_rcp_f32_e32 v52, v52
	v_exp_f32_e32 v69, v69
	v_mul_f32_e32 v73, 0x3fb8aa3b, v73
	v_add_f32_e32 v74, v74, v66
	v_fmac_f32_dpp v68, v68, v72 row_shl:2 row_mask:0xf bank_mask:0xf bound_ctrl:1
	v_mul_f32_dpp v72, v72, v72 row_shl:2 row_mask:0xf bank_mask:0xf
	v_exp_f32_e32 v73, v73
	v_mul_f32_e32 v74, 0xbfb8aa3b, v74
	v_exp_f32_e32 v74, v74
	v_add_f32_e32 v71, v71, v63
	v_fmac_f32_dpp v68, v68, v72 row_shl:4 row_mask:0xf bank_mask:0xf bound_ctrl:1
	v_mul_f32_dpp v72, v72, v72 row_shl:4 row_mask:0xf bank_mask:0xf
	v_add_f32_e32 v70, 1.0, v70
	v_mul_f32_e32 v71, 0xbfb8aa3b, v71
	v_add_f32_e32 v48, v48, v60
	v_mul_f32_e32 v52, 0xc1000000, v52
	v_add_f32_e32 v69, 1.0, v69
	v_rcp_f32_e32 v70, v70
	v_exp_f32_e32 v71, v71
	v_mul_f32_e32 v48, 0xbfb8aa3b, v48
	v_mul_f32_e32 v52, v56, v52
	v_fmac_f32_dpp v68, v68, v72 row_shl:8 row_mask:0xf bank_mask:0xf bound_ctrl:1
	v_mul_f32_dpp v72, v72, v72 row_shl:8 row_mask:0xf bank_mask:0xf
	v_rcp_f32_e32 v69, v69
	v_fma_f32 v119, -v73, v73, 1.0
	v_exp_f32_e32 v48, v48
	v_mul_f32_e32 v52, 0x3fb8aa3b, v52
	v_sqrt_f32_e32 v119, v119
	v_add_f32_e32 v74, 1.0, v74
	v_exp_f32_e32 v52, v52
	v_lshlrev_b32_e32 v122, 16, v121
	v_rcp_f32_e32 v74, v74
	v_and_b32_e32 v120, 0xffff0000, v120
	v_mul_f32_e32 v70, v70, v122
	v_add_f32_e32 v71, 1.0, v71
	ds_read_b64 v[122:123], v118 offset:25344
	v_mul_f32_e32 v69, v69, v120
	v_rcp_f32_e32 v71, v71
	v_add_f32_e32 v48, 1.0, v48
	v_mul_f32_e32 v69, v119, v69
	v_rcp_f32_e32 v48, v48
	v_fma_f32 v56, -v52, v52, 1.0
	v_mul_f32_e32 v74, 0xc1000000, v74
	v_sqrt_f32_e32 v56, v56
	v_and_b32_e32 v121, 0xffff0000, v121
	v_fmac_f32_dpp v69, v69, v73 row_shl:1 row_mask:0xf bank_mask:0xf bound_ctrl:1
	v_mul_f32_dpp v73, v73, v73 row_shl:1 row_mask:0xf bank_mask:0xf
	v_mul_f32_e32 v74, v58, v74
	v_mul_f32_e32 v74, 0x3fb8aa3b, v74
	v_add_f32_e32 v75, v75, v67
	v_mul_f32_e32 v71, v71, v121
	s_waitcnt lgkmcnt(0)
; #define LAS __attribute__((address_space(3)))
; __device__ __forceinline__ float fsigmoid(float x) { return __builtin_amdgcn_rcpf(1.0f + __expf(-x)); }
; template <int PASS, bool REV> ...
;     ...
;         for (int tg = 0; tg < 4; ++tg) { const v2u uw = *(const LAS v2u*)(UB + (tg * 16 + fr) * 264 + ch); const float uv[4] = {bflo(uw.x), bfhi(uw.x), bflo(uw.y), bfhi(uw.y)};
; #pragma unroll
;             for (int j = 0; j < 4; ++j) { const float r = fsigmoid(aa[tg][j] + bav[j]), ig = fsigmoid(ax[tg][j] + bxv[j]); const float la = -8.0f * r * sp[j];
;                 float Av = __expf(la); const float om = __builtin_fmaf(-Av, Av, 1.0f);
;                 float Bv = __builtin_amdgcn_sqrtf(om) * (ig * uv[j]);
;                 rg_scan_step<REV, 1>(Av, Bv); rg_scan_step<REV, 2>(Av, Bv); rg_scan_step<REV, 4>(Av, Bv); rg_scan_step<REV, 8>(Av, Bv);
;                 aa[tg][j] = Av; ax[tg][j] = Bv; } }
	v_lshlrev_b32_e32 v121, 16, v122
	v_fmac_f32_dpp v69, v69, v73 row_shl:2 row_mask:0xf bank_mask:0xf bound_ctrl:1
	v_mul_f32_dpp v73, v73, v73 row_shl:2 row_mask:0xf bank_mask:0xf
	v_exp_f32_e32 v74, v74
	v_mul_f32_e32 v75, 0xbfb8aa3b, v75
	v_mul_f32_e32 v48, v48, v121
	v_exp_f32_e32 v75, v75
	v_mul_f32_e32 v56, v56, v48
	v_fmac_f32_dpp v69, v69, v73 row_shl:4 row_mask:0xf bank_mask:0xf bound_ctrl:1
	v_mul_f32_dpp v73, v73, v73 row_shl:4 row_mask:0xf bank_mask:0xf
	v_mov_b32_e32 v48, v52
	v_fmac_f32_dpp v56, v56, v52 row_shl:1 row_mask:0xf bank_mask:0xf bound_ctrl:1
	v_mul_f32_dpp v48, v52, v52 row_shl:1 row_mask:0xf bank_mask:0xf
	v_fmac_f32_dpp v69, v69, v73 row_shl:8 row_mask:0xf bank_mask:0xf bound_ctrl:1
	v_mul_f32_dpp v73, v73, v73 row_shl:8 row_mask:0xf bank_mask:0xf
	v_fma_f32 v119, -v74, v74, 1.0
	v_sqrt_f32_e32 v119, v119
	v_add_f32_e32 v75, 1.0, v75
	v_fmac_f32_dpp v56, v56, v48 row_shl:2 row_mask:0xf bank_mask:0xf bound_ctrl:1
	v_mul_f32_dpp v48, v48, v48 row_shl:2 row_mask:0xf bank_mask:0xf
	v_rcp_f32_e32 v75, v75
	v_fmac_f32_dpp v56, v56, v48 row_shl:4 row_mask:0xf bank_mask:0xf bound_ctrl:1
	v_mul_f32_dpp v48, v48, v48 row_shl:4 row_mask:0xf bank_mask:0xf
	v_mul_f32_e32 v70, v119, v70
	v_fmac_f32_dpp v56, v56, v48 row_shl:8 row_mask:0xf bank_mask:0xf bound_ctrl:1
	v_mul_f32_dpp v48, v48, v48 row_shl:8 row_mask:0xf bank_mask:0xf
	v_add_f32_e32 v52, v53, v65
	v_mul_f32_e32 v75, 0xc1000000, v75
	v_mul_f32_e32 v52, 0xbfb8aa3b, v52
	v_fmac_f32_dpp v70, v70, v74 row_shl:1 row_mask:0xf bank_mask:0xf bound_ctrl:1
	v_mul_f32_dpp v74, v74, v74 row_shl:1 row_mask:0xf bank_mask:0xf
	v_mul_f32_e32 v75, v59, v75
	v_exp_f32_e32 v52, v52
	v_mul_f32_e32 v75, 0x3fb8aa3b, v75
	v_fmac_f32_dpp v70, v70, v74 row_shl:2 row_mask:0xf bank_mask:0xf bound_ctrl:1
	v_mul_f32_dpp v74, v74, v74 row_shl:2 row_mask:0xf bank_mask:0xf
	v_exp_f32_e32 v75, v75
	v_fmac_f32_dpp v70, v70, v74 row_shl:4 row_mask:0xf bank_mask:0xf bound_ctrl:1
	v_mul_f32_dpp v74, v74, v74 row_shl:4 row_mask:0xf bank_mask:0xf
	v_add_f32_e32 v52, 1.0, v52
	v_rcp_f32_e32 v52, v52
	v_fmac_f32_dpp v70, v70, v74 row_shl:8 row_mask:0xf bank_mask:0xf bound_ctrl:1
	v_mul_f32_dpp v74, v74, v74 row_shl:8 row_mask:0xf bank_mask:0xf
	v_fma_f32 v119, -v75, v75, 1.0
	v_sqrt_f32_e32 v119, v119
	v_add_f32_e32 v49, v49, v61
	v_mul_f32_e32 v52, 0xc1000000, v52
	v_mul_f32_e32 v49, 0xbfb8aa3b, v49
	v_mul_f32_e32 v52, v57, v52
	v_mul_f32_e32 v71, v119, v71
	v_exp_f32_e32 v49, v49
	v_mul_f32_e32 v52, 0x3fb8aa3b, v52
	v_exp_f32_e32 v52, v52
	v_fmac_f32_dpp v71, v71, v75 row_shl:1 row_mask:0xf bank_mask:0xf bound_ctrl:1
	v_mul_f32_dpp v75, v75, v75 row_shl:1 row_mask:0xf bank_mask:0xf
	s_nop 0
	v_fmac_f32_dpp v71, v71, v75 row_shl:2 row_mask:0xf bank_mask:0xf bound_ctrl:1
	v_add_f32_e32 v49, 1.0, v49
	v_mul_f32_dpp v75, v75, v75 row_shl:2 row_mask:0xf bank_mask:0xf
	v_rcp_f32_e32 v49, v49
	v_fma_f32 v53, -v52, v52, 1.0
	v_fmac_f32_dpp v71, v71, v75 row_shl:4 row_mask:0xf bank_mask:0xf bound_ctrl:1
	v_sqrt_f32_e32 v53, v53
	v_mul_f32_dpp v75, v75, v75 row_shl:4 row_mask:0xf bank_mask:0xf
	v_fmac_f32_dpp v71, v71, v75 row_shl:8 row_mask:0xf bank_mask:0xf bound_ctrl:1
	v_and_b32_e32 v120, 0xffff0000, v122
	v_mul_f32_e32 v49, v49, v120
	v_mul_f32_e32 v53, v53, v49
	v_add_f32_e32 v50, v50, v62
	v_mov_b32_e32 v49, v52
	v_fmac_f32_dpp v53, v53, v52 row_shl:1 row_mask:0xf bank_mask:0xf bound_ctrl:1
	v_mul_f32_dpp v49, v52, v52 row_shl:1 row_mask:0xf bank_mask:0xf
	v_mul_f32_e32 v50, 0xbfb8aa3b, v50
	v_fmac_f32_dpp v53, v53, v49 row_shl:2 row_mask:0xf bank_mask:0xf bound_ctrl:1
	v_mul_f32_dpp v49, v49, v49 row_shl:2 row_mask:0xf bank_mask:0xf
	v_exp_f32_e32 v50, v50
	v_fmac_f32_dpp v53, v53, v49 row_shl:4 row_mask:0xf bank_mask:0xf bound_ctrl:1
	v_mul_f32_dpp v49, v49, v49 row_shl:4 row_mask:0xf bank_mask:0xf
	v_add_f32_e32 v50, 1.0, v50
	v_fmac_f32_dpp v53, v53, v49 row_shl:8 row_mask:0xf bank_mask:0xf bound_ctrl:1
	v_mul_f32_dpp v49, v49, v49 row_shl:8 row_mask:0xf bank_mask:0xf
	v_add_f32_e32 v52, v54, v66
	v_mul_f32_e32 v52, 0xbfb8aa3b, v52
	v_exp_f32_e32 v52, v52
	v_rcp_f32_e32 v50, v50
	v_add_f32_e32 v52, 1.0, v52
	v_rcp_f32_e32 v52, v52
	v_mul_f32_dpp v75, v75, v75 row_shl:8 row_mask:0xf bank_mask:0xf
; #define LAS __attribute__((address_space(3)))
; __device__ __forceinline__ float fsigmoid(float x) { return __builtin_amdgcn_rcpf(1.0f + __expf(-x)); }
; __device__ __forceinline__ float bperm_f(int idx4, float x) { return __builtin_bit_cast(float, __builtin_amdgcn_ds_bpermute(idx4, __builtin_bit_cast(int, x))); }
; template <int PASS, bool REV> ...
;     ...
;         for (int tg = 0; tg < 4; ++tg) { const v2u uw = *(const LAS v2u*)(UB + (tg * 16 + fr) * 264 + ch); const float uv[4] = {bflo(uw.x), bfhi(uw.x), bflo(uw.y), bfhi(uw.y)};
; #pragma unroll
;             for (int j = 0; j < 4; ++j) { const float r = fsigmoid(aa[tg][j] + bav[j]), ig = fsigmoid(ax[tg][j] + bxv[j]); const float la = -8.0f * r * sp[j];
;                 float Av = __expf(la); const float om = __builtin_fmaf(-Av, Av, 1.0f);
;                 float Bv = __builtin_amdgcn_sqrtf(om) * (ig * uv[j]);
;                 rg_scan_step<REV, 1>(Av, Bv); rg_scan_step<REV, 2>(Av, Bv); rg_scan_step<REV, 4>(Av, Bv); rg_scan_step<REV, 8>(Av, Bv);
;                 aa[tg][j] = Av; ax[tg][j] = Bv; } }
;         const int lastl4 = ((lane & 48) | (REV ? 0 : 15)) << 2;
;         if (PASS == 1) {
;             f32x4 At = (f32x4){1.f, 1.f, 1.f, 1.f}, Bt = (f32x4){0.f, 0.f, 0.f, 0.f};
; #pragma unroll
;             for (int t4 = 0; t4 < 4; ++t4) { const int tg = REV ? 3 - t4 : t4;
; #pragma unroll
;                 for (int j = 0; j < 4; ++j) { const float ta = bperm_f(lastl4, aa[tg][j]), tb = bperm_f(lastl4, ax[tg][j]); Bt[j] = ta * Bt[j] + tb; At[j] = At[j] * ta; } }
;             if (fr == 0) { f32x4* cp = (f32x4*)(CAR + ((size_t)u * 2 + d) * 256 + ch); cp[0] = (f32x4){At[0], Bt[0], At[1], Bt[1]}; cp[1] = (f32x4){At[2], Bt[2], At[3], Bt[3]}; }
	v_lshlrev_b32_e32 v119, 16, v123
	v_mul_f32_e32 v52, 0xc1000000, v52
	v_mul_f32_e32 v52, v58, v52
	v_mul_f32_e32 v52, 0x3fb8aa3b, v52
	v_exp_f32_e32 v52, v52
	v_mul_f32_e32 v50, v50, v119
	v_add_f32_e32 v51, v51, v63
	v_mul_f32_e32 v51, 0xbfb8aa3b, v51
	v_fma_f32 v54, -v52, v52, 1.0
	v_sqrt_f32_e32 v54, v54
	v_exp_f32_e32 v51, v51
	v_and_b32_e32 v118, 0xffff0000, v123
	ds_bpermute_b32 v48, v101, v48
	v_mul_f32_e32 v54, v54, v50
	v_add_f32_e32 v51, 1.0, v51
	v_mov_b32_e32 v50, v52
	v_fmac_f32_dpp v54, v54, v52 row_shl:1 row_mask:0xf bank_mask:0xf bound_ctrl:1
	v_mul_f32_dpp v50, v52, v52 row_shl:1 row_mask:0xf bank_mask:0xf
	v_rcp_f32_e32 v51, v51
	v_fmac_f32_dpp v54, v54, v50 row_shl:2 row_mask:0xf bank_mask:0xf bound_ctrl:1
	v_mul_f32_dpp v50, v50, v50 row_shl:2 row_mask:0xf bank_mask:0xf
	v_mul_f32_e32 v51, v51, v118
	v_fmac_f32_dpp v54, v54, v50 row_shl:4 row_mask:0xf bank_mask:0xf bound_ctrl:1
	v_mul_f32_dpp v50, v50, v50 row_shl:4 row_mask:0xf bank_mask:0xf
	ds_bpermute_b32 v49, v101, v49
	v_fmac_f32_dpp v54, v54, v50 row_shl:8 row_mask:0xf bank_mask:0xf bound_ctrl:1
	v_mul_f32_dpp v50, v50, v50 row_shl:8 row_mask:0xf bank_mask:0xf
	v_add_f32_e32 v52, v55, v67
	v_mul_f32_e32 v52, 0xbfb8aa3b, v52
	v_exp_f32_e32 v52, v52
	ds_bpermute_b32 v53, v101, v53
	ds_bpermute_b32 v50, v101, v50
	v_add_f32_e32 v52, 1.0, v52
	v_rcp_f32_e32 v52, v52
	ds_bpermute_b32 v54, v101, v54
	ds_bpermute_b32 v60, v101, v68
	ds_bpermute_b32 v61, v101, v69
	v_mul_f32_e32 v52, 0xc1000000, v52
	v_mul_f32_e32 v52, v59, v52
	v_mul_f32_e32 v52, 0x3fb8aa3b, v52
	v_exp_f32_e32 v52, v52
	ds_bpermute_b32 v58, v101, v74
	ds_bpermute_b32 v62, v101, v70
	ds_bpermute_b32 v59, v101, v75
	v_fma_f32 v55, -v52, v52, 1.0
	v_sqrt_f32_e32 v55, v55
	ds_bpermute_b32 v63, v101, v71
	ds_bpermute_b32 v64, v101, v80
	ds_bpermute_b32 v68, v101, v76
	v_mul_f32_e32 v55, v55, v51
	ds_bpermute_b32 v65, v101, v81
	v_mov_b32_e32 v51, v52
	v_fmac_f32_dpp v55, v55, v52 row_shl:1 row_mask:0xf bank_mask:0xf bound_ctrl:1
	v_mul_f32_dpp v51, v52, v52 row_shl:1 row_mask:0xf bank_mask:0xf
	ds_bpermute_b32 v69, v101, v77
	v_fmac_f32_dpp v55, v55, v51 row_shl:2 row_mask:0xf bank_mask:0xf bound_ctrl:1
	v_mul_f32_dpp v51, v51, v51 row_shl:2 row_mask:0xf bank_mask:0xf
	ds_bpermute_b32 v66, v101, v82
	v_fmac_f32_dpp v55, v55, v51 row_shl:4 row_mask:0xf bank_mask:0xf bound_ctrl:1
	v_mul_f32_dpp v51, v51, v51 row_shl:4 row_mask:0xf bank_mask:0xf
	ds_bpermute_b32 v70, v101, v78
	v_fmac_f32_dpp v55, v55, v51 row_shl:8 row_mask:0xf bank_mask:0xf bound_ctrl:1
	v_mul_f32_dpp v51, v51, v51 row_shl:8 row_mask:0xf bank_mask:0xf
	ds_bpermute_b32 v52, v101, v56
	ds_bpermute_b32 v51, v101, v51
	ds_bpermute_b32 v55, v101, v55
	ds_bpermute_b32 v56, v101, v72
	ds_bpermute_b32 v57, v101, v73
	ds_bpermute_b32 v67, v101, v83
	ds_bpermute_b32 v71, v101, v79
	ds_bpermute_b32 v72, v101, v88
	ds_bpermute_b32 v76, v101, v84
	ds_bpermute_b32 v73, v101, v89
	ds_bpermute_b32 v77, v101, v85
	ds_bpermute_b32 v74, v101, v90
	ds_bpermute_b32 v78, v101, v86
	ds_bpermute_b32 v75, v101, v91
	ds_bpermute_b32 v79, v101, v87
	s_and_saveexec_b64 s[0:1], s[36:37]
	s_cbranch_execz .LBB0_552
	s_waitcnt lgkmcnt(10)
	v_pk_mul_f32 v[80:81], v[48:49], v[56:57]
	v_pk_fma_f32 v[48:49], v[48:49], 0, v[52:53] op_sel_hi:[1,0,1]
	v_pk_mul_f32 v[80:81], v[80:81], v[64:65]
	v_pk_fma_f32 v[48:49], v[48:49], v[56:57], v[60:61]
	v_pk_mul_f32 v[82:83], v[50:51], v[58:59]
	v_pk_fma_f32 v[48:49], v[48:49], v[64:65], v[68:69]
	s_waitcnt lgkmcnt(5)
	v_pk_mul_f32 v[80:81], v[80:81], v[72:73]
	s_waitcnt lgkmcnt(4)
	v_pk_fma_f32 v[52:53], v[48:49], v[72:73], v[76:77]
	v_pk_fma_f32 v[48:49], v[50:51], 0, v[54:55] op_sel_hi:[1,0,1]
	v_pk_mul_f32 v[82:83], v[82:83], v[66:67]
	v_pk_fma_f32 v[48:49], v[48:49], v[58:59], v[62:63]
	s_waitcnt lgkmcnt(1)
	v_pk_mul_f32 v[82:83], v[82:83], v[74:75]
	v_pk_fma_f32 v[48:49], v[48:49], v[66:67], v[70:71]
	v_mov_b32_e32 v50, v80
	s_waitcnt lgkmcnt(0)
	v_pk_fma_f32 v[54:55], v[48:49], v[74:75], v[78:79]
	v_mov_b32_e32 v51, v52
	v_mov_b32_e32 v52, v81
	global_store_dwordx4 v[102:103], v[50:53], off offset:-16
	s_nop 1
	v_mov_b32_e32 v52, v82
	v_mov_b32_e32 v53, v54
	v_mov_b32_e32 v54, v83
	global_store_dwordx4 v[102:103], v[52:55], off
	s_branch .LBB0_552
